# QG epilogue + mLSTM out: exact 1/x division sequences replaced by v_rcp_f32 (f32, 1 ulp)
# speedup vs baseline: 1.0147x; 1.0026x over previous
; #define LAS __attribute__((address_space(3)))
; __device__ __forceinline__ unsigned pk2(float lo, float hi) { return __builtin_amdgcn_perm(__builtin_bit_cast(unsigned, hi) + 0x8000u, __builtin_bit_cast(unsigned, lo) + 0x8000u, 0x07060302u); }
; __device__ __forceinline__ void ph_mlstm_out(const Frame& F) {
;     ...
;         const bf16* ogp = HB + (size_t)(t0 + l15) * 6144 + 4096 + h * 256 + 32 * wave + 4 * g;
;         v2u ogn0 = *(const v2u*)ogp, ogn1 = *(const v2u*)(ogp + 16);
; #pragma unroll
;         for (int tt = 0; tt < 8; ++tt) {
;             const int t = 16 * tt + l15;
;             const v2u ogc[2] = {ogn0, ogn1};
;             if (tt < 7) { ogn0 = *(const v2u*)(ogp + (size_t)(16 * (tt + 1)) * 6144); ogn1 = *(const v2u*)(ogp + (size_t)(16 * (tt + 1)) * 6144 + 16); }
;             bf16x8 qf[4];
; #pragma unroll
;             for (int st = 0; st < 4; ++st) qf[st] = *(const LAS bf16x8*)(lds + MLO_Q_OFF + t * ML_ROW + 16 * g + 64 * st);
;             const int nst = (tt >> 1) + 1;
;             bf16x8 pf[4];
; #pragma unroll
;             for (int st = 0; st < 4; ++st) if (st < nst) pf[st] = *(const LAS bf16x8*)(lds + ML_K_OFF + t * ML_ROW + 16 * g + 64 * st);
;             const float ai = ais[t], rd = rds[t];
; #pragma unroll
;             for (int vt = 0; vt < 2; ++vt) {
;                 f32x4 ci = (f32x4){0.f, 0.f, 0.f, 0.f}, cx = (f32x4){0.f, 0.f, 0.f, 0.f};
; #pragma unroll
;                 for (int st = 0; st < 4; ++st) ci = __builtin_amdgcn_mfma_f32_16x16x32_bf16(cf[vt][st], qf[st], ci, 0, 0, 0);
;                 const LAS unsigned char* vr = lds + ML_V_OFF + (16 * (2 * wave + vt) + l15) * ML_ROW + 16 * g;
; #pragma unroll
;                 for (int st = 0; st < 4; ++st) if (st < nst) cx = __builtin_amdgcn_mfma_f32_16x16x32_bf16(*(const LAS bf16x8*)(vr + 64 * st), pf[st], cx, 0, 0, 0);
;                 const int vcol = h * 256 + 16 * (2 * wave + vt) + 4 * g;
;                 const v2u ogw = ogc[vt];
;                 const float y0 = (ai * ci[0] + cx[0]) * rd * sigmoidf_(bflo(ogw.x)), y1 = (ai * ci[1] + cx[1]) * rd * sigmoidf_(bfhi(ogw.x));
;                 const float y2 = (ai * ci[2] + cx[2]) * rd * sigmoidf_(bflo(ogw.y)), y3 = (ai * ci[3] + cx[3]) * rd * sigmoidf_(bfhi(ogw.y));
;                 v2u w; w.x = pk2(y0, y1); w.y = pk2(y2, y3);
;                 *(v2u*)(YB + (size_t)(t0 + t) * 2048 + vcol) = w;
;             }
.LBB0_591:
	s_lshr_b32 s62, s57, 26
	s_add_i32 s62, s56, s62
	s_ashr_i32 s62, s62, 6
	s_lshr_b32 s57, s57, 23
	s_add_i32 s56, s56, s57
	s_lshr_b32 s57, s62, 29
	s_add_i32 s57, s62, s57
	s_and_b32 s57, s57, 0xfffff8
	s_lshl_b32 s56, s56, 4
	s_sub_i32 s63, s62, s57
	s_and_b32 s56, s56, 0xffffe000
	s_lshl_b32 s57, s62, 13
	s_sub_i32 s56, s56, s57
	s_add_i32 s56, s56, s43
	v_add_u32_e32 v188, s56, v235
	v_mov_b64_e32 v[98:99], s[24:25]
	s_movk_i32 s56, 0x3000
	v_mad_i64_i32 v[98:99], s[56:57], v188, s56, v[98:99]
	s_lshl_b32 s56, s63, 8
	s_ashr_i32 s57, s56, 31
	v_lshl_add_u64 v[98:99], s[56:57], 1, v[98:99]
	v_lshl_add_u64 v[98:99], s[92:93], 1, v[98:99]
	v_lshlrev_b32_e32 v0, 1, v178
	v_lshl_add_u64 v[138:139], v[98:99], 0, v[0:1]
	s_movk_i32 s57, 0x2000
	v_add_co_u32_e32 v100, vcc, s57, v138
	s_mov_b64 s[62:63], 0x2000
	s_nop 0
	v_addc_co_u32_e32 v101, vcc, 0, v139, vcc
	v_lshl_add_u64 v[98:99], v[138:139], 0, s[62:63]
	global_load_dwordx2 v[140:141], v[100:101], off
	global_load_dwordx2 v[142:143], v[98:99], off offset:32
	v_or_b32_e32 v0, s56, v178
	s_mov_b32 s56, 0x32000
	v_add_co_u32_e32 v98, vcc, s56, v138
	v_ashrrev_i32_e32 v189, 31, v188
	s_nop 0
	v_addc_co_u32_e32 v99, vcc, 0, v139, vcc
	global_load_dwordx2 v[112:113], v[98:99], off
	global_load_dwordx2 v[106:107], v[98:99], off offset:32
	v_add_u32_e32 v98, v204, v221
	ds_read_b128 v[118:121], v98
	ds_read_b128 v[122:125], v98 offset:64
	ds_read_b128 v[126:129], v98 offset:128
	ds_read_b128 v[130:133], v98 offset:192
	ds_read_b128 v[114:117], v116 offset:4096
	s_waitcnt lgkmcnt(4)
	v_mfma_f32_16x16x32_bf16 v[134:137], v[94:97], v[118:121], 0
	ds_read_b128 v[102:105], v247 offset:38912
	v_add_u32_e32 v158, 0x800, v233
	ds_read2_b32 v[108:109], v158 offset0:128 offset1:144
	s_waitcnt lgkmcnt(5)
	v_mfma_f32_16x16x32_bf16 v[134:137], v[82:85], v[122:125], v[134:137]
	v_lshlrev_b64 v[98:99], 12, v[188:189]
	v_lshl_add_u64 v[144:145], s[22:23], 0, v[98:99]
	v_add_u32_e32 v159, 0xc00, v233
	s_waitcnt lgkmcnt(4)
	v_mfma_f32_16x16x32_bf16 v[134:137], v[86:89], v[126:129], v[134:137]
	ds_read2_b32 v[110:111], v159 offset1:16
	v_add_u32_e32 v146, s92, v0
	v_add_u32_e32 v181, v204, v234
	s_waitcnt lgkmcnt(2)
	v_mfma_f32_16x16x32_bf16 v[98:101], v[102:105], v[114:117], 0
	s_add_i32 s43, s43, s20
	v_mfma_f32_16x16x32_bf16 v[134:137], v[90:93], v[130:133], v[134:137]
	v_mfma_f32_16x16x32_bf16 v[118:121], v[78:81], v[118:121], 0
	v_mfma_f32_16x16x32_bf16 v[118:121], v[66:69], v[122:125], v[118:121]
	s_waitcnt lgkmcnt(1)
	s_nop 4
	v_fma_f32 v98, v108, v134, v98
	s_waitcnt lgkmcnt(0)
	v_mul_f32_e32 v98, v110, v98
	v_fma_f32 v99, v108, v135, v99
	v_mul_f32_e32 v99, v110, v99
	v_fma_f32 v100, v108, v136, v100
	v_mul_f32_e32 v100, v110, v100
	v_fmac_f32_e32 v101, v108, v137
	v_mul_f32_e32 v101, v110, v101
	v_mfma_f32_16x16x32_bf16 v[118:121], v[70:73], v[126:129], v[118:121]
	v_add_u32_e32 v122, s36, v0
	s_waitcnt vmcnt(3)
	v_lshlrev_b32_e32 v134, 16, v140
	v_mul_f32_e32 v134, 0xbfb8aa3b, v134
	v_exp_f32_e32 v134, v134
	v_mfma_f32_16x16x32_bf16 v[118:121], v[74:77], v[130:133], v[118:121]
	v_add_f32_e32 v134, 1.0, v134
	v_rcp_f32_e32 v134, v134
	s_nop 0
	v_mul_f32_e32 v98, v134, v98
	v_and_b32_e32 v134, 0xffff0000, v140
	v_mul_f32_e32 v134, 0xbfb8aa3b, v134
	v_exp_f32_e32 v134, v134
	v_add_u32_e32 v98, 0x8000, v98
	v_add_f32_e32 v134, 1.0, v134
	v_rcp_f32_e32 v134, v134
	s_nop 0
	v_mul_f32_e32 v99, v134, v99
	v_lshlrev_b32_e32 v134, 16, v141
	v_mul_f32_e32 v134, 0xbfb8aa3b, v134
	v_exp_f32_e32 v134, v134
	v_add_u32_e32 v99, 0x8000, v99
	v_perm_b32 v98, v99, v98, s33
	v_add_f32_e32 v134, 1.0, v134
	v_rcp_f32_e32 v134, v134
	s_nop 0
	v_mul_f32_e32 v100, v134, v100
	v_and_b32_e32 v134, 0xffff0000, v141
	v_mul_f32_e32 v134, 0xbfb8aa3b, v134
	v_exp_f32_e32 v134, v134
	v_ashrrev_i32_e32 v147, 31, v146
	v_add_u32_e32 v100, 0x8000, v100
	v_lshlrev_b64 v[186:187], 1, v[146:147]
	v_add_f32_e32 v134, 1.0, v134
	v_rcp_f32_e32 v134, v134
	s_nop 0
	v_mul_f32_e32 v101, v134, v101
	v_add_u32_e32 v99, 0x8000, v101
	v_perm_b32 v99, v99, v100, s33
	v_lshl_add_u64 v[100:101], v[144:145], 0, v[186:187]
	global_store_dwordx2 v[100:101], v[98:99], off
	ds_read_b128 v[98:101], v248 offset:38912
	s_waitcnt lgkmcnt(0)
	v_mfma_f32_16x16x32_bf16 v[114:117], v[98:101], v[114:117], 0
	v_add_u32_e32 v134, 16, v188
	v_ashrrev_i32_e32 v135, 31, v134
	v_lshlrev_b64 v[134:135], 12, v[134:135]
	s_nop 4
	v_fma_f32 v0, v108, v118, v114
	s_waitcnt vmcnt(3)
; #define LAS __attribute__((address_space(3)))
; __device__ __forceinline__ unsigned pk2(float lo, float hi) { return __builtin_amdgcn_perm(__builtin_bit_cast(unsigned, hi) + 0x8000u, __builtin_bit_cast(unsigned, lo) + 0x8000u, 0x07060302u); }
; __device__ __forceinline__ float sigmoidf_(float x) { return 1.0f / (1.0f + __expf(-x)); }
; __device__ __forceinline__ void ph_mlstm_out(const Frame& F) {
;     ...
;         for (int tt = 0; tt < 8; ++tt) {
;             const int t = 16 * tt + l15;
;             const v2u ogc[2] = {ogn0, ogn1};
;             if (tt < 7) { ogn0 = *(const v2u*)(ogp + (size_t)(16 * (tt + 1)) * 6144); ogn1 = *(const v2u*)(ogp + (size_t)(16 * (tt + 1)) * 6144 + 16); }
;             bf16x8 qf[4];
; #pragma unroll
;             for (int st = 0; st < 4; ++st) qf[st] = *(const LAS bf16x8*)(lds + MLO_Q_OFF + t * ML_ROW + 16 * g + 64 * st);
;             const int nst = (tt >> 1) + 1;
;             bf16x8 pf[4];
; #pragma unroll
;             for (int st = 0; st < 4; ++st) if (st < nst) pf[st] = *(const LAS bf16x8*)(lds + ML_K_OFF + t * ML_ROW + 16 * g + 64 * st);
;             const float ai = ais[t], rd = rds[t];
; #pragma unroll
;             for (int vt = 0; vt < 2; ++vt) {
;                 f32x4 ci = (f32x4){0.f, 0.f, 0.f, 0.f}, cx = (f32x4){0.f, 0.f, 0.f, 0.f};
; #pragma unroll
;                 for (int st = 0; st < 4; ++st) ci = __builtin_amdgcn_mfma_f32_16x16x32_bf16(cf[vt][st], qf[st], ci, 0, 0, 0);
;                 const LAS unsigned char* vr = lds + ML_V_OFF + (16 * (2 * wave + vt) + l15) * ML_ROW + 16 * g;
; #pragma unroll
;                 for (int st = 0; st < 4; ++st) if (st < nst) cx = __builtin_amdgcn_mfma_f32_16x16x32_bf16(*(const LAS bf16x8*)(vr + 64 * st), pf[st], cx, 0, 0, 0);
;                 const int vcol = h * 256 + 16 * (2 * wave + vt) + 4 * g;
;                 const v2u ogw = ogc[vt];
;                 const float y0 = (ai * ci[0] + cx[0]) * rd * sigmoidf_(bflo(ogw.x)), y1 = (ai * ci[1] + cx[1]) * rd * sigmoidf_(bfhi(ogw.x));
;                 const float y2 = (ai * ci[2] + cx[2]) * rd * sigmoidf_(bflo(ogw.y)), y3 = (ai * ci[3] + cx[3]) * rd * sigmoidf_(bfhi(ogw.y));
;                 v2u w; w.x = pk2(y0, y1); w.y = pk2(y2, y3);
;                 *(v2u*)(YB + (size_t)(t0 + t) * 2048 + vcol) = w;
;             }
	v_lshlrev_b32_e32 v114, 16, v142
	v_mul_f32_e32 v114, 0xbfb8aa3b, v114
	v_exp_f32_e32 v114, v114
	v_mul_f32_e32 v0, v110, v0
	v_fmac_f32_e32 v117, v108, v121
	v_add_f32_e32 v114, 1.0, v114
	v_rcp_f32_e32 v114, v114
	s_nop 0
	v_mul_f32_e32 v0, v114, v0
	v_fma_f32 v114, v108, v119, v115
	v_and_b32_e32 v115, 0xffff0000, v142
	v_mul_f32_e32 v115, 0xbfb8aa3b, v115
	v_exp_f32_e32 v115, v115
	v_mul_f32_e32 v114, v110, v114
	v_add_u32_e32 v0, 0x8000, v0
	v_add_f32_e32 v115, 1.0, v115
	v_rcp_f32_e32 v115, v115
	s_nop 0
	v_mul_f32_e32 v114, v115, v114
	v_fma_f32 v115, v108, v120, v116
	v_lshlrev_b32_e32 v116, 16, v143
	v_mul_f32_e32 v116, 0xbfb8aa3b, v116
	v_exp_f32_e32 v116, v116
	v_mul_f32_e32 v115, v110, v115
	v_mul_f32_e32 v108, v110, v117
	v_and_b32_e32 v110, 0xffff0000, v143
	v_add_f32_e32 v116, 1.0, v116
	v_div_scale_f32 v118, s[56:57], v116, v116, 1.0
	v_rcp_f32_e32 v119, v118
	v_mul_f32_e32 v110, 0xbfb8aa3b, v110
	v_exp_f32_e32 v110, v110
	v_fma_f32 v120, -v118, v119, 1.0
	v_fmac_f32_e32 v119, v120, v119
	v_div_scale_f32 v120, vcc, 1.0, v116, 1.0
	v_mul_f32_e32 v123, v120, v119
	v_fma_f32 v124, -v118, v123, v120
	v_fmac_f32_e32 v123, v124, v119
	v_fma_f32 v118, -v118, v123, v120
	v_div_fmas_f32 v118, v118, v119, v123
	v_div_fixup_f32 v116, v118, v116, 1.0
	v_add_f32_e32 v110, 1.0, v110
	v_mul_f32_e32 v115, v116, v115
	v_div_scale_f32 v116, s[56:57], v110, v110, 1.0
	v_rcp_f32_e32 v117, v116
	v_ashrrev_i32_e32 v123, 31, v122
	v_lshlrev_b64 v[184:185], 1, v[122:123]
	s_mov_b32 s56, 0x62000
	v_fma_f32 v118, -v116, v117, 1.0
	v_fmac_f32_e32 v117, v118, v117
	v_div_scale_f32 v118, vcc, 1.0, v110, 1.0
	v_mul_f32_e32 v119, v118, v117
	v_fma_f32 v120, -v116, v119, v118
	v_fmac_f32_e32 v119, v120, v117
	v_fma_f32 v116, -v116, v119, v118
	v_div_fmas_f32 v116, v116, v117, v119
	v_div_fixup_f32 v110, v116, v110, 1.0
	v_mul_f32_e32 v108, v110, v108
	v_add_u32_e32 v110, 0x8000, v114
	v_perm_b32 v114, v110, v0, s33
	v_add_u32_e32 v0, 0x8000, v108
	v_add_u32_e32 v108, 0x8000, v115
	v_perm_b32 v115, v0, v108, s33
	v_lshl_add_u64 v[116:117], v[144:145], 0, v[184:185]
	global_store_dwordx2 v[116:117], v[114:115], off
	v_add_co_u32_e32 v114, vcc, s56, v138
	v_add_u32_e32 v0, v179, v234
	s_nop 0
	v_addc_co_u32_e32 v115, vcc, 0, v139, vcc
	global_load_dwordx2 v[152:153], v[114:115], off
	global_load_dwordx2 v[148:149], v[114:115], off offset:32
	ds_read_b128 v[114:117], v181
	ds_read_b128 v[118:121], v181 offset:64
	ds_read_b128 v[122:125], v181 offset:128
	ds_read_b128 v[126:129], v181 offset:192
	s_waitcnt lgkmcnt(3)
	v_mfma_f32_16x16x32_bf16 v[140:143], v[94:97], v[114:117], 0
	ds_read_b128 v[130:133], v0 offset:4096
	s_waitcnt vmcnt(5)
	v_lshlrev_b32_e32 v110, 16, v112
	v_mul_f32_e32 v110, 0xbfb8aa3b, v110
	s_waitcnt lgkmcnt(3)
	v_mfma_f32_16x16x32_bf16 v[140:143], v[82:85], v[118:121], v[140:143]
	v_exp_f32_e32 v110, v110
	v_lshl_add_u64 v[144:145], s[22:23], 0, v[134:135]
	v_and_b32_e32 v112, 0xffff0000, v112
	s_waitcnt lgkmcnt(2)
	v_mfma_f32_16x16x32_bf16 v[140:143], v[86:89], v[122:125], v[140:143]
	v_add_f32_e32 v110, 1.0, v110
	v_mul_f32_e32 v112, 0xbfb8aa3b, v112
	v_exp_f32_e32 v112, v112
	s_waitcnt lgkmcnt(0)
	v_mfma_f32_16x16x32_bf16 v[134:137], v[102:105], v[130:133], 0
	v_add_f32_e32 v112, 1.0, v112
	v_mfma_f32_16x16x32_bf16 v[140:143], v[90:93], v[126:129], v[140:143]
	v_mfma_f32_16x16x32_bf16 v[130:133], v[98:101], v[130:133], 0
	s_nop 6
	v_fma_f32 v108, v109, v140, v134
	v_div_scale_f32 v134, s[56:57], v110, v110, 1.0
	v_rcp_f32_e32 v140, v134
	v_mul_f32_e32 v108, v111, v108
	v_fmac_f32_e32 v137, v109, v143
	v_fma_f32 v146, -v134, v140, 1.0
	v_fmac_f32_e32 v140, v146, v140
	v_div_scale_f32 v146, vcc, 1.0, v110, 1.0
	v_mul_f32_e32 v147, v146, v140
	v_fma_f32 v150, -v134, v147, v146
	v_fmac_f32_e32 v147, v150, v140
	v_fma_f32 v134, -v134, v147, v146
	v_div_fmas_f32 v134, v134, v140, v147
	v_div_fixup_f32 v110, v134, v110, 1.0
	v_div_scale_f32 v134, s[56:57], v112, v112, 1.0
	v_mul_f32_e32 v108, v110, v108
	v_fma_f32 v110, v109, v141, v135
	v_rcp_f32_e32 v135, v134
	v_mul_f32_e32 v110, v111, v110
	v_add_u32_e32 v108, 0x8000, v108
	v_fma_f32 v140, -v134, v135, 1.0
	v_fmac_f32_e32 v135, v140, v135
	v_div_scale_f32 v140, vcc, 1.0, v112, 1.0
	v_mul_f32_e32 v141, v140, v135
	v_fma_f32 v146, -v134, v141, v140
	v_fmac_f32_e32 v141, v146, v135
	v_fma_f32 v134, -v134, v141, v140
	v_div_fmas_f32 v134, v134, v135, v141
	v_div_fixup_f32 v112, v134, v112, 1.0
	v_lshlrev_b32_e32 v134, 16, v113
	v_mul_f32_e32 v134, 0xbfb8aa3b, v134
	v_exp_f32_e32 v134, v134
	v_mul_f32_e32 v110, v112, v110
	v_fma_f32 v112, v109, v142, v136
	v_and_b32_e32 v113, 0xffff0000, v113
	v_add_f32_e32 v134, 1.0, v134
	v_div_scale_f32 v135, s[56:57], v134, v134, 1.0
	v_rcp_f32_e32 v136, v135
	v_mul_f32_e32 v113, 0xbfb8aa3b, v113
	v_exp_f32_e32 v113, v113
	v_mul_f32_e32 v112, v111, v112
	v_fma_f32 v140, -v135, v136, 1.0
	v_fmac_f32_e32 v136, v140, v136
	v_div_scale_f32 v140, vcc, 1.0, v134, 1.0
	v_mul_f32_e32 v141, v140, v136
	v_fma_f32 v142, -v135, v141, v140
	v_fmac_f32_e32 v141, v142, v136
	v_fma_f32 v135, -v135, v141, v140
	v_div_fmas_f32 v135, v135, v136, v141
	v_add_f32_e32 v113, 1.0, v113
	v_div_fixup_f32 v134, v135, v134, 1.0
	v_div_scale_f32 v135, s[56:57], v113, v113, 1.0
	v_rcp_f32_e32 v136, v135
	v_mul_f32_e32 v134, v134, v112
	v_mul_f32_e32 v112, v111, v137
	v_add_u32_e32 v110, 0x8000, v110
	v_fma_f32 v137, -v135, v136, 1.0
	v_fmac_f32_e32 v136, v137, v136
	v_div_scale_f32 v137, vcc, 1.0, v113, 1.0
	v_mul_f32_e32 v140, v137, v136
	v_fma_f32 v141, -v135, v140, v137
	v_fmac_f32_e32 v140, v141, v136
	v_fma_f32 v135, -v135, v140, v137
	v_div_fmas_f32 v135, v135, v136, v140
	v_div_fixup_f32 v113, v135, v113, 1.0
	v_mul_f32_e32 v113, v113, v112
	v_perm_b32 v112, v110, v108, s33
	v_add_u32_e32 v108, 0x8000, v113
	v_add_u32_e32 v110, 0x8000, v134
	v_perm_b32 v113, v108, v110, s33
	v_lshl_add_u64 v[134:135], v[144:145], 0, v[186:187]
	global_store_dwordx2 v[134:135], v[112:113], off
	v_mfma_f32_16x16x32_bf16 v[112:115], v[78:81], v[114:117], 0
	s_waitcnt vmcnt(5)
; #define LAS __attribute__((address_space(3)))
; __device__ __forceinline__ unsigned pk2(float lo, float hi) { return __builtin_amdgcn_perm(__builtin_bit_cast(unsigned, hi) + 0x8000u, __builtin_bit_cast(unsigned, lo) + 0x8000u, 0x07060302u); }
; __device__ __forceinline__ float sigmoidf_(float x) { return 1.0f / (1.0f + __expf(-x)); }
; __device__ __forceinline__ void ph_mlstm_out(const Frame& F) {
;     ...
;         for (int tt = 0; tt < 8; ++tt) {
;             const int t = 16 * tt + l15;
;             const v2u ogc[2] = {ogn0, ogn1};
;             if (tt < 7) { ogn0 = *(const v2u*)(ogp + (size_t)(16 * (tt + 1)) * 6144); ogn1 = *(const v2u*)(ogp + (size_t)(16 * (tt + 1)) * 6144 + 16); }
;             bf16x8 qf[4];
; #pragma unroll
;             for (int st = 0; st < 4; ++st) qf[st] = *(const LAS bf16x8*)(lds + MLO_Q_OFF + t * ML_ROW + 16 * g + 64 * st);
;             const int nst = (tt >> 1) + 1;
;             bf16x8 pf[4];
; #pragma unroll
;             for (int st = 0; st < 4; ++st) if (st < nst) pf[st] = *(const LAS bf16x8*)(lds + ML_K_OFF + t * ML_ROW + 16 * g + 64 * st);
;             const float ai = ais[t], rd = rds[t];
; #pragma unroll
;             for (int vt = 0; vt < 2; ++vt) {
;                 f32x4 ci = (f32x4){0.f, 0.f, 0.f, 0.f}, cx = (f32x4){0.f, 0.f, 0.f, 0.f};
; #pragma unroll
;                 for (int st = 0; st < 4; ++st) ci = __builtin_amdgcn_mfma_f32_16x16x32_bf16(cf[vt][st], qf[st], ci, 0, 0, 0);
;                 const LAS unsigned char* vr = lds + ML_V_OFF + (16 * (2 * wave + vt) + l15) * ML_ROW + 16 * g;
; #pragma unroll
;                 for (int st = 0; st < 4; ++st) if (st < nst) cx = __builtin_amdgcn_mfma_f32_16x16x32_bf16(*(const LAS bf16x8*)(vr + 64 * st), pf[st], cx, 0, 0, 0);
;                 const int vcol = h * 256 + 16 * (2 * wave + vt) + 4 * g;
;                 const v2u ogw = ogc[vt];
;                 const float y0 = (ai * ci[0] + cx[0]) * rd * sigmoidf_(bflo(ogw.x)), y1 = (ai * ci[1] + cx[1]) * rd * sigmoidf_(bfhi(ogw.x));
;                 const float y2 = (ai * ci[2] + cx[2]) * rd * sigmoidf_(bflo(ogw.y)), y3 = (ai * ci[3] + cx[3]) * rd * sigmoidf_(bfhi(ogw.y));
;                 v2u w; w.x = pk2(y0, y1); w.y = pk2(y2, y3);
;                 *(v2u*)(YB + (size_t)(t0 + t) * 2048 + vcol) = w;
;             }
	v_lshlrev_b32_e32 v110, 16, v106
	v_mul_f32_e32 v110, 0xbfb8aa3b, v110
	v_exp_f32_e32 v110, v110
	v_mfma_f32_16x16x32_bf16 v[112:115], v[66:69], v[118:121], v[112:115]
	v_and_b32_e32 v106, 0xffff0000, v106
	v_mul_f32_e32 v106, 0xbfb8aa3b, v106
	v_add_f32_e32 v110, 1.0, v110
	v_mfma_f32_16x16x32_bf16 v[112:115], v[70:73], v[122:125], v[112:115]
	v_exp_f32_e32 v106, v106
	s_nop 0
	v_add_f32_e32 v106, 1.0, v106
	v_mfma_f32_16x16x32_bf16 v[112:115], v[74:77], v[126:129], v[112:115]
	s_nop 7
	v_fma_f32 v108, v109, v112, v130
	v_div_scale_f32 v112, s[56:57], v110, v110, 1.0
	v_rcp_f32_e32 v116, v112
	v_mul_f32_e32 v108, v111, v108
	v_fmac_f32_e32 v133, v109, v115
	v_fma_f32 v117, -v112, v116, 1.0
	v_fmac_f32_e32 v116, v117, v116
	v_div_scale_f32 v117, vcc, 1.0, v110, 1.0
	v_mul_f32_e32 v118, v117, v116
	v_fma_f32 v119, -v112, v118, v117
	v_fmac_f32_e32 v118, v119, v116
	v_fma_f32 v112, -v112, v118, v117
	v_div_fmas_f32 v112, v112, v116, v118
	v_div_fixup_f32 v110, v112, v110, 1.0
	v_div_scale_f32 v112, s[56:57], v106, v106, 1.0
	v_mul_f32_e32 v108, v110, v108
	v_fma_f32 v110, v109, v113, v131
	v_rcp_f32_e32 v113, v112
	v_mul_f32_e32 v110, v111, v110
	v_add_u32_e32 v108, 0x8000, v108
	v_fma_f32 v116, -v112, v113, 1.0
	v_fmac_f32_e32 v113, v116, v113
	v_div_scale_f32 v116, vcc, 1.0, v106, 1.0
	v_mul_f32_e32 v117, v116, v113
	v_fma_f32 v118, -v112, v117, v116
	v_fmac_f32_e32 v117, v118, v113
	v_fma_f32 v112, -v112, v117, v116
	v_div_fmas_f32 v112, v112, v113, v117
	v_div_fixup_f32 v106, v112, v106, 1.0
	v_lshlrev_b32_e32 v112, 16, v107
	v_mul_f32_e32 v112, 0xbfb8aa3b, v112
	v_exp_f32_e32 v112, v112
	v_mul_f32_e32 v106, v106, v110
	v_fma_f32 v110, v109, v114, v132
	v_and_b32_e32 v107, 0xffff0000, v107
	v_add_f32_e32 v112, 1.0, v112
	v_div_scale_f32 v113, s[56:57], v112, v112, 1.0
	v_rcp_f32_e32 v114, v113
	v_mul_f32_e32 v107, 0xbfb8aa3b, v107
	v_exp_f32_e32 v107, v107
	v_mul_f32_e32 v110, v111, v110
	v_fma_f32 v116, -v113, v114, 1.0
	v_fmac_f32_e32 v114, v116, v114
	v_div_scale_f32 v116, vcc, 1.0, v112, 1.0
	v_mul_f32_e32 v117, v116, v114
	v_fma_f32 v118, -v113, v117, v116
	v_fmac_f32_e32 v117, v118, v114
	v_fma_f32 v113, -v113, v117, v116
	v_div_fmas_f32 v113, v113, v114, v117
	v_add_f32_e32 v107, 1.0, v107
	v_div_fixup_f32 v112, v113, v112, 1.0
	v_mul_f32_e32 v109, v111, v133
	v_div_scale_f32 v111, s[56:57], v107, v107, 1.0
	v_mul_f32_e32 v110, v112, v110
	v_rcp_f32_e32 v112, v111
	v_add_u32_e32 v106, 0x8000, v106
	v_perm_b32 v106, v106, v108, s33
	v_add_u32_e32 v108, 0x8000, v110
	v_fma_f32 v113, -v111, v112, 1.0
	v_fmac_f32_e32 v112, v113, v112
	v_div_scale_f32 v113, vcc, 1.0, v107, 1.0
	v_mul_f32_e32 v114, v113, v112
	v_fma_f32 v115, -v111, v114, v113
	v_fmac_f32_e32 v114, v115, v112
	v_fma_f32 v111, -v111, v114, v113
	v_div_fmas_f32 v111, v111, v112, v114
	v_div_fixup_f32 v107, v111, v107, 1.0
	v_mul_f32_e32 v107, v107, v109
	v_add_u32_e32 v107, 0x8000, v107
	v_perm_b32 v107, v107, v108, s33
	v_lshl_add_u64 v[108:109], v[144:145], 0, v[184:185]
	s_mov_b32 s56, 0x92000
	global_store_dwordx2 v[108:109], v[106:107], off
	v_add_co_u32_e32 v106, vcc, s56, v138
	s_nop 1
	v_addc_co_u32_e32 v107, vcc, 0, v139, vcc
	global_load_dwordx2 v[146:147], v[106:107], off
	global_load_dwordx2 v[140:141], v[106:107], off offset:32
	ds_read_b128 v[114:117], v181 offset:4352
	ds_read_b128 v[118:121], v181 offset:4416
	ds_read_b128 v[122:125], v181 offset:4480
	ds_read_b128 v[126:129], v181 offset:4544
	ds_read_b128 v[110:113], v0 offset:8448
	ds_read_b128 v[130:133], v0 offset:8512
	ds_read2_b32 v[142:143], v158 offset0:160 offset1:176
	ds_read2_b32 v[144:145], v159 offset0:32 offset1:48
	v_add_u32_e32 v106, 32, v188
	s_waitcnt lgkmcnt(7)
	v_mfma_f32_16x16x32_bf16 v[154:157], v[94:97], v[114:117], 0
	v_ashrrev_i32_e32 v107, 31, v106
	v_lshlrev_b64 v[106:107], 12, v[106:107]
	v_lshl_add_u64 v[150:151], s[22:23], 0, v[106:107]
	ds_read_b128 v[106:109], v247 offset:38976
	s_waitcnt lgkmcnt(7)
	v_mfma_f32_16x16x32_bf16 v[154:157], v[82:85], v[118:121], v[154:157]
	s_waitcnt lgkmcnt(4)
	v_mfma_f32_16x16x32_bf16 v[134:137], v[102:105], v[110:113], 0
	v_mfma_f32_16x16x32_bf16 v[154:157], v[86:89], v[122:125], v[154:157]
	s_waitcnt lgkmcnt(0)
	v_mfma_f32_16x16x32_bf16 v[134:137], v[106:109], v[130:133], v[134:137]
	v_mfma_f32_16x16x32_bf16 v[154:157], v[90:93], v[126:129], v[154:157]
	v_mfma_f32_16x16x32_bf16 v[114:117], v[78:81], v[114:117], 0
	v_mfma_f32_16x16x32_bf16 v[114:117], v[66:69], v[118:121], v[114:117]
	s_nop 5
	v_fma_f32 v134, v142, v154, v134
	s_waitcnt vmcnt(5)
	v_lshlrev_b32_e32 v154, 16, v152
	v_mul_f32_e32 v154, 0xbfb8aa3b, v154
	v_exp_f32_e32 v154, v154
	v_and_b32_e32 v152, 0xffff0000, v152
	v_mul_f32_e32 v152, 0xbfb8aa3b, v152
	v_exp_f32_e32 v152, v152
	v_add_f32_e32 v154, 1.0, v154
	v_div_scale_f32 v160, s[56:57], v154, v154, 1.0
	v_rcp_f32_e32 v161, v160
	v_mul_f32_e32 v134, v144, v134
	v_add_f32_e32 v152, 1.0, v152
	v_fma_f32 v135, v142, v155, v135
	v_fma_f32 v164, -v160, v161, 1.0
	v_fmac_f32_e32 v161, v164, v161
	v_div_scale_f32 v164, vcc, 1.0, v154, 1.0
	v_mul_f32_e32 v165, v164, v161
	v_fma_f32 v166, -v160, v165, v164
	v_fmac_f32_e32 v165, v166, v161
	v_fma_f32 v160, -v160, v165, v164
	v_div_fmas_f32 v160, v160, v161, v165
	v_div_fixup_f32 v154, v160, v154, 1.0
	v_mul_f32_e32 v134, v154, v134
	v_div_scale_f32 v154, s[56:57], v152, v152, 1.0
	v_rcp_f32_e32 v155, v154
	v_mul_f32_e32 v135, v144, v135
	v_fma_f32 v136, v142, v156, v136
	v_mul_f32_e32 v136, v144, v136
	v_fma_f32 v160, -v154, v155, 1.0
	v_fmac_f32_e32 v155, v160, v155
	v_div_scale_f32 v160, vcc, 1.0, v152, 1.0
	v_mul_f32_e32 v161, v160, v155
	v_fma_f32 v164, -v154, v161, v160
	v_fmac_f32_e32 v161, v164, v155
	v_fma_f32 v154, -v154, v161, v160
	v_div_fmas_f32 v154, v154, v155, v161
	v_div_fixup_f32 v152, v154, v152, 1.0
	v_mul_f32_e32 v135, v152, v135
	v_lshlrev_b32_e32 v152, 16, v153
	v_mul_f32_e32 v152, 0xbfb8aa3b, v152
	v_exp_f32_e32 v152, v152
	v_fmac_f32_e32 v137, v142, v157
	s_waitcnt vmcnt(4)
; #define LAS __attribute__((address_space(3)))
; __device__ __forceinline__ unsigned pk2(float lo, float hi) { return __builtin_amdgcn_perm(__builtin_bit_cast(unsigned, hi) + 0x8000u, __builtin_bit_cast(unsigned, lo) + 0x8000u, 0x07060302u); }
; __device__ __forceinline__ float sigmoidf_(float x) { return 1.0f / (1.0f + __expf(-x)); }
; __device__ __forceinline__ void ph_mlstm_out(const Frame& F) {
;     ...
;         for (int tt = 0; tt < 8; ++tt) {
;             const int t = 16 * tt + l15;
;             const v2u ogc[2] = {ogn0, ogn1};
;             if (tt < 7) { ogn0 = *(const v2u*)(ogp + (size_t)(16 * (tt + 1)) * 6144); ogn1 = *(const v2u*)(ogp + (size_t)(16 * (tt + 1)) * 6144 + 16); }
;             bf16x8 qf[4];
; #pragma unroll
;             for (int st = 0; st < 4; ++st) qf[st] = *(const LAS bf16x8*)(lds + MLO_Q_OFF + t * ML_ROW + 16 * g + 64 * st);
;             const int nst = (tt >> 1) + 1;
;             bf16x8 pf[4];
; #pragma unroll
;             for (int st = 0; st < 4; ++st) if (st < nst) pf[st] = *(const LAS bf16x8*)(lds + ML_K_OFF + t * ML_ROW + 16 * g + 64 * st);
;             const float ai = ais[t], rd = rds[t];
; #pragma unroll
;             for (int vt = 0; vt < 2; ++vt) {
;                 f32x4 ci = (f32x4){0.f, 0.f, 0.f, 0.f}, cx = (f32x4){0.f, 0.f, 0.f, 0.f};
; #pragma unroll
;                 for (int st = 0; st < 4; ++st) ci = __builtin_amdgcn_mfma_f32_16x16x32_bf16(cf[vt][st], qf[st], ci, 0, 0, 0);
;                 const LAS unsigned char* vr = lds + ML_V_OFF + (16 * (2 * wave + vt) + l15) * ML_ROW + 16 * g;
; #pragma unroll
;                 for (int st = 0; st < 4; ++st) if (st < nst) cx = __builtin_amdgcn_mfma_f32_16x16x32_bf16(*(const LAS bf16x8*)(vr + 64 * st), pf[st], cx, 0, 0, 0);
;                 const int vcol = h * 256 + 16 * (2 * wave + vt) + 4 * g;
;                 const v2u ogw = ogc[vt];
;                 const float y0 = (ai * ci[0] + cx[0]) * rd * sigmoidf_(bflo(ogw.x)), y1 = (ai * ci[1] + cx[1]) * rd * sigmoidf_(bfhi(ogw.x));
;                 const float y2 = (ai * ci[2] + cx[2]) * rd * sigmoidf_(bflo(ogw.y)), y3 = (ai * ci[3] + cx[3]) * rd * sigmoidf_(bfhi(ogw.y));
;                 v2u w; w.x = pk2(y0, y1); w.y = pk2(y2, y3);
;                 *(v2u*)(YB + (size_t)(t0 + t) * 2048 + vcol) = w;
;             }
	v_lshlrev_b32_e32 v118, 16, v148
	v_mul_f32_e32 v137, v144, v137
	v_add_f32_e32 v152, 1.0, v152
	v_div_scale_f32 v154, s[56:57], v152, v152, 1.0
	v_rcp_f32_e32 v155, v154
	v_mul_f32_e32 v118, 0xbfb8aa3b, v118
	v_add_u32_e32 v135, 0x8000, v135
	v_add_u32_e32 v134, 0x8000, v134
	v_fma_f32 v156, -v154, v155, 1.0
	v_fmac_f32_e32 v155, v156, v155
	v_div_scale_f32 v156, vcc, 1.0, v152, 1.0
	v_mul_f32_e32 v160, v156, v155
	v_fma_f32 v161, -v154, v160, v156
	v_fmac_f32_e32 v160, v161, v155
	v_fma_f32 v154, -v154, v160, v156
	v_div_fmas_f32 v154, v154, v155, v160
	v_div_fixup_f32 v152, v154, v152, 1.0
	v_mul_f32_e32 v136, v152, v136
	v_and_b32_e32 v152, 0xffff0000, v153
	v_mul_f32_e32 v152, 0xbfb8aa3b, v152
	v_exp_f32_e32 v152, v152
	v_exp_f32_e32 v118, v118
	v_perm_b32 v134, v135, v134, s33
	v_add_u32_e32 v136, 0x8000, v136
	v_add_f32_e32 v152, 1.0, v152
	v_div_scale_f32 v153, s[56:57], v152, v152, 1.0
	v_rcp_f32_e32 v154, v153
	v_add_f32_e32 v118, 1.0, v118
	v_div_scale_f32 v119, s[56:57], v118, v118, 1.0
	v_fma_f32 v155, -v153, v154, 1.0
	v_fmac_f32_e32 v154, v155, v154
	v_div_scale_f32 v155, vcc, 1.0, v152, 1.0
	v_mul_f32_e32 v156, v155, v154
	v_fma_f32 v157, -v153, v156, v155
	v_fmac_f32_e32 v156, v157, v154
	v_fma_f32 v153, -v153, v156, v155
	v_div_fmas_f32 v153, v153, v154, v156
	v_div_fixup_f32 v152, v153, v152, 1.0
	v_mul_f32_e32 v137, v152, v137
	v_add_u32_e32 v135, 0x8000, v137
	v_perm_b32 v135, v135, v136, s33
	v_lshl_add_u64 v[136:137], v[150:151], 0, v[186:187]
	global_store_dwordx2 v[136:137], v[134:135], off
	v_mfma_f32_16x16x32_bf16 v[134:137], v[98:101], v[110:113], 0
	ds_read_b128 v[110:113], v248 offset:38976
	v_rcp_f32_e32 v120, v119
	v_add_u32_e32 v152, 48, v188
	v_mfma_f32_16x16x32_bf16 v[114:117], v[70:73], v[122:125], v[114:117]
	v_ashrrev_i32_e32 v153, 31, v152
	v_fma_f32 v121, -v119, v120, 1.0
	v_fmac_f32_e32 v120, v121, v120
	v_div_scale_f32 v121, vcc, 1.0, v118, 1.0
	s_waitcnt lgkmcnt(0)
	v_mfma_f32_16x16x32_bf16 v[130:133], v[110:113], v[130:133], v[134:137]
	v_mul_f32_e32 v122, v121, v120
	v_fma_f32 v123, -v119, v122, v121
	v_fmac_f32_e32 v122, v123, v120
	v_mfma_f32_16x16x32_bf16 v[114:117], v[74:77], v[126:129], v[114:117]
	v_fma_f32 v119, -v119, v122, v121
	v_div_fmas_f32 v119, v119, v120, v122
	v_div_fixup_f32 v118, v119, v118, 1.0
	v_lshlrev_b64 v[152:153], 12, v[152:153]
	v_lshl_add_u64 v[156:157], s[22:23], 0, v[152:153]
	s_nop 2
	v_fma_f32 v114, v142, v114, v130
	v_mul_f32_e32 v114, v144, v114
	v_mul_f32_e32 v114, v118, v114
	v_and_b32_e32 v118, 0xffff0000, v148
	v_mul_f32_e32 v118, 0xbfb8aa3b, v118
	v_exp_f32_e32 v118, v118
	v_fma_f32 v115, v142, v115, v131
	v_mul_f32_e32 v115, v144, v115
	v_fma_f32 v116, v142, v116, v132
	v_add_f32_e32 v118, 1.0, v118
	v_div_scale_f32 v119, s[56:57], v118, v118, 1.0
	v_rcp_f32_e32 v120, v119
	v_mul_f32_e32 v116, v144, v116
	v_fmac_f32_e32 v133, v142, v117
	v_mul_f32_e32 v117, v144, v133
	v_fma_f32 v121, -v119, v120, 1.0
	v_fmac_f32_e32 v120, v121, v120
	v_div_scale_f32 v121, vcc, 1.0, v118, 1.0
	v_mul_f32_e32 v122, v121, v120
	v_fma_f32 v123, -v119, v122, v121
	v_fmac_f32_e32 v122, v123, v120
	v_fma_f32 v119, -v119, v122, v121
	v_div_fmas_f32 v119, v119, v120, v122
	v_div_fixup_f32 v118, v119, v118, 1.0
	v_mul_f32_e32 v115, v118, v115
	v_lshlrev_b32_e32 v118, 16, v149
	v_mul_f32_e32 v118, 0xbfb8aa3b, v118
	v_exp_f32_e32 v118, v118
	v_add_u32_e32 v115, 0x8000, v115
	v_add_u32_e32 v114, 0x8000, v114
	v_perm_b32 v114, v115, v114, s33
	v_add_f32_e32 v118, 1.0, v118
	v_div_scale_f32 v119, s[56:57], v118, v118, 1.0
	v_rcp_f32_e32 v120, v119
	s_waitcnt vmcnt(2)
	v_lshlrev_b32_e32 v144, 16, v146
	v_mul_f32_e32 v144, 0xbfb8aa3b, v144
	v_exp_f32_e32 v144, v144
	v_fma_f32 v121, -v119, v120, 1.0
	v_fmac_f32_e32 v120, v121, v120
	v_div_scale_f32 v121, vcc, 1.0, v118, 1.0
	v_mul_f32_e32 v122, v121, v120
	v_fma_f32 v123, -v119, v122, v121
	v_fmac_f32_e32 v122, v123, v120
	v_fma_f32 v119, -v119, v122, v121
	v_div_fmas_f32 v119, v119, v120, v122
	v_div_fixup_f32 v118, v119, v118, 1.0
	v_mul_f32_e32 v116, v118, v116
	v_and_b32_e32 v118, 0xffff0000, v149
	v_mul_f32_e32 v118, 0xbfb8aa3b, v118
	v_exp_f32_e32 v118, v118
	v_add_u32_e32 v116, 0x8000, v116
	v_add_f32_e32 v144, 1.0, v144
	v_and_b32_e32 v146, 0xffff0000, v146
	v_add_f32_e32 v118, 1.0, v118
	v_div_scale_f32 v119, s[56:57], v118, v118, 1.0
	v_rcp_f32_e32 v120, v119
	s_mov_b32 s56, 0xc2000
	v_mul_f32_e32 v146, 0xbfb8aa3b, v146
	v_exp_f32_e32 v146, v146
	v_fma_f32 v121, -v119, v120, 1.0
	v_fmac_f32_e32 v120, v121, v120
	v_div_scale_f32 v121, vcc, 1.0, v118, 1.0
	v_mul_f32_e32 v122, v121, v120
	v_fma_f32 v123, -v119, v122, v121
	v_fmac_f32_e32 v122, v123, v120
	v_fma_f32 v119, -v119, v122, v121
	v_div_fmas_f32 v119, v119, v120, v122
	v_div_fixup_f32 v118, v119, v118, 1.0
	v_mul_f32_e32 v117, v118, v117
	v_add_u32_e32 v115, 0x8000, v117
	v_perm_b32 v115, v115, v116, s33
	v_lshl_add_u64 v[116:117], v[150:151], 0, v[184:185]
	global_store_dwordx2 v[116:117], v[114:115], off
	v_add_co_u32_e32 v114, vcc, s56, v138
	v_add_f32_e32 v146, 1.0, v146
	s_nop 0
	v_addc_co_u32_e32 v115, vcc, 0, v139, vcc
	global_load_dwordx2 v[150:151], v[114:115], off
	global_load_dwordx2 v[148:149], v[114:115], off offset:32
	ds_read_b128 v[114:117], v181 offset:8704
	ds_read_b128 v[118:121], v181 offset:8768
	ds_read_b128 v[122:125], v181 offset:8832
	ds_read_b128 v[126:129], v181 offset:8896
	ds_read_b128 v[130:133], v0 offset:12800
	ds_read_b128 v[134:137], v0 offset:12864
	s_waitcnt lgkmcnt(5)
	v_mfma_f32_16x16x32_bf16 v[164:167], v[94:97], v[114:117], 0
	s_waitcnt lgkmcnt(4)
	v_mfma_f32_16x16x32_bf16 v[164:167], v[82:85], v[118:121], v[164:167]
	s_waitcnt lgkmcnt(1)
; #define LAS __attribute__((address_space(3)))
; __device__ __forceinline__ unsigned pk2(float lo, float hi) { return __builtin_amdgcn_perm(__builtin_bit_cast(unsigned, hi) + 0x8000u, __builtin_bit_cast(unsigned, lo) + 0x8000u, 0x07060302u); }
; __device__ __forceinline__ float sigmoidf_(float x) { return 1.0f / (1.0f + __expf(-x)); }
; __device__ __forceinline__ void ph_mlstm_out(const Frame& F) {
;     ...
;         for (int tt = 0; tt < 8; ++tt) {
;             const int t = 16 * tt + l15;
;             const v2u ogc[2] = {ogn0, ogn1};
;             if (tt < 7) { ogn0 = *(const v2u*)(ogp + (size_t)(16 * (tt + 1)) * 6144); ogn1 = *(const v2u*)(ogp + (size_t)(16 * (tt + 1)) * 6144 + 16); }
;             bf16x8 qf[4];
; #pragma unroll
;             for (int st = 0; st < 4; ++st) qf[st] = *(const LAS bf16x8*)(lds + MLO_Q_OFF + t * ML_ROW + 16 * g + 64 * st);
;             const int nst = (tt >> 1) + 1;
;             bf16x8 pf[4];
; #pragma unroll
;             for (int st = 0; st < 4; ++st) if (st < nst) pf[st] = *(const LAS bf16x8*)(lds + ML_K_OFF + t * ML_ROW + 16 * g + 64 * st);
;             const float ai = ais[t], rd = rds[t];
; #pragma unroll
;             for (int vt = 0; vt < 2; ++vt) {
;                 f32x4 ci = (f32x4){0.f, 0.f, 0.f, 0.f}, cx = (f32x4){0.f, 0.f, 0.f, 0.f};
; #pragma unroll
;                 for (int st = 0; st < 4; ++st) ci = __builtin_amdgcn_mfma_f32_16x16x32_bf16(cf[vt][st], qf[st], ci, 0, 0, 0);
;                 const LAS unsigned char* vr = lds + ML_V_OFF + (16 * (2 * wave + vt) + l15) * ML_ROW + 16 * g;
; #pragma unroll
;                 for (int st = 0; st < 4; ++st) if (st < nst) cx = __builtin_amdgcn_mfma_f32_16x16x32_bf16(*(const LAS bf16x8*)(vr + 64 * st), pf[st], cx, 0, 0, 0);
;                 const int vcol = h * 256 + 16 * (2 * wave + vt) + 4 * g;
;                 const v2u ogw = ogc[vt];
;                 const float y0 = (ai * ci[0] + cx[0]) * rd * sigmoidf_(bflo(ogw.x)), y1 = (ai * ci[1] + cx[1]) * rd * sigmoidf_(bfhi(ogw.x));
;                 const float y2 = (ai * ci[2] + cx[2]) * rd * sigmoidf_(bflo(ogw.y)), y3 = (ai * ci[3] + cx[3]) * rd * sigmoidf_(bfhi(ogw.y));
;                 v2u w; w.x = pk2(y0, y1); w.y = pk2(y2, y3);
;                 *(v2u*)(YB + (size_t)(t0 + t) * 2048 + vcol) = w;
;             }
	v_mfma_f32_16x16x32_bf16 v[152:155], v[102:105], v[130:133], 0
	v_mfma_f32_16x16x32_bf16 v[164:167], v[86:89], v[122:125], v[164:167]
	s_waitcnt lgkmcnt(0)
	v_mfma_f32_16x16x32_bf16 v[152:155], v[106:109], v[134:137], v[152:155]
	v_mfma_f32_16x16x32_bf16 v[164:167], v[90:93], v[126:129], v[164:167]
	v_mfma_f32_16x16x32_bf16 v[114:117], v[78:81], v[114:117], 0
	v_mfma_f32_16x16x32_bf16 v[114:117], v[66:69], v[118:121], v[114:117]
	s_nop 5
	v_fma_f32 v142, v143, v164, v152
	v_div_scale_f32 v152, s[56:57], v144, v144, 1.0
	v_rcp_f32_e32 v160, v152
	v_mul_f32_e32 v142, v145, v142
	s_waitcnt vmcnt(4)
	v_lshlrev_b32_e32 v118, 16, v140
	v_mul_f32_e32 v118, 0xbfb8aa3b, v118
	v_fma_f32 v161, -v152, v160, 1.0
	v_fmac_f32_e32 v160, v161, v160
	v_div_scale_f32 v161, vcc, 1.0, v144, 1.0
	v_mul_f32_e32 v164, v161, v160
	v_fma_f32 v183, -v152, v164, v161
	v_fmac_f32_e32 v164, v183, v160
	v_fma_f32 v152, -v152, v164, v161
	v_div_fmas_f32 v152, v152, v160, v164
	v_div_fixup_f32 v144, v152, v144, 1.0
	v_div_scale_f32 v152, s[56:57], v146, v146, 1.0
	v_mul_f32_e32 v142, v144, v142
	v_fma_f32 v144, v143, v165, v153
	v_rcp_f32_e32 v153, v152
	v_mul_f32_e32 v144, v145, v144
	v_exp_f32_e32 v118, v118
	v_fmac_f32_e32 v155, v143, v167
	v_fma_f32 v160, -v152, v153, 1.0
	v_fmac_f32_e32 v153, v160, v153
	v_div_scale_f32 v160, vcc, 1.0, v146, 1.0
	v_mul_f32_e32 v161, v160, v153
	v_fma_f32 v164, -v152, v161, v160
	v_fmac_f32_e32 v161, v164, v153
	v_fma_f32 v152, -v152, v161, v160
	v_div_fmas_f32 v152, v152, v153, v161
	v_div_fixup_f32 v146, v152, v146, 1.0
	v_lshlrev_b32_e32 v152, 16, v147
	v_mul_f32_e32 v152, 0xbfb8aa3b, v152
	v_exp_f32_e32 v152, v152
	v_mul_f32_e32 v144, v146, v144
	v_fma_f32 v146, v143, v166, v154
	v_and_b32_e32 v147, 0xffff0000, v147
	v_add_f32_e32 v152, 1.0, v152
	v_div_scale_f32 v153, s[56:57], v152, v152, 1.0
	v_rcp_f32_e32 v154, v153
	v_mul_f32_e32 v147, 0xbfb8aa3b, v147
	v_exp_f32_e32 v147, v147
	v_mul_f32_e32 v146, v145, v146
	v_fma_f32 v160, -v153, v154, 1.0
	v_fmac_f32_e32 v154, v160, v154
	v_div_scale_f32 v160, vcc, 1.0, v152, 1.0
	v_mul_f32_e32 v161, v160, v154
	v_fma_f32 v164, -v153, v161, v160
	v_fmac_f32_e32 v161, v164, v154
	v_fma_f32 v153, -v153, v161, v160
	v_div_fmas_f32 v153, v153, v154, v161
	v_add_f32_e32 v147, 1.0, v147
	v_div_fixup_f32 v152, v153, v152, 1.0
	v_div_scale_f32 v153, s[56:57], v147, v147, 1.0
	v_rcp_f32_e32 v154, v153
	v_add_f32_e32 v118, 1.0, v118
	v_mul_f32_e32 v152, v152, v146
	v_mul_f32_e32 v146, v145, v155
	v_fma_f32 v155, -v153, v154, 1.0
	v_div_scale_f32 v119, s[56:57], v118, v118, 1.0
	v_fmac_f32_e32 v154, v155, v154
	v_div_scale_f32 v155, vcc, 1.0, v147, 1.0
	v_rcp_f32_e32 v120, v119
	v_mul_f32_e32 v160, v155, v154
	v_fma_f32 v161, -v153, v160, v155
	v_mfma_f32_16x16x32_bf16 v[130:133], v[98:101], v[130:133], 0
	v_fmac_f32_e32 v160, v161, v154
	v_fma_f32 v153, -v153, v160, v155
	v_fma_f32 v121, -v119, v120, 1.0
	v_mfma_f32_16x16x32_bf16 v[114:117], v[70:73], v[122:125], v[114:117]
	v_div_fmas_f32 v153, v153, v154, v160
	v_fmac_f32_e32 v120, v121, v120
	v_div_scale_f32 v121, vcc, 1.0, v118, 1.0
	v_mfma_f32_16x16x32_bf16 v[130:133], v[110:113], v[134:137], v[130:133]
	v_mul_f32_e32 v122, v121, v120
	v_fma_f32 v123, -v119, v122, v121
	v_fmac_f32_e32 v122, v123, v120
	v_mfma_f32_16x16x32_bf16 v[114:117], v[74:77], v[126:129], v[114:117]
	v_fma_f32 v119, -v119, v122, v121
	v_div_fmas_f32 v119, v119, v120, v122
	v_div_fixup_f32 v118, v119, v118, 1.0
	v_div_fixup_f32 v147, v153, v147, 1.0
	v_mul_f32_e32 v147, v147, v146
	s_nop 2
	v_fma_f32 v114, v143, v114, v130
	v_mul_f32_e32 v114, v145, v114
	v_mul_f32_e32 v114, v118, v114
	v_and_b32_e32 v118, 0xffff0000, v140
	v_mul_f32_e32 v118, 0xbfb8aa3b, v118
	v_exp_f32_e32 v118, v118
	v_fma_f32 v115, v143, v115, v131
	v_mul_f32_e32 v115, v145, v115
	v_fma_f32 v116, v143, v116, v132
	v_add_f32_e32 v118, 1.0, v118
	v_div_scale_f32 v119, s[56:57], v118, v118, 1.0
	v_rcp_f32_e32 v120, v119
	v_mul_f32_e32 v116, v145, v116
	v_fmac_f32_e32 v133, v143, v117
	v_mul_f32_e32 v117, v145, v133
	v_fma_f32 v121, -v119, v120, 1.0
	v_fmac_f32_e32 v120, v121, v120
	v_div_scale_f32 v121, vcc, 1.0, v118, 1.0
	v_mul_f32_e32 v122, v121, v120
	v_fma_f32 v123, -v119, v122, v121
	v_fmac_f32_e32 v122, v123, v120
	v_fma_f32 v119, -v119, v122, v121
	v_div_fmas_f32 v119, v119, v120, v122
	v_div_fixup_f32 v118, v119, v118, 1.0
	v_mul_f32_e32 v115, v118, v115
	v_lshlrev_b32_e32 v118, 16, v141
	v_mul_f32_e32 v118, 0xbfb8aa3b, v118
	v_exp_f32_e32 v118, v118
	v_add_u32_e32 v144, 0x8000, v144
	v_add_u32_e32 v142, 0x8000, v142
	v_add_u32_e32 v115, 0x8000, v115
	v_add_f32_e32 v118, 1.0, v118
	v_div_scale_f32 v119, s[56:57], v118, v118, 1.0
	v_rcp_f32_e32 v120, v119
	v_add_u32_e32 v114, 0x8000, v114
	v_perm_b32 v146, v144, v142, s33
	v_add_u32_e32 v142, 0x8000, v147
	v_fma_f32 v121, -v119, v120, 1.0
	v_fmac_f32_e32 v120, v121, v120
	v_div_scale_f32 v121, vcc, 1.0, v118, 1.0
	v_mul_f32_e32 v122, v121, v120
	v_fma_f32 v123, -v119, v122, v121
	v_fmac_f32_e32 v122, v123, v120
	v_fma_f32 v119, -v119, v122, v121
	v_div_fmas_f32 v119, v119, v120, v122
	v_div_fixup_f32 v118, v119, v118, 1.0
	v_mul_f32_e32 v116, v118, v116
	v_and_b32_e32 v118, 0xffff0000, v141
	v_mul_f32_e32 v118, 0xbfb8aa3b, v118
	v_exp_f32_e32 v118, v118
	v_add_u32_e32 v144, 0x8000, v152
	v_perm_b32 v114, v115, v114, s33
	v_add_u32_e32 v116, 0x8000, v116
	v_add_f32_e32 v118, 1.0, v118
	v_div_scale_f32 v119, s[56:57], v118, v118, 1.0
	v_rcp_f32_e32 v120, v119
	v_perm_b32 v147, v142, v144, s33
	v_lshl_add_u64 v[152:153], v[156:157], 0, v[186:187]
	s_mov_b32 s56, 0xf2000
	v_fma_f32 v121, -v119, v120, 1.0
	v_fmac_f32_e32 v120, v121, v120
	v_div_scale_f32 v121, vcc, 1.0, v118, 1.0
	v_mul_f32_e32 v122, v121, v120
	v_fma_f32 v123, -v119, v122, v121
	v_fmac_f32_e32 v122, v123, v120
	v_fma_f32 v119, -v119, v122, v121
	v_div_fmas_f32 v119, v119, v120, v122
	v_div_fixup_f32 v118, v119, v118, 1.0
	v_mul_f32_e32 v117, v118, v117
	v_add_u32_e32 v115, 0x8000, v117
	v_perm_b32 v115, v115, v116, s33
	v_lshl_add_u64 v[116:117], v[156:157], 0, v[184:185]
	global_store_dwordx2 v[152:153], v[146:147], off
	global_store_dwordx2 v[116:117], v[114:115], off
	v_add_co_u32_e32 v114, vcc, s56, v138
	v_add_u32_e32 v118, 64, v188
	s_nop 0
	v_addc_co_u32_e32 v115, vcc, 0, v139, vcc
	v_ashrrev_i32_e32 v119, 31, v118
	global_load_dwordx2 v[142:143], v[114:115], off
	global_load_dwordx2 v[140:141], v[114:115], off offset:32
	ds_read_b128 v[122:125], v181 offset:13056
	ds_read_b128 v[126:129], v181 offset:13120
	ds_read_b128 v[130:133], v181 offset:13184
	ds_read_b128 v[134:137], v181 offset:13248
	ds_read_b128 v[114:117], v0 offset:17152
	ds_read_b128 v[152:155], v0 offset:17216
	ds_read_b128 v[164:167], v0 offset:17280
	ds_read2_b32 v[144:145], v158 offset0:192 offset1:208
	ds_read2_b32 v[146:147], v159 offset0:64 offset1:80
	v_lshlrev_b64 v[118:119], 12, v[118:119]
	v_lshl_add_u64 v[156:157], s[22:23], 0, v[118:119]
	s_waitcnt lgkmcnt(4)
; #define LAS __attribute__((address_space(3)))
; __device__ __forceinline__ unsigned pk2(float lo, float hi) { return __builtin_amdgcn_perm(__builtin_bit_cast(unsigned, hi) + 0x8000u, __builtin_bit_cast(unsigned, lo) + 0x8000u, 0x07060302u); }
; __device__ __forceinline__ float sigmoidf_(float x) { return 1.0f / (1.0f + __expf(-x)); }
; __device__ __forceinline__ void ph_mlstm_out(const Frame& F) {
;     ...
;         for (int tt = 0; tt < 8; ++tt) {
;             const int t = 16 * tt + l15;
;             const v2u ogc[2] = {ogn0, ogn1};
;             if (tt < 7) { ogn0 = *(const v2u*)(ogp + (size_t)(16 * (tt + 1)) * 6144); ogn1 = *(const v2u*)(ogp + (size_t)(16 * (tt + 1)) * 6144 + 16); }
;             bf16x8 qf[4];
; #pragma unroll
;             for (int st = 0; st < 4; ++st) qf[st] = *(const LAS bf16x8*)(lds + MLO_Q_OFF + t * ML_ROW + 16 * g + 64 * st);
;             const int nst = (tt >> 1) + 1;
;             bf16x8 pf[4];
; #pragma unroll
;             for (int st = 0; st < 4; ++st) if (st < nst) pf[st] = *(const LAS bf16x8*)(lds + ML_K_OFF + t * ML_ROW + 16 * g + 64 * st);
;             const float ai = ais[t], rd = rds[t];
; #pragma unroll
;             for (int vt = 0; vt < 2; ++vt) {
;                 f32x4 ci = (f32x4){0.f, 0.f, 0.f, 0.f}, cx = (f32x4){0.f, 0.f, 0.f, 0.f};
; #pragma unroll
;                 for (int st = 0; st < 4; ++st) ci = __builtin_amdgcn_mfma_f32_16x16x32_bf16(cf[vt][st], qf[st], ci, 0, 0, 0);
;                 const LAS unsigned char* vr = lds + ML_V_OFF + (16 * (2 * wave + vt) + l15) * ML_ROW + 16 * g;
; #pragma unroll
;                 for (int st = 0; st < 4; ++st) if (st < nst) cx = __builtin_amdgcn_mfma_f32_16x16x32_bf16(*(const LAS bf16x8*)(vr + 64 * st), pf[st], cx, 0, 0, 0);
;                 const int vcol = h * 256 + 16 * (2 * wave + vt) + 4 * g;
;                 const v2u ogw = ogc[vt];
;                 const float y0 = (ai * ci[0] + cx[0]) * rd * sigmoidf_(bflo(ogw.x)), y1 = (ai * ci[1] + cx[1]) * rd * sigmoidf_(bfhi(ogw.x));
;                 const float y2 = (ai * ci[2] + cx[2]) * rd * sigmoidf_(bflo(ogw.y)), y3 = (ai * ci[3] + cx[3]) * rd * sigmoidf_(bfhi(ogw.y));
;                 v2u w; w.x = pk2(y0, y1); w.y = pk2(y2, y3);
;                 *(v2u*)(YB + (size_t)(t0 + t) * 2048 + vcol) = w;
;             }
	v_mfma_f32_16x16x32_bf16 v[118:121], v[102:105], v[114:117], 0
	s_waitcnt vmcnt(5)
	v_lshlrev_b32_e32 v161, 16, v150
	v_mul_f32_e32 v161, 0xbfb8aa3b, v161
	v_exp_f32_e32 v161, v161
	v_mfma_f32_16x16x32_bf16 v[194:197], v[94:97], v[122:125], 0
	v_and_b32_e32 v150, 0xffff0000, v150
	v_mul_f32_e32 v150, 0xbfb8aa3b, v150
	v_add_f32_e32 v161, 1.0, v161
	s_waitcnt lgkmcnt(3)
	v_mfma_f32_16x16x32_bf16 v[190:193], v[106:109], v[152:155], v[118:121]
	v_div_scale_f32 v183, s[56:57], v161, v161, 1.0
	v_rcp_f32_e32 v189, v183
	s_nop 0
	ds_read_b128 v[118:121], v247 offset:39040
	v_mfma_f32_16x16x32_bf16 v[194:197], v[82:85], v[126:129], v[194:197]
	v_exp_f32_e32 v150, v150
	s_nop 0
	v_add_f32_e32 v150, 1.0, v150
	v_mfma_f32_16x16x32_bf16 v[194:197], v[86:89], v[130:133], v[194:197]
	s_waitcnt lgkmcnt(0)
	v_mfma_f32_16x16x32_bf16 v[190:193], v[118:121], v[164:167], v[190:193]
	v_mfma_f32_16x16x32_bf16 v[194:197], v[90:93], v[134:137], v[194:197]
	v_mfma_f32_16x16x32_bf16 v[122:125], v[78:81], v[122:125], 0
	v_mfma_f32_16x16x32_bf16 v[122:125], v[66:69], v[126:129], v[122:125]
	s_nop 5
	v_fma_f32 v160, v144, v194, v190
	v_fma_f32 v190, -v183, v189, 1.0
	v_fmac_f32_e32 v189, v190, v189
	v_div_scale_f32 v190, vcc, 1.0, v161, 1.0
	v_mul_f32_e32 v194, v190, v189
	v_fma_f32 v198, -v183, v194, v190
	v_fmac_f32_e32 v194, v198, v189
	v_fma_f32 v183, -v183, v194, v190
	v_div_fmas_f32 v183, v183, v189, v194
	v_div_fixup_f32 v161, v183, v161, 1.0
	v_div_scale_f32 v183, s[56:57], v150, v150, 1.0
	v_rcp_f32_e32 v189, v183
	v_mul_f32_e32 v160, v146, v160
	v_mul_f32_e32 v160, v161, v160
	v_fma_f32 v161, v144, v195, v191
	v_fma_f32 v190, -v183, v189, 1.0
	v_fmac_f32_e32 v189, v190, v189
	v_div_scale_f32 v190, vcc, 1.0, v150, 1.0
	v_mul_f32_e32 v191, v190, v189
	v_fma_f32 v194, -v183, v191, v190
	v_fmac_f32_e32 v191, v194, v189
	v_fma_f32 v183, -v183, v191, v190
	v_div_fmas_f32 v183, v183, v189, v191
	v_div_fixup_f32 v150, v183, v150, 1.0
	v_lshlrev_b32_e32 v183, 16, v151
	v_mul_f32_e32 v183, 0xbfb8aa3b, v183
	v_exp_f32_e32 v183, v183
	v_and_b32_e32 v151, 0xffff0000, v151
	v_mul_f32_e32 v161, v146, v161
	v_mul_f32_e32 v151, 0xbfb8aa3b, v151
	v_add_f32_e32 v183, 1.0, v183
	v_div_scale_f32 v189, s[56:57], v183, v183, 1.0
	v_rcp_f32_e32 v190, v189
	v_mul_f32_e32 v150, v150, v161
	v_fma_f32 v161, v144, v196, v192
	v_exp_f32_e32 v151, v151
	v_fma_f32 v191, -v189, v190, 1.0
	v_fmac_f32_e32 v190, v191, v190
	v_div_scale_f32 v191, vcc, 1.0, v183, 1.0
	v_mul_f32_e32 v192, v191, v190
	v_fma_f32 v194, -v189, v192, v191
	v_fmac_f32_e32 v192, v194, v190
	v_fma_f32 v189, -v189, v192, v191
	v_div_fmas_f32 v189, v189, v190, v192
	v_add_f32_e32 v151, 1.0, v151
	v_div_fixup_f32 v183, v189, v183, 1.0
	v_div_scale_f32 v189, s[56:57], v151, v151, 1.0
	v_rcp_f32_e32 v190, v189
	v_mul_f32_e32 v161, v146, v161
	v_fmac_f32_e32 v193, v144, v197
	v_mul_f32_e32 v161, v183, v161
	v_fma_f32 v191, -v189, v190, 1.0
	v_fmac_f32_e32 v190, v191, v190
	v_div_scale_f32 v191, vcc, 1.0, v151, 1.0
	v_mul_f32_e32 v192, v191, v190
	v_mul_f32_e32 v183, v146, v193
	v_fma_f32 v193, -v189, v192, v191
	v_fmac_f32_e32 v192, v193, v190
	v_fma_f32 v189, -v189, v192, v191
	v_div_fmas_f32 v189, v189, v190, v192
	s_waitcnt vmcnt(4)
	v_lshlrev_b32_e32 v126, 16, v148
	v_div_fixup_f32 v151, v189, v151, 1.0
	v_mfma_f32_16x16x32_bf16 v[114:117], v[98:101], v[114:117], 0
	v_mul_f32_e32 v126, 0xbfb8aa3b, v126
	v_mul_f32_e32 v151, v151, v183
	v_add_u32_e32 v150, 0x8000, v150
	v_add_u32_e32 v160, 0x8000, v160
	v_exp_f32_e32 v126, v126
	v_perm_b32 v150, v150, v160, s33
	v_add_u32_e32 v151, 0x8000, v151
	v_add_u32_e32 v160, 0x8000, v161
	v_perm_b32 v151, v151, v160, s33
	v_lshl_add_u64 v[160:161], v[156:157], 0, v[186:187]
	global_store_dwordx2 v[160:161], v[150:151], off
	v_mfma_f32_16x16x32_bf16 v[150:153], v[110:113], v[152:155], v[114:117]
	v_add_f32_e32 v126, 1.0, v126
	v_div_scale_f32 v127, s[56:57], v126, v126, 1.0
	s_nop 0
	ds_read_b128 v[114:117], v248 offset:39040
	v_rcp_f32_e32 v128, v127
	v_mfma_f32_16x16x32_bf16 v[122:125], v[70:73], v[130:133], v[122:125]
	v_fma_f32 v129, -v127, v128, 1.0
	v_fmac_f32_e32 v128, v129, v128
	v_div_scale_f32 v129, vcc, 1.0, v126, 1.0
	s_waitcnt lgkmcnt(0)
	v_mfma_f32_16x16x32_bf16 v[150:153], v[114:117], v[164:167], v[150:153]
	v_mul_f32_e32 v130, v129, v128
	v_fma_f32 v131, -v127, v130, v129
	v_fmac_f32_e32 v130, v131, v128
	v_mfma_f32_16x16x32_bf16 v[122:125], v[74:77], v[134:137], v[122:125]
	v_fma_f32 v127, -v127, v130, v129
	v_div_fmas_f32 v127, v127, v128, v130
	v_div_fixup_f32 v126, v127, v126, 1.0
	s_nop 4
	v_fma_f32 v122, v144, v122, v150
	v_mul_f32_e32 v122, v146, v122
	v_mul_f32_e32 v122, v126, v122
	v_and_b32_e32 v126, 0xffff0000, v148
	v_mul_f32_e32 v126, 0xbfb8aa3b, v126
	v_exp_f32_e32 v126, v126
	v_fma_f32 v123, v144, v123, v151
	v_mul_f32_e32 v123, v146, v123
	v_fma_f32 v124, v144, v124, v152
	v_add_f32_e32 v126, 1.0, v126
	v_div_scale_f32 v127, s[56:57], v126, v126, 1.0
	v_rcp_f32_e32 v128, v127
	v_mul_f32_e32 v124, v146, v124
	v_fmac_f32_e32 v153, v144, v125
	v_mul_f32_e32 v125, v146, v153
	v_fma_f32 v129, -v127, v128, 1.0
	v_fmac_f32_e32 v128, v129, v128
	v_div_scale_f32 v129, vcc, 1.0, v126, 1.0
	v_mul_f32_e32 v130, v129, v128
	v_fma_f32 v131, -v127, v130, v129
	v_fmac_f32_e32 v130, v131, v128
	v_fma_f32 v127, -v127, v130, v129
	v_div_fmas_f32 v127, v127, v128, v130
	v_div_fixup_f32 v126, v127, v126, 1.0
	v_mul_f32_e32 v123, v126, v123
	v_lshlrev_b32_e32 v126, 16, v149
	v_mul_f32_e32 v126, 0xbfb8aa3b, v126
	v_exp_f32_e32 v126, v126
	v_add_u32_e32 v123, 0x8000, v123
	v_add_u32_e32 v122, 0x8000, v122
	v_perm_b32 v122, v123, v122, s33
	v_add_f32_e32 v126, 1.0, v126
	v_div_scale_f32 v127, s[56:57], v126, v126, 1.0
	v_rcp_f32_e32 v128, v127
	s_waitcnt vmcnt(2)
; #define LAS __attribute__((address_space(3)))
; __device__ __forceinline__ unsigned pk2(float lo, float hi) { return __builtin_amdgcn_perm(__builtin_bit_cast(unsigned, hi) + 0x8000u, __builtin_bit_cast(unsigned, lo) + 0x8000u, 0x07060302u); }
; __device__ __forceinline__ float sigmoidf_(float x) { return 1.0f / (1.0f + __expf(-x)); }
; __device__ __forceinline__ void ph_mlstm_out(const Frame& F) {
;     ...
;         for (int tt = 0; tt < 8; ++tt) {
;             const int t = 16 * tt + l15;
;             const v2u ogc[2] = {ogn0, ogn1};
;             if (tt < 7) { ogn0 = *(const v2u*)(ogp + (size_t)(16 * (tt + 1)) * 6144); ogn1 = *(const v2u*)(ogp + (size_t)(16 * (tt + 1)) * 6144 + 16); }
;             bf16x8 qf[4];
; #pragma unroll
;             for (int st = 0; st < 4; ++st) qf[st] = *(const LAS bf16x8*)(lds + MLO_Q_OFF + t * ML_ROW + 16 * g + 64 * st);
;             const int nst = (tt >> 1) + 1;
;             bf16x8 pf[4];
; #pragma unroll
;             for (int st = 0; st < 4; ++st) if (st < nst) pf[st] = *(const LAS bf16x8*)(lds + ML_K_OFF + t * ML_ROW + 16 * g + 64 * st);
;             const float ai = ais[t], rd = rds[t];
; #pragma unroll
;             for (int vt = 0; vt < 2; ++vt) {
;                 f32x4 ci = (f32x4){0.f, 0.f, 0.f, 0.f}, cx = (f32x4){0.f, 0.f, 0.f, 0.f};
; #pragma unroll
;                 for (int st = 0; st < 4; ++st) ci = __builtin_amdgcn_mfma_f32_16x16x32_bf16(cf[vt][st], qf[st], ci, 0, 0, 0);
;                 const LAS unsigned char* vr = lds + ML_V_OFF + (16 * (2 * wave + vt) + l15) * ML_ROW + 16 * g;
; #pragma unroll
;                 for (int st = 0; st < 4; ++st) if (st < nst) cx = __builtin_amdgcn_mfma_f32_16x16x32_bf16(*(const LAS bf16x8*)(vr + 64 * st), pf[st], cx, 0, 0, 0);
;                 const int vcol = h * 256 + 16 * (2 * wave + vt) + 4 * g;
;                 const v2u ogw = ogc[vt];
;                 const float y0 = (ai * ci[0] + cx[0]) * rd * sigmoidf_(bflo(ogw.x)), y1 = (ai * ci[1] + cx[1]) * rd * sigmoidf_(bfhi(ogw.x));
;                 const float y2 = (ai * ci[2] + cx[2]) * rd * sigmoidf_(bflo(ogw.y)), y3 = (ai * ci[3] + cx[3]) * rd * sigmoidf_(bfhi(ogw.y));
;                 v2u w; w.x = pk2(y0, y1); w.y = pk2(y2, y3);
;                 *(v2u*)(YB + (size_t)(t0 + t) * 2048 + vcol) = w;
;             }
	v_lshlrev_b32_e32 v146, 16, v142
	v_mul_f32_e32 v146, 0xbfb8aa3b, v146
	v_exp_f32_e32 v146, v146
	v_fma_f32 v129, -v127, v128, 1.0
	v_fmac_f32_e32 v128, v129, v128
	v_div_scale_f32 v129, vcc, 1.0, v126, 1.0
	v_mul_f32_e32 v130, v129, v128
	v_fma_f32 v131, -v127, v130, v129
	v_fmac_f32_e32 v130, v131, v128
	v_fma_f32 v127, -v127, v130, v129
	v_div_fmas_f32 v127, v127, v128, v130
	v_div_fixup_f32 v126, v127, v126, 1.0
	v_mul_f32_e32 v124, v126, v124
	v_and_b32_e32 v126, 0xffff0000, v149
	v_mul_f32_e32 v126, 0xbfb8aa3b, v126
	v_exp_f32_e32 v126, v126
	v_add_u32_e32 v124, 0x8000, v124
	v_add_f32_e32 v146, 1.0, v146
	v_and_b32_e32 v142, 0xffff0000, v142
	v_add_f32_e32 v126, 1.0, v126
	v_div_scale_f32 v127, s[56:57], v126, v126, 1.0
	v_rcp_f32_e32 v128, v127
	s_mov_b32 s56, 0x122000
	v_mul_f32_e32 v142, 0xbfb8aa3b, v142
	v_exp_f32_e32 v142, v142
	v_fma_f32 v129, -v127, v128, 1.0
	v_fmac_f32_e32 v128, v129, v128
	v_div_scale_f32 v129, vcc, 1.0, v126, 1.0
	v_mul_f32_e32 v130, v129, v128
	v_fma_f32 v131, -v127, v130, v129
	v_fmac_f32_e32 v130, v131, v128
	v_fma_f32 v127, -v127, v130, v129
	v_div_fmas_f32 v127, v127, v128, v130
	v_div_fixup_f32 v126, v127, v126, 1.0
	v_mul_f32_e32 v125, v126, v125
	v_add_u32_e32 v123, 0x8000, v125
	v_perm_b32 v123, v123, v124, s33
	v_lshl_add_u64 v[124:125], v[156:157], 0, v[184:185]
	global_store_dwordx2 v[124:125], v[122:123], off
	v_add_co_u32_e32 v122, vcc, s56, v138
	v_div_scale_f32 v160, s[56:57], v146, v146, 1.0
	s_nop 0
	v_addc_co_u32_e32 v123, vcc, 0, v139, vcc
	global_load_dwordx2 v[202:203], v[122:123], off
	global_load_dwordx2 v[198:199], v[122:123], off offset:32
	ds_read_b128 v[122:125], v181 offset:17408
	ds_read_b128 v[126:129], v181 offset:17472
	ds_read_b128 v[130:133], v181 offset:17536
	ds_read_b128 v[134:137], v181 offset:17600
	ds_read_b128 v[148:151], v0 offset:21504
	ds_read_b128 v[152:155], v0 offset:21568
	ds_read_b128 v[164:167], v0 offset:21632
	s_waitcnt lgkmcnt(6)
	v_mfma_f32_16x16x32_bf16 v[194:197], v[94:97], v[122:125], 0
	v_rcp_f32_e32 v161, v160
	v_add_f32_e32 v142, 1.0, v142
	v_add_u32_e32 v156, 0x50, v188
	s_waitcnt lgkmcnt(2)
	v_mfma_f32_16x16x32_bf16 v[190:193], v[102:105], v[148:151], 0
	v_fma_f32 v183, -v160, v161, 1.0
	v_fmac_f32_e32 v161, v183, v161
	v_div_scale_f32 v183, vcc, 1.0, v146, 1.0
	v_mfma_f32_16x16x32_bf16 v[194:197], v[82:85], v[126:129], v[194:197]
	v_mul_f32_e32 v189, v183, v161
	v_ashrrev_i32_e32 v157, 31, v156
	v_lshlrev_b64 v[156:157], 12, v[156:157]
	s_waitcnt lgkmcnt(1)
	v_mfma_f32_16x16x32_bf16 v[190:193], v[106:109], v[152:155], v[190:193]
	v_lshl_add_u64 v[156:157], s[22:23], 0, v[156:157]
	v_mfma_f32_16x16x32_bf16 v[194:197], v[86:89], v[130:133], v[194:197]
	s_waitcnt lgkmcnt(0)
	v_mfma_f32_16x16x32_bf16 v[190:193], v[118:121], v[164:167], v[190:193]
	v_mfma_f32_16x16x32_bf16 v[194:197], v[90:93], v[134:137], v[194:197]
	v_mfma_f32_16x16x32_bf16 v[122:125], v[78:81], v[122:125], 0
	v_mfma_f32_16x16x32_bf16 v[122:125], v[66:69], v[126:129], v[122:125]
	s_nop 5
	v_fma_f32 v144, v145, v194, v190
	v_fma_f32 v190, -v160, v189, v183
	v_fmac_f32_e32 v189, v190, v161
	v_fma_f32 v160, -v160, v189, v183
	v_div_fmas_f32 v160, v160, v161, v189
	v_div_fixup_f32 v146, v160, v146, 1.0
	v_div_scale_f32 v160, s[56:57], v142, v142, 1.0
	v_rcp_f32_e32 v161, v160
	v_mul_f32_e32 v144, v147, v144
	v_mul_f32_e32 v144, v146, v144
	v_fma_f32 v146, v145, v195, v191
	v_fma_f32 v183, -v160, v161, 1.0
	v_fmac_f32_e32 v161, v183, v161
	v_div_scale_f32 v183, vcc, 1.0, v142, 1.0
	v_mul_f32_e32 v189, v183, v161
	v_fma_f32 v190, -v160, v189, v183
	v_fmac_f32_e32 v189, v190, v161
	v_fma_f32 v160, -v160, v189, v183
	v_div_fmas_f32 v160, v160, v161, v189
	v_div_fixup_f32 v142, v160, v142, 1.0
	v_lshlrev_b32_e32 v160, 16, v143
	v_mul_f32_e32 v160, 0xbfb8aa3b, v160
	v_exp_f32_e32 v160, v160
	v_and_b32_e32 v143, 0xffff0000, v143
	v_mul_f32_e32 v143, 0xbfb8aa3b, v143
	v_exp_f32_e32 v143, v143
	v_add_f32_e32 v160, 1.0, v160
	v_div_scale_f32 v161, s[56:57], v160, v160, 1.0
	v_rcp_f32_e32 v183, v161
	s_waitcnt vmcnt(4)
	v_lshlrev_b32_e32 v126, 16, v140
	v_add_f32_e32 v143, 1.0, v143
	v_mul_f32_e32 v126, 0xbfb8aa3b, v126
	v_fma_f32 v189, -v161, v183, 1.0
	v_fmac_f32_e32 v183, v189, v183
	v_div_scale_f32 v189, vcc, 1.0, v160, 1.0
	v_mul_f32_e32 v190, v189, v183
	v_fma_f32 v191, -v161, v190, v189
	v_fmac_f32_e32 v190, v191, v183
	v_fma_f32 v161, -v161, v190, v189
	v_div_fmas_f32 v161, v161, v183, v190
	v_div_fixup_f32 v160, v161, v160, 1.0
	v_div_scale_f32 v161, s[56:57], v143, v143, 1.0
	v_exp_f32_e32 v126, v126
	v_rcp_f32_e32 v183, v161
	v_mfma_f32_16x16x32_bf16 v[148:151], v[98:101], v[148:151], 0
	v_mul_f32_e32 v146, v147, v146
	v_add_f32_e32 v126, 1.0, v126
	v_fma_f32 v189, -v161, v183, 1.0
	v_div_scale_f32 v127, s[56:57], v126, v126, 1.0
	v_fmac_f32_e32 v183, v189, v183
	v_div_scale_f32 v189, vcc, 1.0, v143, 1.0
	v_rcp_f32_e32 v128, v127
	v_mul_f32_e32 v190, v189, v183
	v_fma_f32 v191, -v161, v190, v189
	v_mfma_f32_16x16x32_bf16 v[148:151], v[110:113], v[152:155], v[148:151]
	v_fmac_f32_e32 v190, v191, v183
	v_fma_f32 v161, -v161, v190, v189
	v_fma_f32 v129, -v127, v128, 1.0
	v_mfma_f32_16x16x32_bf16 v[122:125], v[70:73], v[130:133], v[122:125]
	v_div_fmas_f32 v161, v161, v183, v190
	v_fmac_f32_e32 v128, v129, v128
	v_div_scale_f32 v129, vcc, 1.0, v126, 1.0
	v_mfma_f32_16x16x32_bf16 v[148:151], v[114:117], v[164:167], v[148:151]
	v_mul_f32_e32 v130, v129, v128
	v_fma_f32 v131, -v127, v130, v129
	v_fmac_f32_e32 v130, v131, v128
	v_mfma_f32_16x16x32_bf16 v[122:125], v[74:77], v[134:137], v[122:125]
	v_fma_f32 v127, -v127, v130, v129
	v_div_fmas_f32 v127, v127, v128, v130
; #define LAS __attribute__((address_space(3)))
; __device__ __forceinline__ unsigned pk2(float lo, float hi) { return __builtin_amdgcn_perm(__builtin_bit_cast(unsigned, hi) + 0x8000u, __builtin_bit_cast(unsigned, lo) + 0x8000u, 0x07060302u); }
; __device__ __forceinline__ float sigmoidf_(float x) { return 1.0f / (1.0f + __expf(-x)); }
; __device__ __forceinline__ void ph_mlstm_out(const Frame& F) {
;     ...
;         for (int tt = 0; tt < 8; ++tt) {
;             const int t = 16 * tt + l15;
;             const v2u ogc[2] = {ogn0, ogn1};
;             if (tt < 7) { ogn0 = *(const v2u*)(ogp + (size_t)(16 * (tt + 1)) * 6144); ogn1 = *(const v2u*)(ogp + (size_t)(16 * (tt + 1)) * 6144 + 16); }
;             bf16x8 qf[4];
; #pragma unroll
;             for (int st = 0; st < 4; ++st) qf[st] = *(const LAS bf16x8*)(lds + MLO_Q_OFF + t * ML_ROW + 16 * g + 64 * st);
;             const int nst = (tt >> 1) + 1;
;             bf16x8 pf[4];
; #pragma unroll
;             for (int st = 0; st < 4; ++st) if (st < nst) pf[st] = *(const LAS bf16x8*)(lds + ML_K_OFF + t * ML_ROW + 16 * g + 64 * st);
;             const float ai = ais[t], rd = rds[t];
; #pragma unroll
;             for (int vt = 0; vt < 2; ++vt) {
;                 f32x4 ci = (f32x4){0.f, 0.f, 0.f, 0.f}, cx = (f32x4){0.f, 0.f, 0.f, 0.f};
; #pragma unroll
;                 for (int st = 0; st < 4; ++st) ci = __builtin_amdgcn_mfma_f32_16x16x32_bf16(cf[vt][st], qf[st], ci, 0, 0, 0);
;                 const LAS unsigned char* vr = lds + ML_V_OFF + (16 * (2 * wave + vt) + l15) * ML_ROW + 16 * g;
; #pragma unroll
;                 for (int st = 0; st < 4; ++st) if (st < nst) cx = __builtin_amdgcn_mfma_f32_16x16x32_bf16(*(const LAS bf16x8*)(vr + 64 * st), pf[st], cx, 0, 0, 0);
;                 const int vcol = h * 256 + 16 * (2 * wave + vt) + 4 * g;
;                 const v2u ogw = ogc[vt];
;                 const float y0 = (ai * ci[0] + cx[0]) * rd * sigmoidf_(bflo(ogw.x)), y1 = (ai * ci[1] + cx[1]) * rd * sigmoidf_(bfhi(ogw.x));
;                 const float y2 = (ai * ci[2] + cx[2]) * rd * sigmoidf_(bflo(ogw.y)), y3 = (ai * ci[3] + cx[3]) * rd * sigmoidf_(bfhi(ogw.y));
;                 v2u w; w.x = pk2(y0, y1); w.y = pk2(y2, y3);
;                 *(v2u*)(YB + (size_t)(t0 + t) * 2048 + vcol) = w;
;             }
	v_div_fixup_f32 v126, v127, v126, 1.0
	v_mul_f32_e32 v142, v142, v146
	v_fma_f32 v146, v145, v196, v192
	s_nop 2
	v_fma_f32 v122, v145, v122, v148
	v_mul_f32_e32 v122, v147, v122
	v_mul_f32_e32 v122, v126, v122
	v_and_b32_e32 v126, 0xffff0000, v140
	v_mul_f32_e32 v126, 0xbfb8aa3b, v126
	v_exp_f32_e32 v126, v126
	v_fma_f32 v123, v145, v123, v149
	v_mul_f32_e32 v123, v147, v123
	v_fma_f32 v124, v145, v124, v150
	v_add_f32_e32 v126, 1.0, v126
	v_div_scale_f32 v127, s[56:57], v126, v126, 1.0
	v_rcp_f32_e32 v128, v127
	v_mul_f32_e32 v124, v147, v124
	v_mul_f32_e32 v146, v147, v146
	v_fmac_f32_e32 v193, v145, v197
	v_fma_f32 v129, -v127, v128, 1.0
	v_fmac_f32_e32 v128, v129, v128
	v_div_scale_f32 v129, vcc, 1.0, v126, 1.0
	v_mul_f32_e32 v130, v129, v128
	v_fma_f32 v131, -v127, v130, v129
	v_fmac_f32_e32 v130, v131, v128
	v_fma_f32 v127, -v127, v130, v129
	v_div_fmas_f32 v127, v127, v128, v130
	v_div_fixup_f32 v126, v127, v126, 1.0
	v_mul_f32_e32 v123, v126, v123
	v_lshlrev_b32_e32 v126, 16, v141
	v_mul_f32_e32 v126, 0xbfb8aa3b, v126
	v_exp_f32_e32 v126, v126
	v_fmac_f32_e32 v151, v145, v125
	v_mul_f32_e32 v146, v160, v146
	v_mul_f32_e32 v160, v147, v193
	v_add_f32_e32 v126, 1.0, v126
	v_div_scale_f32 v127, s[56:57], v126, v126, 1.0
	v_rcp_f32_e32 v128, v127
	v_div_fixup_f32 v143, v161, v143, 1.0
	v_mul_f32_e32 v125, v147, v151
	v_mul_f32_e32 v143, v143, v160
	v_fma_f32 v129, -v127, v128, 1.0
	v_fmac_f32_e32 v128, v129, v128
	v_div_scale_f32 v129, vcc, 1.0, v126, 1.0
	v_mul_f32_e32 v130, v129, v128
	v_fma_f32 v131, -v127, v130, v129
	v_fmac_f32_e32 v130, v131, v128
	v_fma_f32 v127, -v127, v130, v129
	v_div_fmas_f32 v127, v127, v128, v130
	v_div_fixup_f32 v126, v127, v126, 1.0
	v_mul_f32_e32 v124, v126, v124
	v_and_b32_e32 v126, 0xffff0000, v141
	v_mul_f32_e32 v126, 0xbfb8aa3b, v126
	v_exp_f32_e32 v126, v126
	v_add_u32_e32 v142, 0x8000, v142
	v_add_u32_e32 v144, 0x8000, v144
	v_add_u32_e32 v123, 0x8000, v123
	v_add_f32_e32 v126, 1.0, v126
	v_div_scale_f32 v127, s[56:57], v126, v126, 1.0
	v_rcp_f32_e32 v128, v127
	v_add_u32_e32 v122, 0x8000, v122
	v_perm_b32 v142, v142, v144, s33
	v_add_u32_e32 v143, 0x8000, v143
	v_fma_f32 v129, -v127, v128, 1.0
	v_fmac_f32_e32 v128, v129, v128
	v_div_scale_f32 v129, vcc, 1.0, v126, 1.0
	v_mul_f32_e32 v130, v129, v128
	v_fma_f32 v131, -v127, v130, v129
	v_fmac_f32_e32 v130, v131, v128
	v_fma_f32 v127, -v127, v130, v129
	v_div_fmas_f32 v127, v127, v128, v130
	v_div_fixup_f32 v126, v127, v126, 1.0
	v_mul_f32_e32 v125, v126, v125
	v_add_u32_e32 v144, 0x8000, v146
	v_perm_b32 v122, v123, v122, s33
	v_add_u32_e32 v123, 0x8000, v125
	v_add_u32_e32 v124, 0x8000, v124
	v_perm_b32 v143, v143, v144, s33
	v_lshl_add_u64 v[160:161], v[156:157], 0, v[186:187]
	v_perm_b32 v123, v123, v124, s33
	v_lshl_add_u64 v[124:125], v[156:157], 0, v[184:185]
	s_mov_b32 s56, 0x152000
	global_store_dwordx2 v[160:161], v[142:143], off
	global_store_dwordx2 v[124:125], v[122:123], off
	v_add_co_u32_e32 v122, vcc, s56, v138
	s_nop 1
	v_addc_co_u32_e32 v123, vcc, 0, v139, vcc
	global_load_dwordx2 v[196:197], v[122:123], off
	global_load_dwordx2 v[190:191], v[122:123], off offset:32
	v_add_u32_e32 v122, 0x60, v188
	v_ashrrev_i32_e32 v123, 31, v122
	v_lshlrev_b64 v[122:123], 12, v[122:123]
	ds_read_b128 v[130:133], v181 offset:21760
	ds_read_b128 v[134:137], v181 offset:21824
	ds_read_b128 v[138:141], v181 offset:21888
	ds_read_b128 v[142:145], v181 offset:21952
	ds_read_b128 v[126:129], v0 offset:25856
	ds_read_b128 v[150:153], v0 offset:25920
	ds_read_b128 v[154:157], v0 offset:25984
	ds_read_b128 v[146:149], v0 offset:26048
	ds_read2_b32 v[192:193], v158 offset0:224 offset1:240
	ds_read2_b32 v[194:195], v159 offset0:96 offset1:112
	v_lshl_add_u64 v[200:201], s[22:23], 0, v[122:123]
	s_waitcnt lgkmcnt(5)
	v_mfma_f32_16x16x32_bf16 v[122:125], v[102:105], v[126:129], 0
	s_waitcnt lgkmcnt(4)
	v_mfma_f32_16x16x32_bf16 v[122:125], v[106:109], v[150:153], v[122:125]
	v_mfma_f32_16x16x32_bf16 v[164:167], v[94:97], v[130:133], 0
	s_waitcnt lgkmcnt(3)
	v_mfma_f32_16x16x32_bf16 v[158:161], v[118:121], v[154:157], v[122:125]
	s_nop 4
	ds_read_b128 v[122:125], v247 offset:39104
	v_mfma_f32_16x16x32_bf16 v[164:167], v[82:85], v[134:137], v[164:167]
	v_mfma_f32_16x16x32_bf16 v[126:129], v[98:101], v[126:129], 0
	v_mfma_f32_16x16x32_bf16 v[164:167], v[86:89], v[138:141], v[164:167]
	v_mfma_f32_16x16x32_bf16 v[126:129], v[110:113], v[150:153], v[126:129]
	v_mfma_f32_16x16x32_bf16 v[164:167], v[90:93], v[142:145], v[164:167]
	v_mfma_f32_16x16x32_bf16 v[150:153], v[114:117], v[154:157], v[126:129]
	s_nop 5
	ds_read_b128 v[126:129], v248 offset:39104
	s_waitcnt lgkmcnt(1)
	v_mfma_f32_16x16x32_bf16 v[158:161], v[122:125], v[146:149], v[158:161]
	v_mfma_f32_16x16x32_bf16 v[130:133], v[78:81], v[130:133], 0
	v_mfma_f32_16x16x32_bf16 v[130:133], v[66:69], v[134:137], v[130:133]
	s_nop 5
	v_fma_f32 v158, v192, v164, v158
	s_waitcnt vmcnt(5)
	v_lshlrev_b32_e32 v164, 16, v202
	v_mul_f32_e32 v164, 0xbfb8aa3b, v164
	v_exp_f32_e32 v164, v164
	v_mul_f32_e32 v158, v194, v158
	v_fma_f32 v159, v192, v165, v159
	v_mul_f32_e32 v159, v194, v159
	v_add_f32_e32 v164, 1.0, v164
	v_div_scale_f32 v183, s[56:57], v164, v164, 1.0
	v_rcp_f32_e32 v189, v183
	v_fma_f32 v160, v192, v166, v160
	v_mul_f32_e32 v160, v194, v160
	s_waitcnt vmcnt(4)
; #define LAS __attribute__((address_space(3)))
; __device__ __forceinline__ unsigned pk2(float lo, float hi) { return __builtin_amdgcn_perm(__builtin_bit_cast(unsigned, hi) + 0x8000u, __builtin_bit_cast(unsigned, lo) + 0x8000u, 0x07060302u); }
; __device__ __forceinline__ float sigmoidf_(float x) { return 1.0f / (1.0f + __expf(-x)); }
; __device__ __forceinline__ void ph_mlstm_out(const Frame& F) {
;     ...
;         for (int tt = 0; tt < 8; ++tt) {
;             const int t = 16 * tt + l15;
;             const v2u ogc[2] = {ogn0, ogn1};
;             if (tt < 7) { ogn0 = *(const v2u*)(ogp + (size_t)(16 * (tt + 1)) * 6144); ogn1 = *(const v2u*)(ogp + (size_t)(16 * (tt + 1)) * 6144 + 16); }
;             bf16x8 qf[4];
; #pragma unroll
;             for (int st = 0; st < 4; ++st) qf[st] = *(const LAS bf16x8*)(lds + MLO_Q_OFF + t * ML_ROW + 16 * g + 64 * st);
;             const int nst = (tt >> 1) + 1;
;             bf16x8 pf[4];
; #pragma unroll
;             for (int st = 0; st < 4; ++st) if (st < nst) pf[st] = *(const LAS bf16x8*)(lds + ML_K_OFF + t * ML_ROW + 16 * g + 64 * st);
;             const float ai = ais[t], rd = rds[t];
; #pragma unroll
;             for (int vt = 0; vt < 2; ++vt) {
;                 f32x4 ci = (f32x4){0.f, 0.f, 0.f, 0.f}, cx = (f32x4){0.f, 0.f, 0.f, 0.f};
; #pragma unroll
;                 for (int st = 0; st < 4; ++st) ci = __builtin_amdgcn_mfma_f32_16x16x32_bf16(cf[vt][st], qf[st], ci, 0, 0, 0);
;                 const LAS unsigned char* vr = lds + ML_V_OFF + (16 * (2 * wave + vt) + l15) * ML_ROW + 16 * g;
; #pragma unroll
;                 for (int st = 0; st < 4; ++st) if (st < nst) cx = __builtin_amdgcn_mfma_f32_16x16x32_bf16(*(const LAS bf16x8*)(vr + 64 * st), pf[st], cx, 0, 0, 0);
;                 const int vcol = h * 256 + 16 * (2 * wave + vt) + 4 * g;
;                 const v2u ogw = ogc[vt];
;                 const float y0 = (ai * ci[0] + cx[0]) * rd * sigmoidf_(bflo(ogw.x)), y1 = (ai * ci[1] + cx[1]) * rd * sigmoidf_(bfhi(ogw.x));
;                 const float y2 = (ai * ci[2] + cx[2]) * rd * sigmoidf_(bflo(ogw.y)), y3 = (ai * ci[3] + cx[3]) * rd * sigmoidf_(bfhi(ogw.y));
;                 v2u w; w.x = pk2(y0, y1); w.y = pk2(y2, y3);
;                 *(v2u*)(YB + (size_t)(t0 + t) * 2048 + vcol) = w;
;             }
	v_lshlrev_b32_e32 v134, 16, v198
	v_fma_f32 v249, -v183, v189, 1.0
	v_fmac_f32_e32 v189, v249, v189
	v_div_scale_f32 v249, vcc, 1.0, v164, 1.0
	v_mul_f32_e32 v250, v249, v189
	v_fma_f32 v251, -v183, v250, v249
	v_fmac_f32_e32 v250, v251, v189
	v_fma_f32 v183, -v183, v250, v249
	v_div_fmas_f32 v183, v183, v189, v250
	v_div_fixup_f32 v164, v183, v164, 1.0
	v_mul_f32_e32 v158, v164, v158
	v_and_b32_e32 v164, 0xffff0000, v202
	v_mul_f32_e32 v164, 0xbfb8aa3b, v164
	v_exp_f32_e32 v164, v164
	v_mul_f32_e32 v134, 0xbfb8aa3b, v134
	v_exp_f32_e32 v134, v134
	v_fmac_f32_e32 v161, v192, v167
	v_add_f32_e32 v164, 1.0, v164
	v_div_scale_f32 v165, s[56:57], v164, v164, 1.0
	v_rcp_f32_e32 v183, v165
	v_add_f32_e32 v134, 1.0, v134
	v_div_scale_f32 v135, s[56:57], v134, v134, 1.0
	v_fma_f32 v189, -v165, v183, 1.0
	v_fmac_f32_e32 v183, v189, v183
	v_div_scale_f32 v189, vcc, 1.0, v164, 1.0
	v_mul_f32_e32 v202, v189, v183
	v_fma_f32 v249, -v165, v202, v189
	v_fmac_f32_e32 v202, v249, v183
	v_fma_f32 v165, -v165, v202, v189
	v_div_fmas_f32 v165, v165, v183, v202
	v_div_fixup_f32 v164, v165, v164, 1.0
	v_mul_f32_e32 v159, v164, v159
	v_lshlrev_b32_e32 v164, 16, v203
	v_mul_f32_e32 v164, 0xbfb8aa3b, v164
	v_exp_f32_e32 v164, v164
	v_rcp_f32_e32 v136, v135
	v_mfma_f32_16x16x32_bf16 v[130:133], v[70:73], v[138:141], v[130:133]
	v_mul_f32_e32 v161, v194, v161
	v_add_f32_e32 v164, 1.0, v164
	v_div_scale_f32 v165, s[56:57], v164, v164, 1.0
	v_rcp_f32_e32 v166, v165
	v_fma_f32 v137, -v135, v136, 1.0
	v_fmac_f32_e32 v136, v137, v136
	s_waitcnt lgkmcnt(0)
	v_mfma_f32_16x16x32_bf16 v[146:149], v[126:129], v[146:149], v[150:153]
	v_fma_f32 v183, -v165, v166, 1.0
	v_fmac_f32_e32 v166, v183, v166
	v_div_scale_f32 v183, vcc, 1.0, v164, 1.0
	v_mul_f32_e32 v189, v183, v166
	v_fma_f32 v202, -v165, v189, v183
	v_fmac_f32_e32 v189, v202, v166
	v_fma_f32 v165, -v165, v189, v183
	v_div_fmas_f32 v165, v165, v166, v189
	v_div_fixup_f32 v164, v165, v164, 1.0
	v_mul_f32_e32 v160, v164, v160
	v_and_b32_e32 v164, 0xffff0000, v203
	v_mul_f32_e32 v164, 0xbfb8aa3b, v164
	v_exp_f32_e32 v164, v164
	v_mfma_f32_16x16x32_bf16 v[130:133], v[74:77], v[142:145], v[130:133]
	v_add_u32_e32 v159, 0x8000, v159
	v_add_u32_e32 v158, 0x8000, v158
	v_add_f32_e32 v164, 1.0, v164
	v_div_scale_f32 v165, s[56:57], v164, v164, 1.0
	v_rcp_f32_e32 v166, v165
	s_nop 2
	v_fma_f32 v130, v192, v130, v146
	v_mul_f32_e32 v130, v194, v130
	v_fma_f32 v131, v192, v131, v147
	v_fma_f32 v167, -v165, v166, 1.0
	v_fmac_f32_e32 v166, v167, v166
	v_div_scale_f32 v167, vcc, 1.0, v164, 1.0
	v_mul_f32_e32 v183, v167, v166
	v_fma_f32 v189, -v165, v183, v167
	v_fmac_f32_e32 v183, v189, v166
	v_fma_f32 v165, -v165, v183, v167
	v_div_fmas_f32 v165, v165, v166, v183
	v_div_scale_f32 v137, vcc, 1.0, v134, 1.0
	v_mul_f32_e32 v138, v137, v136
	v_fma_f32 v139, -v135, v138, v137
	v_fmac_f32_e32 v138, v139, v136
	v_fma_f32 v135, -v135, v138, v137
	v_div_fmas_f32 v135, v135, v136, v138
	v_div_fixup_f32 v134, v135, v134, 1.0
	v_mul_f32_e32 v130, v134, v130
	v_and_b32_e32 v134, 0xffff0000, v198
	v_mul_f32_e32 v134, 0xbfb8aa3b, v134
	v_exp_f32_e32 v134, v134
	v_mul_f32_e32 v131, v194, v131
	v_fma_f32 v132, v192, v132, v148
	v_mul_f32_e32 v132, v194, v132
	v_add_f32_e32 v134, 1.0, v134
	v_div_scale_f32 v135, s[56:57], v134, v134, 1.0
	v_rcp_f32_e32 v136, v135
	v_fmac_f32_e32 v149, v192, v133
	v_div_fixup_f32 v164, v165, v164, 1.0
	v_mul_f32_e32 v133, v194, v149
	v_fma_f32 v137, -v135, v136, 1.0
	v_fmac_f32_e32 v136, v137, v136
	v_div_scale_f32 v137, vcc, 1.0, v134, 1.0
	v_mul_f32_e32 v138, v137, v136
	v_fma_f32 v139, -v135, v138, v137
	v_fmac_f32_e32 v138, v139, v136
	v_fma_f32 v135, -v135, v138, v137
	v_div_fmas_f32 v135, v135, v136, v138
	v_div_fixup_f32 v134, v135, v134, 1.0
	v_mul_f32_e32 v131, v134, v131
	v_lshlrev_b32_e32 v134, 16, v199
	v_mul_f32_e32 v134, 0xbfb8aa3b, v134
	v_exp_f32_e32 v134, v134
	v_mul_f32_e32 v161, v164, v161
	v_add_u32_e32 v131, 0x8000, v131
	v_add_u32_e32 v130, 0x8000, v130
	v_add_f32_e32 v134, 1.0, v134
	v_div_scale_f32 v135, s[56:57], v134, v134, 1.0
	v_rcp_f32_e32 v136, v135
	v_perm_b32 v158, v159, v158, s33
	v_add_u32_e32 v159, 0x8000, v161
	v_add_u32_e32 v160, 0x8000, v160
	v_fma_f32 v137, -v135, v136, 1.0
	v_fmac_f32_e32 v136, v137, v136
	v_div_scale_f32 v137, vcc, 1.0, v134, 1.0
	v_mul_f32_e32 v138, v137, v136
	v_fma_f32 v139, -v135, v138, v137
	v_fmac_f32_e32 v138, v139, v136
	v_fma_f32 v135, -v135, v138, v137
	v_div_fmas_f32 v135, v135, v136, v138
	v_div_fixup_f32 v134, v135, v134, 1.0
	v_mul_f32_e32 v132, v134, v132
	v_and_b32_e32 v134, 0xffff0000, v199
	v_mul_f32_e32 v134, 0xbfb8aa3b, v134
	v_exp_f32_e32 v134, v134
	v_perm_b32 v130, v131, v130, s33
	v_add_u32_e32 v132, 0x8000, v132
	v_perm_b32 v159, v159, v160, s33
	v_add_f32_e32 v134, 1.0, v134
	v_div_scale_f32 v135, s[56:57], v134, v134, 1.0
	v_rcp_f32_e32 v136, v135
	v_lshl_add_u64 v[160:161], v[200:201], 0, v[186:187]
	global_store_dwordx2 v[160:161], v[158:159], off
	v_add_u32_e32 v164, 0x70, v188
	v_fma_f32 v137, -v135, v136, 1.0
	v_fmac_f32_e32 v136, v137, v136
	v_div_scale_f32 v137, vcc, 1.0, v134, 1.0
	v_mul_f32_e32 v138, v137, v136
	v_fma_f32 v139, -v135, v138, v137
	v_fmac_f32_e32 v138, v139, v136
	v_fma_f32 v135, -v135, v138, v137
	v_div_fmas_f32 v135, v135, v136, v138
	v_div_fixup_f32 v134, v135, v134, 1.0
	v_mul_f32_e32 v133, v134, v133
	v_add_u32_e32 v131, 0x8000, v133
	v_perm_b32 v131, v131, v132, s33
	v_lshl_add_u64 v[132:133], v[200:201], 0, v[184:185]
	global_store_dwordx2 v[132:133], v[130:131], off
	ds_read_b128 v[142:145], v181 offset:26112
	ds_read_b128 v[130:133], v181 offset:26176
	ds_read_b128 v[134:137], v181 offset:26240
	ds_read_b128 v[138:141], v181 offset:26304
	ds_read_b128 v[146:149], v0 offset:30208
	ds_read_b128 v[158:161], v0 offset:30272
	ds_read_b128 v[154:157], v0 offset:30336
	ds_read_b128 v[150:153], v0 offset:30400
	s_waitcnt lgkmcnt(3)
; #define LAS __attribute__((address_space(3)))
; __device__ __forceinline__ unsigned pk2(float lo, float hi) { return __builtin_amdgcn_perm(__builtin_bit_cast(unsigned, hi) + 0x8000u, __builtin_bit_cast(unsigned, lo) + 0x8000u, 0x07060302u); }
; __device__ __forceinline__ float sigmoidf_(float x) { return 1.0f / (1.0f + __expf(-x)); }
; __device__ __forceinline__ void ph_mlstm_out(const Frame& F) {
;     ...
;         for (int tt = 0; tt < 8; ++tt) {
;             const int t = 16 * tt + l15;
;             const v2u ogc[2] = {ogn0, ogn1};
;             if (tt < 7) { ogn0 = *(const v2u*)(ogp + (size_t)(16 * (tt + 1)) * 6144); ogn1 = *(const v2u*)(ogp + (size_t)(16 * (tt + 1)) * 6144 + 16); }
;             bf16x8 qf[4];
; #pragma unroll
;             for (int st = 0; st < 4; ++st) qf[st] = *(const LAS bf16x8*)(lds + MLO_Q_OFF + t * ML_ROW + 16 * g + 64 * st);
;             const int nst = (tt >> 1) + 1;
;             bf16x8 pf[4];
; #pragma unroll
;             for (int st = 0; st < 4; ++st) if (st < nst) pf[st] = *(const LAS bf16x8*)(lds + ML_K_OFF + t * ML_ROW + 16 * g + 64 * st);
;             const float ai = ais[t], rd = rds[t];
; #pragma unroll
;             for (int vt = 0; vt < 2; ++vt) {
;                 f32x4 ci = (f32x4){0.f, 0.f, 0.f, 0.f}, cx = (f32x4){0.f, 0.f, 0.f, 0.f};
; #pragma unroll
;                 for (int st = 0; st < 4; ++st) ci = __builtin_amdgcn_mfma_f32_16x16x32_bf16(cf[vt][st], qf[st], ci, 0, 0, 0);
;                 const LAS unsigned char* vr = lds + ML_V_OFF + (16 * (2 * wave + vt) + l15) * ML_ROW + 16 * g;
; #pragma unroll
;                 for (int st = 0; st < 4; ++st) if (st < nst) cx = __builtin_amdgcn_mfma_f32_16x16x32_bf16(*(const LAS bf16x8*)(vr + 64 * st), pf[st], cx, 0, 0, 0);
;                 const int vcol = h * 256 + 16 * (2 * wave + vt) + 4 * g;
;                 const v2u ogw = ogc[vt];
;                 const float y0 = (ai * ci[0] + cx[0]) * rd * sigmoidf_(bflo(ogw.x)), y1 = (ai * ci[1] + cx[1]) * rd * sigmoidf_(bfhi(ogw.x));
;                 const float y2 = (ai * ci[2] + cx[2]) * rd * sigmoidf_(bflo(ogw.y)), y3 = (ai * ci[3] + cx[3]) * rd * sigmoidf_(bfhi(ogw.y));
;                 v2u w; w.x = pk2(y0, y1); w.y = pk2(y2, y3);
;                 *(v2u*)(YB + (size_t)(t0 + t) * 2048 + vcol) = w;
;             }
;         }
	v_mfma_f32_16x16x32_bf16 v[102:105], v[102:105], v[146:149], 0
	v_ashrrev_i32_e32 v165, 31, v164
	v_lshlrev_b64 v[164:165], 12, v[164:165]
	v_lshl_add_u64 v[188:189], s[22:23], 0, v[164:165]
	v_mfma_f32_16x16x32_bf16 v[94:97], v[94:97], v[142:145], 0
	s_waitcnt lgkmcnt(2)
	v_mfma_f32_16x16x32_bf16 v[102:105], v[106:109], v[158:161], v[102:105]
	v_mfma_f32_16x16x32_bf16 v[82:85], v[82:85], v[130:133], v[94:97]
	s_waitcnt lgkmcnt(1)
	v_mfma_f32_16x16x32_bf16 v[102:105], v[118:121], v[154:157], v[102:105]
	v_mfma_f32_16x16x32_bf16 v[82:85], v[86:89], v[134:137], v[82:85]
	s_waitcnt lgkmcnt(0)
	v_mfma_f32_16x16x32_bf16 v[102:105], v[122:125], v[150:153], v[102:105]
	v_mfma_f32_16x16x32_bf16 v[82:85], v[90:93], v[138:141], v[82:85]
	v_mfma_f32_16x16x32_bf16 v[78:81], v[78:81], v[142:145], 0
	v_mfma_f32_16x16x32_bf16 v[66:69], v[66:69], v[130:133], v[78:81]
	s_nop 5
	v_fma_f32 v0, v193, v82, v102
	s_waitcnt vmcnt(3)
	v_lshlrev_b32_e32 v82, 16, v196
	v_mul_f32_e32 v82, 0xbfb8aa3b, v82
	v_exp_f32_e32 v82, v82
	v_mul_f32_e32 v0, v195, v0
	v_fmac_f32_e32 v105, v193, v85
	v_and_b32_e32 v85, 0xffff0000, v197
	v_add_f32_e32 v82, 1.0, v82
	v_div_scale_f32 v86, s[56:57], v82, v82, 1.0
	v_rcp_f32_e32 v87, v86
	v_mul_f32_e32 v85, 0xbfb8aa3b, v85
	v_exp_f32_e32 v85, v85
	v_mfma_f32_16x16x32_bf16 v[66:69], v[70:73], v[134:137], v[66:69]
	v_fma_f32 v88, -v86, v87, 1.0
	v_fmac_f32_e32 v87, v88, v87
	v_div_scale_f32 v88, vcc, 1.0, v82, 1.0
	v_mul_f32_e32 v89, v88, v87
	v_fma_f32 v90, -v86, v89, v88
	v_fmac_f32_e32 v89, v90, v87
	v_fma_f32 v86, -v86, v89, v88
	v_div_fmas_f32 v86, v86, v87, v89
	v_div_fixup_f32 v82, v86, v82, 1.0
	v_mul_f32_e32 v0, v82, v0
	v_fma_f32 v82, v193, v83, v103
	v_and_b32_e32 v83, 0xffff0000, v196
	v_mul_f32_e32 v83, 0xbfb8aa3b, v83
	v_exp_f32_e32 v83, v83
	v_mul_f32_e32 v82, v195, v82
	v_add_f32_e32 v85, 1.0, v85
	v_add_u32_e32 v0, 0x8000, v0
	v_add_f32_e32 v83, 1.0, v83
	v_mfma_f32_16x16x32_bf16 v[66:69], v[74:77], v[138:141], v[66:69]
	v_rcp_f32_e32 v83, v83
	s_nop 0
	v_mul_f32_e32 v82, v83, v82
	v_fma_f32 v83, v193, v84, v104
	v_lshlrev_b32_e32 v84, 16, v197
	v_mul_f32_e32 v84, 0xbfb8aa3b, v84
	v_exp_f32_e32 v84, v84
	v_mul_f32_e32 v83, v195, v83
	v_add_u32_e32 v82, 0x8000, v82
	v_perm_b32 v82, v82, v0, s33
	v_add_f32_e32 v84, 1.0, v84
	v_rcp_f32_e32 v84, v84
	s_nop 0
	v_div_scale_f32 v86, s[56:57], v85, v85, 1.0
	v_rcp_f32_e32 v87, v86
	v_mul_f32_e32 v83, v84, v83
	v_mul_f32_e32 v84, v195, v105
	v_add_u32_e32 v83, 0x8000, v83
	v_fma_f32 v88, -v86, v87, 1.0
	v_fmac_f32_e32 v87, v88, v87
	v_div_scale_f32 v88, vcc, 1.0, v85, 1.0
	v_mul_f32_e32 v89, v88, v87
	v_fma_f32 v90, -v86, v89, v88
	v_fmac_f32_e32 v89, v90, v87
	v_fma_f32 v86, -v86, v89, v88
	v_div_fmas_f32 v86, v86, v87, v89
	v_div_fixup_f32 v85, v86, v85, 1.0
	v_mul_f32_e32 v84, v85, v84
	v_add_u32_e32 v0, 0x8000, v84
	v_perm_b32 v83, v0, v83, s33
	v_lshl_add_u64 v[84:85], v[188:189], 0, v[186:187]
	global_store_dwordx2 v[84:85], v[82:83], off
	v_mfma_f32_16x16x32_bf16 v[82:85], v[98:101], v[146:149], 0
	v_mfma_f32_16x16x32_bf16 v[82:85], v[110:113], v[158:161], v[82:85]
	v_mfma_f32_16x16x32_bf16 v[82:85], v[114:117], v[154:157], v[82:85]
	v_mfma_f32_16x16x32_bf16 v[82:85], v[126:129], v[150:153], v[82:85]
	s_nop 7
	v_fma_f32 v0, v193, v66, v82
	s_waitcnt vmcnt(3)
	v_lshlrev_b32_e32 v66, 16, v190
	v_mul_f32_e32 v66, 0xbfb8aa3b, v66
	v_exp_f32_e32 v66, v66
	v_mul_f32_e32 v0, v195, v0
	v_fmac_f32_e32 v85, v193, v69
	v_and_b32_e32 v69, 0xffff0000, v191
	v_add_f32_e32 v66, 1.0, v66
	v_div_scale_f32 v70, s[56:57], v66, v66, 1.0
	v_rcp_f32_e32 v71, v70
	v_mul_f32_e32 v69, 0xbfb8aa3b, v69
	v_exp_f32_e32 v69, v69
	v_fma_f32 v72, -v70, v71, 1.0
	v_fmac_f32_e32 v71, v72, v71
	v_div_scale_f32 v72, vcc, 1.0, v66, 1.0
	v_mul_f32_e32 v73, v72, v71
	v_fma_f32 v74, -v70, v73, v72
	v_fmac_f32_e32 v73, v74, v71
	v_fma_f32 v70, -v70, v73, v72
	v_div_fmas_f32 v70, v70, v71, v73
	v_div_fixup_f32 v66, v70, v66, 1.0
	v_mul_f32_e32 v0, v66, v0
	v_fma_f32 v66, v193, v67, v83
	v_and_b32_e32 v67, 0xffff0000, v190
	v_mul_f32_e32 v67, 0xbfb8aa3b, v67
	v_exp_f32_e32 v67, v67
	v_mul_f32_e32 v66, v195, v66
	v_add_f32_e32 v69, 1.0, v69
	v_add_u32_e32 v0, 0x8000, v0
	v_add_f32_e32 v67, 1.0, v67
	v_rcp_f32_e32 v67, v67
	s_nop 0
	v_mul_f32_e32 v66, v67, v66
	v_fma_f32 v67, v193, v68, v84
	v_lshlrev_b32_e32 v68, 16, v191
	v_mul_f32_e32 v68, 0xbfb8aa3b, v68
	v_exp_f32_e32 v68, v68
	v_mul_f32_e32 v67, v195, v67
	v_add_u32_e32 v66, 0x8000, v66
	v_perm_b32 v66, v66, v0, s33
	v_add_f32_e32 v68, 1.0, v68
	v_rcp_f32_e32 v68, v68
	s_nop 0
	v_div_scale_f32 v70, s[56:57], v69, v69, 1.0
	v_rcp_f32_e32 v71, v70
	v_mul_f32_e32 v67, v68, v67
	v_mul_f32_e32 v68, v195, v85
	v_add_u32_e32 v67, 0x8000, v67
	v_fma_f32 v72, -v70, v71, 1.0
	v_fmac_f32_e32 v71, v72, v71
	v_div_scale_f32 v72, vcc, 1.0, v69, 1.0
	v_mul_f32_e32 v73, v72, v71
	v_fma_f32 v74, -v70, v73, v72
	v_fmac_f32_e32 v73, v74, v71
	v_fma_f32 v70, -v70, v73, v72
	v_div_fmas_f32 v70, v70, v71, v73
	v_div_fixup_f32 v69, v70, v69, 1.0
	v_mul_f32_e32 v68, v69, v68
	v_add_u32_e32 v0, 0x8000, v68
	v_perm_b32 v67, v0, v67, s33
	v_lshl_add_u64 v[68:69], v[188:189], 0, v[184:185]
	s_andn2_b64 vcc, exec, s[54:55]
	s_mov_b32 s56, s21
	global_store_dwordx2 v[68:69], v[66:67], off
	s_cbranch_vccz .LBB0_623

; __device__ __forceinline__ float sigmoidf_(float x) { return 1.0f / (1.0f + __expf(-x)); }
;     __device__ __forceinline__ void operator()(const pg8::f32x4 (&acc)[2][2][4][2], const pg8::Unit& u, int wr, int wc, int fr_, int fq_) const {
;     ...
;             for (int m = 0; m < 4; ++m) rsv[ai * 4 + m] = *(const f32x2*)(RS + (size_t)(row0 + ai * 128 + m * 16) * 2);
;         const bool isq = u.pn < 8;
;         bf16* const OUTP = QB + (isq ? (size_t)0 : (size_t)((WS_PLE - WS_QB) / 2));
;         const int col0 = (isq ? u.pn : u.pn - 8) * 256 + wc * 32 + 8 * fq, ncol = u.pn * 256 + wc * 32 + 8 * fq;
; #pragma unroll
;         for (int bj = 0; bj < 2; ++bj) {
;             const pg8::f32x4* cp = (const pg8::f32x4*)(C12 + (size_t)(ncol + bj * 128) * 2);
;             const pg8::f32x4 k0 = cp[0], k1 = cp[1], k2 = cp[2], k3 = cp[3];
;             const pg8::f32x4 w0 = *(const pg8::f32x4*)(SWQ + ncol + bj * 128), w1 = *(const pg8::f32x4*)(SWQ + ncol + bj * 128 + 4);
; #pragma unroll
;             for (int ai = 0; ai < 2; ++ai)
; #pragma unroll
;                 for (int m = 0; m < 4; ++m) { const size_t ro = (size_t)(row0 + ai * 128 + m * 16) * D + col0 + bj * 128;
;                     const float rz = rsv[ai * 4 + m].x, mr = rsv[ai * 4 + m].y;
;                     pg8::f32x4 v0 = __builtin_convertvector(__builtin_bit_cast(i32x4_, acc[ai][bj][m][0]), pg8::f32x4) * (w0 * rz);
;                     pg8::f32x4 v1 = __builtin_convertvector(__builtin_bit_cast(i32x4_, acc[ai][bj][m][1]), pg8::f32x4) * (w1 * rz);
;                     v0[0] += mr * k0[0] + k0[1]; v0[1] += mr * k0[2] + k0[3]; v0[2] += mr * k1[0] + k1[1]; v0[3] += mr * k1[2] + k1[3];
;                     v1[0] += mr * k2[0] + k2[1]; v1[1] += mr * k2[2] + k2[3]; v1[2] += mr * k3[0] + k3[1]; v1[3] += mr * k3[2] + k3[3];
;                     if (!isq) { const v4u pj = *(const v4u*)(PJ + ro);
;                         v0[0] = sigmoidf_(v0[0]) * bflo(pj.x); v0[1] = sigmoidf_(v0[1]) * bfhi(pj.x); v0[2] = sigmoidf_(v0[2]) * bflo(pj.y); v0[3] = sigmoidf_(v0[3]) * bfhi(pj.y);
;                         v1[0] = sigmoidf_(v1[0]) * bflo(pj.z); v1[1] = sigmoidf_(v1[1]) * bfhi(pj.z); v1[2] = sigmoidf_(v1[2]) * bflo(pj.w); v1[3] = sigmoidf_(v1[3]) * bfhi(pj.w); }
.LBB0_1216:
	v_mov_b32_e32 v0, v1
	s_lshl_b32 s3, s24, 8
	v_mbcnt_lo_u32_b32 v0, -1, v0
	v_mbcnt_hi_u32_b32 v0, -1, v0
	s_add_i32 s3, s3, s52
	v_and_or_b32 v164, v0, 15, s3
	s_cmp_gt_i32 s2, 7
	v_ashrrev_i32_e32 v165, 31, v164
	v_or_b32_e32 v198, 16, v164
	s_cselect_b64 s[26:27], -1, 0
	s_lshl_b32 s17, s2, 8
	v_lshl_add_u64 v[74:75], v[164:165], 3, s[10:11]
	v_ashrrev_i32_e32 v199, 31, v198
	v_or_b32_e32 v196, 32, v164
	s_add_i32 s19, s17, 0xfffff800
	global_load_dwordx2 v[178:179], v[74:75], off
	v_lshl_add_u64 v[74:75], v[198:199], 3, s[10:11]
	v_ashrrev_i32_e32 v197, 31, v196
	v_or_b32_e32 v194, 48, v164
	s_cmp_lt_i32 s2, 8
	global_load_dwordx2 v[174:175], v[74:75], off
	v_lshl_add_u64 v[74:75], v[196:197], 3, s[10:11]
	v_ashrrev_i32_e32 v195, 31, v194
	v_add_u32_e32 v192, 0x80, v164
	s_cselect_b64 s[2:3], -1, 0
	global_load_dwordx2 v[172:173], v[74:75], off
	v_lshl_add_u64 v[74:75], v[194:195], 3, s[10:11]
	v_ashrrev_i32_e32 v193, 31, v192
	v_add_u32_e32 v190, 0x90, v164
	s_and_b64 vcc, s[2:3], exec
	v_ashrrev_i32_e32 v0, 1, v0
	global_load_dwordx2 v[170:171], v[74:75], off
	v_lshl_add_u64 v[74:75], v[192:193], 3, s[10:11]
	v_ashrrev_i32_e32 v191, 31, v190
	v_add_u32_e32 v188, 0xa0, v164
	s_cselect_b32 s19, s17, s19
	v_and_b32_e32 v0, -8, v0
	s_or_b32 s17, s17, s53
	global_load_dwordx2 v[160:161], v[74:75], off
	v_lshl_add_u64 v[74:75], v[190:191], 3, s[10:11]
	v_ashrrev_i32_e32 v189, 31, v188
	v_add_u32_e32 v186, 0xb0, v164
	v_add_u32_e32 v182, s17, v0
	global_load_dwordx2 v[158:159], v[74:75], off
	v_lshl_add_u64 v[74:75], v[188:189], 3, s[10:11]
	v_ashrrev_i32_e32 v187, 31, v186
	v_ashrrev_i32_e32 v183, 31, v182
	global_load_dwordx2 v[156:157], v[74:75], off
	v_lshl_add_u64 v[74:75], v[186:187], 3, s[10:11]
	v_lshl_add_u64 v[86:87], v[182:183], 3, s[8:9]
	global_load_dwordx2 v[154:155], v[74:75], off
	s_nop 0
	global_load_dwordx4 v[74:77], v[86:87], off offset:48
	global_load_dwordx4 v[78:81], v[86:87], off offset:32
	global_load_dwordx4 v[82:85], v[86:87], off offset:16
	s_nop 0
	global_load_dwordx4 v[86:89], v[86:87], off
	v_lshl_add_u64 v[184:185], v[182:183], 2, s[12:13]
	global_load_dwordx4 v[90:93], v[184:185], off offset:16
	global_load_dwordx4 v[94:97], v[184:185], off
	v_lshlrev_b64 v[176:177], 11, v[164:165]
	v_cvt_f32_i32_e32 v165, v151
	v_cvt_f32_i32_e32 v164, v150
	v_cvt_f32_i32_e32 v167, v153
	v_cvt_f32_i32_e32 v166, v152
	v_cvt_f32_i32_e32 v147, v147
	v_cvt_f32_i32_e32 v146, v146
	v_cvt_f32_i32_e32 v149, v149
	v_cvt_f32_i32_e32 v148, v148
	s_or_b32 s19, s19, s53
	v_add_u32_e32 v180, s19, v0
	v_ashrrev_i32_e32 v181, 31, v180
	v_lshl_add_u64 v[200:201], v[176:177], 0, v[180:181]
	s_waitcnt vmcnt(0)
	v_mov_b32_e32 v150, v86
	v_mov_b32_e32 v151, v88
	v_mov_b32_e32 v88, v87
	v_pk_mul_f32 v[152:153], v[178:179], v[94:95] op_sel_hi:[0,1]
	v_pk_fma_f32 v[86:87], v[178:179], v[150:151], v[88:89] op_sel:[1,0,0]
	v_pk_mul_f32 v[202:203], v[178:179], v[96:97] op_sel_hi:[0,1]
	v_pk_fma_f32 v[152:153], v[152:153], v[164:165], v[86:87]
	v_mov_b32_e32 v86, v82
	v_mov_b32_e32 v87, v84
	v_mov_b32_e32 v84, v83
	v_pk_fma_f32 v[82:83], v[178:179], v[86:87], v[84:85] op_sel:[1,0,0]
	v_pk_mul_f32 v[204:205], v[178:179], v[90:91] op_sel_hi:[0,1]
	v_pk_fma_f32 v[202:203], v[202:203], v[166:167], v[82:83]
	v_mov_b32_e32 v82, v78
	v_mov_b32_e32 v83, v80
	v_mov_b32_e32 v80, v79
	v_pk_fma_f32 v[78:79], v[178:179], v[82:83], v[80:81] op_sel:[1,0,0]
	v_pk_mul_f32 v[218:219], v[178:179], v[92:93] op_sel_hi:[0,1]
	v_pk_fma_f32 v[204:205], v[204:205], v[146:147], v[78:79]
	v_mov_b32_e32 v78, v74
	v_mov_b32_e32 v79, v76
	v_mov_b32_e32 v76, v75
	v_pk_fma_f32 v[74:75], v[178:179], v[78:79], v[76:77] op_sel:[1,0,0]
	s_nop 0
	v_pk_fma_f32 v[74:75], v[218:219], v[148:149], v[74:75]
	s_cbranch_vccnz .LBB0_1218
	v_lshl_add_u64 v[146:147], v[200:201], 1, s[6:7]
	global_load_dwordx4 v[146:149], v[146:147], off
	v_mul_f32_e32 v0, 0xbfb8aa3b, v152
	v_exp_f32_e32 v152, v0
	v_mul_f32_e32 v0, 0xbfb8aa3b, v153
	v_exp_f32_e32 v153, v0
	s_nop 0
	v_pk_add_f32 v[152:153], v[152:153], 1.0 op_sel_hi:[1,0]
	s_nop 0
	v_rcp_f32_e32 v153, v153
	s_nop 0
	v_rcp_f32_e32 v152, v152
	s_nop 0
	v_mul_f32_e32 v0, 0xbfb8aa3b, v202
	s_waitcnt vmcnt(0)
	v_lshlrev_b32_e32 v164, 16, v146
	v_and_b32_e32 v165, 0xffff0000, v146
	v_pk_mul_f32 v[152:153], v[152:153], v[164:165]
	v_exp_f32_e32 v164, v0
	v_mul_f32_e32 v0, 0xbfb8aa3b, v203
	v_exp_f32_e32 v165, v0
	s_nop 0
	v_pk_add_f32 v[164:165], v[164:165], 1.0 op_sel_hi:[1,0]
	s_nop 0
	v_rcp_f32_e32 v165, v165
	s_nop 0
	v_rcp_f32_e32 v164, v164
	s_nop 0
	v_lshlrev_b32_e32 v146, 16, v147
	v_and_b32_e32 v147, 0xffff0000, v147
	v_mul_f32_e32 v0, 0xbfb8aa3b, v204
	v_pk_mul_f32 v[202:203], v[164:165], v[146:147]
	v_exp_f32_e32 v146, v0
	v_mul_f32_e32 v0, 0xbfb8aa3b, v205
	v_exp_f32_e32 v147, v0
	s_nop 0
	v_pk_add_f32 v[146:147], v[146:147], 1.0 op_sel_hi:[1,0]
	s_nop 0
	v_rcp_f32_e32 v147, v147
	s_nop 0
	v_rcp_f32_e32 v146, v146
	s_nop 0
	v_mul_f32_e32 v0, 0xbfb8aa3b, v74
	v_exp_f32_e32 v74, v0
	v_mul_f32_e32 v0, 0xbfb8aa3b, v75
	v_exp_f32_e32 v75, v0
	v_lshlrev_b32_e32 v164, 16, v148
	v_and_b32_e32 v165, 0xffff0000, v148
	v_pk_mul_f32 v[204:205], v[146:147], v[164:165]
	v_pk_add_f32 v[74:75], v[74:75], 1.0 op_sel_hi:[1,0]
	s_nop 0
	v_rcp_f32_e32 v75, v75
	s_nop 0
	v_rcp_f32_e32 v74, v74
	s_nop 0
	v_lshlrev_b32_e32 v146, 16, v149
	v_and_b32_e32 v147, 0xffff0000, v149
	v_pk_mul_f32 v[74:75], v[74:75], v[146:147]
; __device__ __forceinline__ unsigned cvt_pk_bf16(float lo, float hi) { unsigned r; asm volatile("v_cvt_pk_bf16_f32 %0, %1, %2" : "=v"(r) : "v"(lo), "v"(hi)); return r; }
; __device__ __forceinline__ float sigmoidf_(float x) { return 1.0f / (1.0f + __expf(-x)); }
;     __device__ __forceinline__ void operator()(const pg8::f32x4 (&acc)[2][2][4][2], const pg8::Unit& u, int wr, int wc, int fr_, int fq_) const {
;     ...
;                 for (int m = 0; m < 4; ++m) { const size_t ro = (size_t)(row0 + ai * 128 + m * 16) * D + col0 + bj * 128;
;                     const float rz = rsv[ai * 4 + m].x, mr = rsv[ai * 4 + m].y;
;                     pg8::f32x4 v0 = __builtin_convertvector(__builtin_bit_cast(i32x4_, acc[ai][bj][m][0]), pg8::f32x4) * (w0 * rz);
;                     pg8::f32x4 v1 = __builtin_convertvector(__builtin_bit_cast(i32x4_, acc[ai][bj][m][1]), pg8::f32x4) * (w1 * rz);
;                     v0[0] += mr * k0[0] + k0[1]; v0[1] += mr * k0[2] + k0[3]; v0[2] += mr * k1[0] + k1[1]; v0[3] += mr * k1[2] + k1[3];
;                     v1[0] += mr * k2[0] + k2[1]; v1[1] += mr * k2[2] + k2[3]; v1[2] += mr * k3[0] + k3[1]; v1[3] += mr * k3[2] + k3[3];
;                     if (!isq) { const v4u pj = *(const v4u*)(PJ + ro);
;                         v0[0] = sigmoidf_(v0[0]) * bflo(pj.x); v0[1] = sigmoidf_(v0[1]) * bfhi(pj.x); v0[2] = sigmoidf_(v0[2]) * bflo(pj.y); v0[3] = sigmoidf_(v0[3]) * bfhi(pj.y);
;                         v1[0] = sigmoidf_(v1[0]) * bflo(pj.z); v1[1] = sigmoidf_(v1[1]) * bfhi(pj.z); v1[2] = sigmoidf_(v1[2]) * bflo(pj.w); v1[3] = sigmoidf_(v1[3]) * bfhi(pj.w); }
;                     v4u w; w.x = pg8::cvt_pk_bf16(v0[0], v0[1]); w.y = pg8::cvt_pk_bf16(v0[2], v0[3]); w.z = pg8::cvt_pk_bf16(v1[0], v1[1]); w.w = pg8::cvt_pk_bf16(v1[2], v1[3]);
;                     *(v4u*)(OUTP + ro) = w; asm volatile("" ::: "memory"); }
.LBB0_1218:
	s_and_b64 s[2:3], s[2:3], exec
	s_cselect_b32 s2, 0, 0x8000000
	s_add_u32 s24, s50, s2
	v_cvt_f32_i32_e32 v143, v143
	v_cvt_f32_i32_e32 v142, v142
	s_addc_u32 s25, s51, 0
	v_cvt_f32_i32_e32 v145, v145
	v_cvt_f32_i32_e32 v144, v144
	v_cvt_pk_bf16_f32 v164, v152, v153
	v_cvt_pk_bf16_f32 v165, v202, v203
	v_lshl_add_u64 v[148:149], v[200:201], 1, s[24:25]
	v_cvt_f32_i32_e32 v139, v139
	v_cvt_f32_i32_e32 v138, v138
	v_cvt_pk_bf16_f32 v166, v204, v205
	v_cvt_pk_bf16_f32 v167, v74, v75
	global_store_dwordx4 v[148:149], v[164:167], off
	v_cvt_f32_i32_e32 v141, v141
	v_cvt_f32_i32_e32 v140, v140
	v_pk_mul_f32 v[164:165], v[174:175], v[94:95] op_sel_hi:[0,1]
	v_pk_fma_f32 v[200:201], v[174:175], v[150:151], v[88:89] op_sel:[1,0,0]
	v_pk_mul_f32 v[152:153], v[174:175], v[96:97] op_sel_hi:[0,1]
	v_pk_fma_f32 v[142:143], v[164:165], v[142:143], v[200:201]
	v_pk_fma_f32 v[164:165], v[174:175], v[86:87], v[84:85] op_sel:[1,0,0]
	v_lshlrev_b64 v[146:147], 11, v[198:199]
	v_pk_mul_f32 v[198:199], v[174:175], v[90:91] op_sel_hi:[0,1]
	v_pk_fma_f32 v[144:145], v[152:153], v[144:145], v[164:165]
	v_pk_fma_f32 v[152:153], v[174:175], v[82:83], v[80:81] op_sel:[1,0,0]
	v_pk_mul_f32 v[166:167], v[174:175], v[92:93] op_sel_hi:[0,1]
	v_pk_fma_f32 v[198:199], v[198:199], v[138:139], v[152:153]
	v_pk_fma_f32 v[138:139], v[174:175], v[78:79], v[76:77] op_sel:[1,0,0]
	v_cndmask_b32_e64 v0, 0, 1, s[26:27]
	v_lshl_add_u64 v[74:75], v[146:147], 0, v[180:181]
	v_cmp_ne_u32_e64 s[2:3], 1, v0
	s_andn2_b64 vcc, exec, s[26:27]
	v_pk_fma_f32 v[152:153], v[166:167], v[140:141], v[138:139]
	s_cbranch_vccnz .LBB0_1220
	v_lshl_add_u64 v[138:139], v[74:75], 1, s[6:7]
	global_load_dwordx4 v[138:141], v[138:139], off
	v_mul_f32_e32 v0, 0xbfb8aa3b, v142
	v_exp_f32_e32 v142, v0
	v_mul_f32_e32 v0, 0xbfb8aa3b, v143
	v_exp_f32_e32 v143, v0
	s_nop 0
	v_pk_add_f32 v[142:143], v[142:143], 1.0 op_sel_hi:[1,0]
	s_nop 0
	v_rcp_f32_e32 v143, v143
	s_nop 0
	v_rcp_f32_e32 v142, v142
	s_nop 0
	v_mul_f32_e32 v0, 0xbfb8aa3b, v144
	v_exp_f32_e32 v144, v0
	v_mul_f32_e32 v0, 0xbfb8aa3b, v145
	v_exp_f32_e32 v145, v0
	s_waitcnt vmcnt(0)
	v_lshlrev_b32_e32 v164, 16, v138
	v_pk_add_f32 v[144:145], v[144:145], 1.0 op_sel_hi:[1,0]
	v_and_b32_e32 v165, 0xffff0000, v138
	v_pk_mul_f32 v[142:143], v[142:143], v[164:165]
	v_rcp_f32_e32 v145, v145
	s_nop 0
	v_rcp_f32_e32 v144, v144
	s_nop 0
	v_lshlrev_b32_e32 v138, 16, v139
	v_and_b32_e32 v139, 0xffff0000, v139
	v_mul_f32_e32 v0, 0xbfb8aa3b, v198
	v_pk_mul_f32 v[144:145], v[144:145], v[138:139]
	v_exp_f32_e32 v138, v0
	v_mul_f32_e32 v0, 0xbfb8aa3b, v199
	v_exp_f32_e32 v139, v0
	s_nop 0
	v_pk_add_f32 v[138:139], v[138:139], 1.0 op_sel_hi:[1,0]
	s_nop 0
	v_rcp_f32_e32 v139, v139
	s_nop 0
	v_rcp_f32_e32 v138, v138
	s_nop 0
	v_lshlrev_b32_e32 v164, 16, v140
	v_and_b32_e32 v165, 0xffff0000, v140
	v_mul_f32_e32 v0, 0xbfb8aa3b, v152
	v_pk_mul_f32 v[198:199], v[138:139], v[164:165]
	v_exp_f32_e32 v138, v0
	v_mul_f32_e32 v0, 0xbfb8aa3b, v153
	v_exp_f32_e32 v139, v0
	s_nop 0
	v_pk_add_f32 v[138:139], v[138:139], 1.0 op_sel_hi:[1,0]
	s_nop 0
	v_rcp_f32_e32 v139, v139
	s_nop 0
	v_rcp_f32_e32 v138, v138
	s_nop 0
	v_lshlrev_b32_e32 v140, 16, v141
	v_and_b32_e32 v141, 0xffff0000, v141
	v_pk_mul_f32 v[152:153], v[138:139], v[140:141]
.LBB0_1220:
	v_cvt_f32_i32_e32 v135, v135
	v_cvt_f32_i32_e32 v134, v134
	v_cvt_f32_i32_e32 v137, v137
	v_cvt_f32_i32_e32 v136, v136
	v_cvt_pk_bf16_f32 v142, v142, v143
	v_cvt_pk_bf16_f32 v143, v144, v145
	v_cvt_pk_bf16_f32 v144, v198, v199
	v_cvt_pk_bf16_f32 v145, v152, v153
	v_lshl_add_u64 v[140:141], v[74:75], 1, s[24:25]
	v_cvt_f32_i32_e32 v131, v131
	v_cvt_f32_i32_e32 v130, v130
	global_store_dwordx4 v[140:141], v[142:145], off
	v_cvt_f32_i32_e32 v133, v133
	v_cvt_f32_i32_e32 v132, v132
	v_pk_mul_f32 v[144:145], v[172:173], v[94:95] op_sel_hi:[0,1]
	v_pk_fma_f32 v[166:167], v[172:173], v[150:151], v[88:89] op_sel:[1,0,0]
	v_pk_mul_f32 v[142:143], v[172:173], v[96:97] op_sel_hi:[0,1]
	v_pk_fma_f32 v[134:135], v[144:145], v[134:135], v[166:167]
	v_pk_fma_f32 v[144:145], v[172:173], v[86:87], v[84:85] op_sel:[1,0,0]
	v_pk_mul_f32 v[164:165], v[172:173], v[90:91] op_sel_hi:[0,1]
	v_pk_fma_f32 v[136:137], v[142:143], v[136:137], v[144:145]
	v_pk_fma_f32 v[142:143], v[172:173], v[82:83], v[80:81] op_sel:[1,0,0]
	v_lshlrev_b64 v[138:139], 11, v[196:197]
	v_pk_mul_f32 v[152:153], v[172:173], v[92:93] op_sel_hi:[0,1]
	v_pk_fma_f32 v[144:145], v[164:165], v[130:131], v[142:143]
	v_pk_fma_f32 v[130:131], v[172:173], v[78:79], v[76:77] op_sel:[1,0,0]
	v_lshl_add_u64 v[74:75], v[138:139], 0, v[180:181]
	s_and_b64 vcc, exec, s[2:3]
	v_pk_fma_f32 v[142:143], v[152:153], v[132:133], v[130:131]
	s_cbranch_vccnz .LBB0_1222
	v_lshl_add_u64 v[130:131], v[74:75], 1, s[6:7]
	global_load_dwordx4 v[130:133], v[130:131], off
	v_mul_f32_e32 v0, 0xbfb8aa3b, v134
	v_exp_f32_e32 v134, v0
	v_mul_f32_e32 v0, 0xbfb8aa3b, v135
	v_exp_f32_e32 v135, v0
	s_nop 0
	v_pk_add_f32 v[134:135], v[134:135], 1.0 op_sel_hi:[1,0]
	s_nop 0
	v_rcp_f32_e32 v135, v135
	s_nop 0
	v_rcp_f32_e32 v134, v134
	s_nop 0
	v_mul_f32_e32 v0, 0xbfb8aa3b, v136
	v_exp_f32_e32 v136, v0
	v_mul_f32_e32 v0, 0xbfb8aa3b, v137
	v_exp_f32_e32 v137, v0
	s_waitcnt vmcnt(0)
	v_lshlrev_b32_e32 v152, 16, v130
	v_pk_add_f32 v[136:137], v[136:137], 1.0 op_sel_hi:[1,0]
	v_and_b32_e32 v153, 0xffff0000, v130
	v_pk_mul_f32 v[134:135], v[134:135], v[152:153]
	v_rcp_f32_e32 v137, v137
	s_nop 0
	v_rcp_f32_e32 v136, v136
	s_nop 0
	v_lshlrev_b32_e32 v130, 16, v131
	v_and_b32_e32 v131, 0xffff0000, v131
	v_mul_f32_e32 v0, 0xbfb8aa3b, v144
	v_pk_mul_f32 v[136:137], v[136:137], v[130:131]
	v_exp_f32_e32 v130, v0
	v_mul_f32_e32 v0, 0xbfb8aa3b, v145
	v_exp_f32_e32 v131, v0
	s_nop 0
	v_pk_add_f32 v[130:131], v[130:131], 1.0 op_sel_hi:[1,0]
	s_nop 0
	v_rcp_f32_e32 v131, v131
	s_nop 0
	v_rcp_f32_e32 v130, v130
	s_nop 0
	v_lshlrev_b32_e32 v144, 16, v132
	v_and_b32_e32 v145, 0xffff0000, v132
	v_mul_f32_e32 v0, 0xbfb8aa3b, v142
	v_pk_mul_f32 v[144:145], v[130:131], v[144:145]
	v_exp_f32_e32 v130, v0
	v_mul_f32_e32 v0, 0xbfb8aa3b, v143
	v_exp_f32_e32 v131, v0
	s_nop 0
	v_pk_add_f32 v[130:131], v[130:131], 1.0 op_sel_hi:[1,0]
	s_nop 0
	v_rcp_f32_e32 v131, v131
	s_nop 0
	v_rcp_f32_e32 v130, v130
	s_nop 0
	v_lshlrev_b32_e32 v132, 16, v133
	v_and_b32_e32 v133, 0xffff0000, v133
	v_pk_mul_f32 v[142:143], v[130:131], v[132:133]
; __device__ __forceinline__ unsigned cvt_pk_bf16(float lo, float hi) { unsigned r; asm volatile("v_cvt_pk_bf16_f32 %0, %1, %2" : "=v"(r) : "v"(lo), "v"(hi)); return r; }
; __device__ __forceinline__ float sigmoidf_(float x) { return 1.0f / (1.0f + __expf(-x)); }
;     __device__ __forceinline__ void operator()(const pg8::f32x4 (&acc)[2][2][4][2], const pg8::Unit& u, int wr, int wc, int fr_, int fq_) const {
;     ...
;                 for (int m = 0; m < 4; ++m) { const size_t ro = (size_t)(row0 + ai * 128 + m * 16) * D + col0 + bj * 128;
;                     const float rz = rsv[ai * 4 + m].x, mr = rsv[ai * 4 + m].y;
;                     pg8::f32x4 v0 = __builtin_convertvector(__builtin_bit_cast(i32x4_, acc[ai][bj][m][0]), pg8::f32x4) * (w0 * rz);
;                     pg8::f32x4 v1 = __builtin_convertvector(__builtin_bit_cast(i32x4_, acc[ai][bj][m][1]), pg8::f32x4) * (w1 * rz);
;                     v0[0] += mr * k0[0] + k0[1]; v0[1] += mr * k0[2] + k0[3]; v0[2] += mr * k1[0] + k1[1]; v0[3] += mr * k1[2] + k1[3];
;                     v1[0] += mr * k2[0] + k2[1]; v1[1] += mr * k2[2] + k2[3]; v1[2] += mr * k3[0] + k3[1]; v1[3] += mr * k3[2] + k3[3];
;                     if (!isq) { const v4u pj = *(const v4u*)(PJ + ro);
;                         v0[0] = sigmoidf_(v0[0]) * bflo(pj.x); v0[1] = sigmoidf_(v0[1]) * bfhi(pj.x); v0[2] = sigmoidf_(v0[2]) * bflo(pj.y); v0[3] = sigmoidf_(v0[3]) * bfhi(pj.y);
;                         v1[0] = sigmoidf_(v1[0]) * bflo(pj.z); v1[1] = sigmoidf_(v1[1]) * bfhi(pj.z); v1[2] = sigmoidf_(v1[2]) * bflo(pj.w); v1[3] = sigmoidf_(v1[3]) * bfhi(pj.w); }
;                     v4u w; w.x = pg8::cvt_pk_bf16(v0[0], v0[1]); w.y = pg8::cvt_pk_bf16(v0[2], v0[3]); w.z = pg8::cvt_pk_bf16(v1[0], v1[1]); w.w = pg8::cvt_pk_bf16(v1[2], v1[3]);
;                     *(v4u*)(OUTP + ro) = w; asm volatile("" ::: "memory"); }
.LBB0_1222:
	v_cvt_f32_i32_e32 v127, v127
	v_cvt_f32_i32_e32 v126, v126
	v_cvt_f32_i32_e32 v129, v129
	v_cvt_f32_i32_e32 v128, v128
	v_cvt_pk_bf16_f32 v134, v134, v135
	v_cvt_pk_bf16_f32 v135, v136, v137
	v_cvt_pk_bf16_f32 v136, v144, v145
	v_cvt_pk_bf16_f32 v137, v142, v143
	v_lshl_add_u64 v[132:133], v[74:75], 1, s[24:25]
	v_cvt_f32_i32_e32 v123, v123
	v_cvt_f32_i32_e32 v122, v122
	global_store_dwordx4 v[132:133], v[134:137], off
	v_cvt_f32_i32_e32 v125, v125
	v_cvt_f32_i32_e32 v124, v124
	v_pk_mul_f32 v[136:137], v[170:171], v[94:95] op_sel_hi:[0,1]
	v_pk_fma_f32 v[152:153], v[170:171], v[150:151], v[88:89] op_sel:[1,0,0]
	v_pk_mul_f32 v[134:135], v[170:171], v[96:97] op_sel_hi:[0,1]
	v_pk_fma_f32 v[126:127], v[136:137], v[126:127], v[152:153]
	v_pk_fma_f32 v[136:137], v[170:171], v[86:87], v[84:85] op_sel:[1,0,0]
	v_pk_mul_f32 v[144:145], v[170:171], v[90:91] op_sel_hi:[0,1]
	v_pk_fma_f32 v[128:129], v[134:135], v[128:129], v[136:137]
	v_pk_fma_f32 v[134:135], v[170:171], v[82:83], v[80:81] op_sel:[1,0,0]
	v_lshlrev_b64 v[130:131], 11, v[194:195]
	v_pk_mul_f32 v[142:143], v[170:171], v[92:93] op_sel_hi:[0,1]
	v_pk_fma_f32 v[136:137], v[144:145], v[122:123], v[134:135]
	v_pk_fma_f32 v[122:123], v[170:171], v[78:79], v[76:77] op_sel:[1,0,0]
	v_lshl_add_u64 v[74:75], v[130:131], 0, v[180:181]
	s_and_b64 vcc, exec, s[2:3]
	v_pk_fma_f32 v[134:135], v[142:143], v[124:125], v[122:123]
	s_cbranch_vccnz .LBB0_1224
	v_lshl_add_u64 v[122:123], v[74:75], 1, s[6:7]
	global_load_dwordx4 v[122:125], v[122:123], off
	v_mul_f32_e32 v0, 0xbfb8aa3b, v126
	v_exp_f32_e32 v126, v0
	v_mul_f32_e32 v0, 0xbfb8aa3b, v127
	v_exp_f32_e32 v127, v0
	s_nop 0
	v_pk_add_f32 v[126:127], v[126:127], 1.0 op_sel_hi:[1,0]
	s_nop 0
	v_rcp_f32_e32 v127, v127
	s_nop 0
	v_rcp_f32_e32 v126, v126
	s_nop 0
	v_mul_f32_e32 v0, 0xbfb8aa3b, v128
	v_exp_f32_e32 v128, v0
	v_mul_f32_e32 v0, 0xbfb8aa3b, v129
	v_exp_f32_e32 v129, v0
	s_waitcnt vmcnt(0)
	v_lshlrev_b32_e32 v142, 16, v122
	v_pk_add_f32 v[128:129], v[128:129], 1.0 op_sel_hi:[1,0]
	v_and_b32_e32 v143, 0xffff0000, v122
	v_pk_mul_f32 v[126:127], v[126:127], v[142:143]
	v_rcp_f32_e32 v129, v129
	s_nop 0
	v_rcp_f32_e32 v128, v128
	s_nop 0
	v_lshlrev_b32_e32 v122, 16, v123
	v_and_b32_e32 v123, 0xffff0000, v123
	v_mul_f32_e32 v0, 0xbfb8aa3b, v136
	v_pk_mul_f32 v[128:129], v[128:129], v[122:123]
	v_exp_f32_e32 v122, v0
	v_mul_f32_e32 v0, 0xbfb8aa3b, v137
	v_exp_f32_e32 v123, v0
	s_nop 0
	v_pk_add_f32 v[122:123], v[122:123], 1.0 op_sel_hi:[1,0]
	s_nop 0
	v_rcp_f32_e32 v123, v123
	s_nop 0
	v_rcp_f32_e32 v122, v122
	s_nop 0
	v_lshlrev_b32_e32 v136, 16, v124
	v_and_b32_e32 v137, 0xffff0000, v124
	v_mul_f32_e32 v0, 0xbfb8aa3b, v134
	v_pk_mul_f32 v[136:137], v[122:123], v[136:137]
	v_exp_f32_e32 v122, v0
	v_mul_f32_e32 v0, 0xbfb8aa3b, v135
	v_exp_f32_e32 v123, v0
	s_nop 0
	v_pk_add_f32 v[122:123], v[122:123], 1.0 op_sel_hi:[1,0]
	s_nop 0
	v_rcp_f32_e32 v123, v123
	s_nop 0
	v_rcp_f32_e32 v122, v122
	s_nop 0
	v_lshlrev_b32_e32 v124, 16, v125
	v_and_b32_e32 v125, 0xffff0000, v125
	v_pk_mul_f32 v[134:135], v[122:123], v[124:125]
.LBB0_1224:
	v_cvt_f32_i32_e32 v119, v119
	v_cvt_f32_i32_e32 v118, v118
	v_cvt_f32_i32_e32 v121, v121
	v_cvt_f32_i32_e32 v120, v120
	v_cvt_pk_bf16_f32 v126, v126, v127
	v_cvt_pk_bf16_f32 v127, v128, v129
	v_cvt_pk_bf16_f32 v128, v136, v137
	v_cvt_pk_bf16_f32 v129, v134, v135
	v_lshl_add_u64 v[124:125], v[74:75], 1, s[24:25]
	v_cvt_f32_i32_e32 v115, v115
	v_cvt_f32_i32_e32 v114, v114
	global_store_dwordx4 v[124:125], v[126:129], off
	v_cvt_f32_i32_e32 v117, v117
	v_cvt_f32_i32_e32 v116, v116
	v_pk_mul_f32 v[128:129], v[160:161], v[94:95] op_sel_hi:[0,1]
	v_pk_fma_f32 v[142:143], v[160:161], v[150:151], v[88:89] op_sel:[1,0,0]
	v_pk_mul_f32 v[126:127], v[160:161], v[96:97] op_sel_hi:[0,1]
	v_pk_fma_f32 v[118:119], v[128:129], v[118:119], v[142:143]
	v_pk_fma_f32 v[128:129], v[160:161], v[86:87], v[84:85] op_sel:[1,0,0]
	v_pk_mul_f32 v[136:137], v[160:161], v[90:91] op_sel_hi:[0,1]
	v_pk_fma_f32 v[120:121], v[126:127], v[120:121], v[128:129]
	v_pk_fma_f32 v[126:127], v[160:161], v[82:83], v[80:81] op_sel:[1,0,0]
	v_lshlrev_b64 v[122:123], 11, v[192:193]
	v_pk_mul_f32 v[134:135], v[160:161], v[92:93] op_sel_hi:[0,1]
	v_pk_fma_f32 v[128:129], v[136:137], v[114:115], v[126:127]
	v_pk_fma_f32 v[114:115], v[160:161], v[78:79], v[76:77] op_sel:[1,0,0]
	v_lshl_add_u64 v[74:75], v[122:123], 0, v[180:181]
	s_and_b64 vcc, exec, s[2:3]
	v_pk_fma_f32 v[126:127], v[134:135], v[116:117], v[114:115]
	s_cbranch_vccnz .LBB0_1226
	v_lshl_add_u64 v[114:115], v[74:75], 1, s[6:7]
	global_load_dwordx4 v[114:117], v[114:115], off
	v_mul_f32_e32 v0, 0xbfb8aa3b, v118
	v_exp_f32_e32 v118, v0
	v_mul_f32_e32 v0, 0xbfb8aa3b, v119
	v_exp_f32_e32 v119, v0
	s_nop 0
	v_pk_add_f32 v[118:119], v[118:119], 1.0 op_sel_hi:[1,0]
	s_nop 0
	v_rcp_f32_e32 v119, v119
	s_nop 0
	v_rcp_f32_e32 v118, v118
	s_nop 0
	v_mul_f32_e32 v0, 0xbfb8aa3b, v120
	v_exp_f32_e32 v120, v0
	v_mul_f32_e32 v0, 0xbfb8aa3b, v121
	v_exp_f32_e32 v121, v0
	s_waitcnt vmcnt(0)
	v_lshlrev_b32_e32 v134, 16, v114
	v_pk_add_f32 v[120:121], v[120:121], 1.0 op_sel_hi:[1,0]
	v_and_b32_e32 v135, 0xffff0000, v114
	v_pk_mul_f32 v[118:119], v[118:119], v[134:135]
	v_rcp_f32_e32 v121, v121
	s_nop 0
	v_rcp_f32_e32 v120, v120
	s_nop 0
	v_lshlrev_b32_e32 v114, 16, v115
	v_and_b32_e32 v115, 0xffff0000, v115
	v_mul_f32_e32 v0, 0xbfb8aa3b, v128
	v_pk_mul_f32 v[120:121], v[120:121], v[114:115]
	v_exp_f32_e32 v114, v0
	v_mul_f32_e32 v0, 0xbfb8aa3b, v129
	v_exp_f32_e32 v115, v0
	s_nop 0
	v_pk_add_f32 v[114:115], v[114:115], 1.0 op_sel_hi:[1,0]
	s_nop 0
	v_rcp_f32_e32 v115, v115
	s_nop 0
	v_rcp_f32_e32 v114, v114
	s_nop 0
	v_lshlrev_b32_e32 v128, 16, v116
	v_and_b32_e32 v129, 0xffff0000, v116
	v_mul_f32_e32 v0, 0xbfb8aa3b, v126
	v_pk_mul_f32 v[128:129], v[114:115], v[128:129]
	v_exp_f32_e32 v114, v0
	v_mul_f32_e32 v0, 0xbfb8aa3b, v127
	v_exp_f32_e32 v115, v0
	s_nop 0
	v_pk_add_f32 v[114:115], v[114:115], 1.0 op_sel_hi:[1,0]
	s_nop 0
	v_rcp_f32_e32 v115, v115
	s_nop 0
	v_rcp_f32_e32 v114, v114
	s_nop 0
	v_lshlrev_b32_e32 v116, 16, v117
	v_and_b32_e32 v117, 0xffff0000, v117
	v_pk_mul_f32 v[126:127], v[114:115], v[116:117]
; __device__ __forceinline__ unsigned cvt_pk_bf16(float lo, float hi) { unsigned r; asm volatile("v_cvt_pk_bf16_f32 %0, %1, %2" : "=v"(r) : "v"(lo), "v"(hi)); return r; }
; __device__ __forceinline__ float sigmoidf_(float x) { return 1.0f / (1.0f + __expf(-x)); }
;     __device__ __forceinline__ void operator()(const pg8::f32x4 (&acc)[2][2][4][2], const pg8::Unit& u, int wr, int wc, int fr_, int fq_) const {
;     ...
;                 for (int m = 0; m < 4; ++m) { const size_t ro = (size_t)(row0 + ai * 128 + m * 16) * D + col0 + bj * 128;
;                     const float rz = rsv[ai * 4 + m].x, mr = rsv[ai * 4 + m].y;
;                     pg8::f32x4 v0 = __builtin_convertvector(__builtin_bit_cast(i32x4_, acc[ai][bj][m][0]), pg8::f32x4) * (w0 * rz);
;                     pg8::f32x4 v1 = __builtin_convertvector(__builtin_bit_cast(i32x4_, acc[ai][bj][m][1]), pg8::f32x4) * (w1 * rz);
;                     v0[0] += mr * k0[0] + k0[1]; v0[1] += mr * k0[2] + k0[3]; v0[2] += mr * k1[0] + k1[1]; v0[3] += mr * k1[2] + k1[3];
;                     v1[0] += mr * k2[0] + k2[1]; v1[1] += mr * k2[2] + k2[3]; v1[2] += mr * k3[0] + k3[1]; v1[3] += mr * k3[2] + k3[3];
;                     if (!isq) { const v4u pj = *(const v4u*)(PJ + ro);
;                         v0[0] = sigmoidf_(v0[0]) * bflo(pj.x); v0[1] = sigmoidf_(v0[1]) * bfhi(pj.x); v0[2] = sigmoidf_(v0[2]) * bflo(pj.y); v0[3] = sigmoidf_(v0[3]) * bfhi(pj.y);
;                         v1[0] = sigmoidf_(v1[0]) * bflo(pj.z); v1[1] = sigmoidf_(v1[1]) * bfhi(pj.z); v1[2] = sigmoidf_(v1[2]) * bflo(pj.w); v1[3] = sigmoidf_(v1[3]) * bfhi(pj.w); }
;                     v4u w; w.x = pg8::cvt_pk_bf16(v0[0], v0[1]); w.y = pg8::cvt_pk_bf16(v0[2], v0[3]); w.z = pg8::cvt_pk_bf16(v1[0], v1[1]); w.w = pg8::cvt_pk_bf16(v1[2], v1[3]);
;                     *(v4u*)(OUTP + ro) = w; asm volatile("" ::: "memory"); }
.LBB0_1226:
	v_cvt_f32_i32_e32 v111, v111
	v_cvt_f32_i32_e32 v110, v110
	v_cvt_f32_i32_e32 v113, v113
	v_cvt_f32_i32_e32 v112, v112
	v_cvt_pk_bf16_f32 v118, v118, v119
	v_cvt_pk_bf16_f32 v119, v120, v121
	v_cvt_pk_bf16_f32 v120, v128, v129
	v_cvt_pk_bf16_f32 v121, v126, v127
	v_lshl_add_u64 v[116:117], v[74:75], 1, s[24:25]
	v_cvt_f32_i32_e32 v107, v107
	v_cvt_f32_i32_e32 v106, v106
	global_store_dwordx4 v[116:117], v[118:121], off
	v_cvt_f32_i32_e32 v109, v109
	v_cvt_f32_i32_e32 v108, v108
	v_pk_mul_f32 v[120:121], v[158:159], v[94:95] op_sel_hi:[0,1]
	v_pk_fma_f32 v[134:135], v[158:159], v[150:151], v[88:89] op_sel:[1,0,0]
	v_pk_mul_f32 v[118:119], v[158:159], v[96:97] op_sel_hi:[0,1]
	v_pk_fma_f32 v[110:111], v[120:121], v[110:111], v[134:135]
	v_pk_fma_f32 v[120:121], v[158:159], v[86:87], v[84:85] op_sel:[1,0,0]
	v_pk_mul_f32 v[128:129], v[158:159], v[90:91] op_sel_hi:[0,1]
	v_pk_fma_f32 v[112:113], v[118:119], v[112:113], v[120:121]
	v_pk_fma_f32 v[118:119], v[158:159], v[82:83], v[80:81] op_sel:[1,0,0]
	v_lshlrev_b64 v[114:115], 11, v[190:191]
	v_pk_mul_f32 v[126:127], v[158:159], v[92:93] op_sel_hi:[0,1]
	v_pk_fma_f32 v[120:121], v[128:129], v[106:107], v[118:119]
	v_pk_fma_f32 v[106:107], v[158:159], v[78:79], v[76:77] op_sel:[1,0,0]
	v_lshl_add_u64 v[74:75], v[114:115], 0, v[180:181]
	s_and_b64 vcc, exec, s[2:3]
	v_pk_fma_f32 v[118:119], v[126:127], v[108:109], v[106:107]
	s_cbranch_vccnz .LBB0_1228
	v_lshl_add_u64 v[106:107], v[74:75], 1, s[6:7]
	global_load_dwordx4 v[106:109], v[106:107], off
	v_mul_f32_e32 v0, 0xbfb8aa3b, v110
	v_exp_f32_e32 v110, v0
	v_mul_f32_e32 v0, 0xbfb8aa3b, v111
	v_exp_f32_e32 v111, v0
	s_nop 0
	v_pk_add_f32 v[110:111], v[110:111], 1.0 op_sel_hi:[1,0]
	s_nop 0
	v_rcp_f32_e32 v111, v111
	s_nop 0
	v_rcp_f32_e32 v110, v110
	s_nop 0
	v_mul_f32_e32 v0, 0xbfb8aa3b, v112
	v_exp_f32_e32 v112, v0
	v_mul_f32_e32 v0, 0xbfb8aa3b, v113
	v_exp_f32_e32 v113, v0
	s_waitcnt vmcnt(0)
	v_lshlrev_b32_e32 v126, 16, v106
	v_pk_add_f32 v[112:113], v[112:113], 1.0 op_sel_hi:[1,0]
	v_and_b32_e32 v127, 0xffff0000, v106
	v_pk_mul_f32 v[110:111], v[110:111], v[126:127]
	v_rcp_f32_e32 v113, v113
	s_nop 0
	v_rcp_f32_e32 v112, v112
	s_nop 0
	v_lshlrev_b32_e32 v106, 16, v107
	v_and_b32_e32 v107, 0xffff0000, v107
	v_mul_f32_e32 v0, 0xbfb8aa3b, v120
	v_pk_mul_f32 v[112:113], v[112:113], v[106:107]
	v_exp_f32_e32 v106, v0
	v_mul_f32_e32 v0, 0xbfb8aa3b, v121
	v_exp_f32_e32 v107, v0
	s_nop 0
	v_pk_add_f32 v[106:107], v[106:107], 1.0 op_sel_hi:[1,0]
	s_nop 0
	v_rcp_f32_e32 v107, v107
	s_nop 0
	v_rcp_f32_e32 v106, v106
	s_nop 0
	v_lshlrev_b32_e32 v120, 16, v108
	v_and_b32_e32 v121, 0xffff0000, v108
	v_mul_f32_e32 v0, 0xbfb8aa3b, v118
	v_pk_mul_f32 v[120:121], v[106:107], v[120:121]
	v_exp_f32_e32 v106, v0
	v_mul_f32_e32 v0, 0xbfb8aa3b, v119
	v_exp_f32_e32 v107, v0
	s_nop 0
	v_pk_add_f32 v[106:107], v[106:107], 1.0 op_sel_hi:[1,0]
	s_nop 0
	v_rcp_f32_e32 v107, v107
	s_nop 0
	v_rcp_f32_e32 v106, v106
	s_nop 0
	v_lshlrev_b32_e32 v108, 16, v109
	v_and_b32_e32 v109, 0xffff0000, v109
	v_pk_mul_f32 v[118:119], v[106:107], v[108:109]
.LBB0_1228:
	v_cvt_f32_i32_e32 v103, v103
	v_cvt_f32_i32_e32 v102, v102
	v_cvt_f32_i32_e32 v105, v105
	v_cvt_f32_i32_e32 v104, v104
	v_cvt_pk_bf16_f32 v110, v110, v111
	v_cvt_pk_bf16_f32 v111, v112, v113
	v_cvt_pk_bf16_f32 v112, v120, v121
	v_cvt_pk_bf16_f32 v113, v118, v119
	v_lshl_add_u64 v[108:109], v[74:75], 1, s[24:25]
	v_cvt_f32_i32_e32 v99, v99
	v_cvt_f32_i32_e32 v98, v98
	global_store_dwordx4 v[108:109], v[110:113], off
	v_cvt_f32_i32_e32 v101, v101
	v_cvt_f32_i32_e32 v100, v100
	v_pk_mul_f32 v[112:113], v[156:157], v[94:95] op_sel_hi:[0,1]
	v_pk_fma_f32 v[126:127], v[156:157], v[150:151], v[88:89] op_sel:[1,0,0]
	v_pk_mul_f32 v[110:111], v[156:157], v[96:97] op_sel_hi:[0,1]
	v_pk_fma_f32 v[102:103], v[112:113], v[102:103], v[126:127]
	v_pk_fma_f32 v[112:113], v[156:157], v[86:87], v[84:85] op_sel:[1,0,0]
	v_pk_mul_f32 v[120:121], v[156:157], v[90:91] op_sel_hi:[0,1]
	v_pk_fma_f32 v[104:105], v[110:111], v[104:105], v[112:113]
	v_pk_fma_f32 v[110:111], v[156:157], v[82:83], v[80:81] op_sel:[1,0,0]
	v_lshlrev_b64 v[106:107], 11, v[188:189]
	v_pk_mul_f32 v[118:119], v[156:157], v[92:93] op_sel_hi:[0,1]
	v_pk_fma_f32 v[112:113], v[120:121], v[98:99], v[110:111]
	v_pk_fma_f32 v[98:99], v[156:157], v[78:79], v[76:77] op_sel:[1,0,0]
	v_lshl_add_u64 v[74:75], v[106:107], 0, v[180:181]
	s_and_b64 vcc, exec, s[2:3]
	v_pk_fma_f32 v[110:111], v[118:119], v[100:101], v[98:99]
	s_cbranch_vccnz .LBB0_1230
	v_lshl_add_u64 v[98:99], v[74:75], 1, s[6:7]
	global_load_dwordx4 v[98:101], v[98:99], off
	v_mul_f32_e32 v0, 0xbfb8aa3b, v102
	v_exp_f32_e32 v102, v0
	v_mul_f32_e32 v0, 0xbfb8aa3b, v103
	v_exp_f32_e32 v103, v0
	s_nop 0
	v_pk_add_f32 v[102:103], v[102:103], 1.0 op_sel_hi:[1,0]
	s_nop 0
	v_rcp_f32_e32 v103, v103
	s_nop 0
	v_rcp_f32_e32 v102, v102
	s_nop 0
	v_mul_f32_e32 v0, 0xbfb8aa3b, v104
	v_exp_f32_e32 v104, v0
	v_mul_f32_e32 v0, 0xbfb8aa3b, v105
	v_exp_f32_e32 v105, v0
	s_waitcnt vmcnt(0)
	v_lshlrev_b32_e32 v118, 16, v98
	v_pk_add_f32 v[104:105], v[104:105], 1.0 op_sel_hi:[1,0]
	v_and_b32_e32 v119, 0xffff0000, v98
	v_pk_mul_f32 v[102:103], v[102:103], v[118:119]
	v_rcp_f32_e32 v105, v105
	s_nop 0
	v_rcp_f32_e32 v104, v104
	s_nop 0
	v_lshlrev_b32_e32 v98, 16, v99
	v_and_b32_e32 v99, 0xffff0000, v99
	v_mul_f32_e32 v0, 0xbfb8aa3b, v112
	v_pk_mul_f32 v[104:105], v[104:105], v[98:99]
	v_exp_f32_e32 v98, v0
	v_mul_f32_e32 v0, 0xbfb8aa3b, v113
	v_exp_f32_e32 v99, v0
	s_nop 0
	v_pk_add_f32 v[98:99], v[98:99], 1.0 op_sel_hi:[1,0]
	s_nop 0
	v_rcp_f32_e32 v99, v99
	s_nop 0
	v_rcp_f32_e32 v98, v98
	s_nop 0
	v_lshlrev_b32_e32 v112, 16, v100
	v_and_b32_e32 v113, 0xffff0000, v100
	v_mul_f32_e32 v0, 0xbfb8aa3b, v110
	v_pk_mul_f32 v[112:113], v[98:99], v[112:113]
	v_exp_f32_e32 v98, v0
	v_mul_f32_e32 v0, 0xbfb8aa3b, v111
	v_exp_f32_e32 v99, v0
	s_nop 0
	v_pk_add_f32 v[98:99], v[98:99], 1.0 op_sel_hi:[1,0]
	s_nop 0
	v_rcp_f32_e32 v99, v99
	s_nop 0
	v_rcp_f32_e32 v98, v98
	s_nop 0
	v_lshlrev_b32_e32 v100, 16, v101
	v_and_b32_e32 v101, 0xffff0000, v101
	v_pk_mul_f32 v[110:111], v[98:99], v[100:101]
; __device__ __forceinline__ unsigned cvt_pk_bf16(float lo, float hi) { unsigned r; asm volatile("v_cvt_pk_bf16_f32 %0, %1, %2" : "=v"(r) : "v"(lo), "v"(hi)); return r; }
; __device__ __forceinline__ float sigmoidf_(float x) { return 1.0f / (1.0f + __expf(-x)); }
;     __device__ __forceinline__ void operator()(const pg8::f32x4 (&acc)[2][2][4][2], const pg8::Unit& u, int wr, int wc, int fr_, int fq_) const {
;     ...
;             const pg8::f32x4* cp = (const pg8::f32x4*)(C12 + (size_t)(ncol + bj * 128) * 2);
;             const pg8::f32x4 k0 = cp[0], k1 = cp[1], k2 = cp[2], k3 = cp[3];
;             const pg8::f32x4 w0 = *(const pg8::f32x4*)(SWQ + ncol + bj * 128), w1 = *(const pg8::f32x4*)(SWQ + ncol + bj * 128 + 4);
; #pragma unroll
;             for (int ai = 0; ai < 2; ++ai)
; #pragma unroll
;                 for (int m = 0; m < 4; ++m) { const size_t ro = (size_t)(row0 + ai * 128 + m * 16) * D + col0 + bj * 128;
;                     const float rz = rsv[ai * 4 + m].x, mr = rsv[ai * 4 + m].y;
;                     pg8::f32x4 v0 = __builtin_convertvector(__builtin_bit_cast(i32x4_, acc[ai][bj][m][0]), pg8::f32x4) * (w0 * rz);
;                     pg8::f32x4 v1 = __builtin_convertvector(__builtin_bit_cast(i32x4_, acc[ai][bj][m][1]), pg8::f32x4) * (w1 * rz);
;                     v0[0] += mr * k0[0] + k0[1]; v0[1] += mr * k0[2] + k0[3]; v0[2] += mr * k1[0] + k1[1]; v0[3] += mr * k1[2] + k1[3];
;                     v1[0] += mr * k2[0] + k2[1]; v1[1] += mr * k2[2] + k2[3]; v1[2] += mr * k3[0] + k3[1]; v1[3] += mr * k3[2] + k3[3];
;                     if (!isq) { const v4u pj = *(const v4u*)(PJ + ro);
;                         v0[0] = sigmoidf_(v0[0]) * bflo(pj.x); v0[1] = sigmoidf_(v0[1]) * bfhi(pj.x); v0[2] = sigmoidf_(v0[2]) * bflo(pj.y); v0[3] = sigmoidf_(v0[3]) * bfhi(pj.y);
;                         v1[0] = sigmoidf_(v1[0]) * bflo(pj.z); v1[1] = sigmoidf_(v1[1]) * bfhi(pj.z); v1[2] = sigmoidf_(v1[2]) * bflo(pj.w); v1[3] = sigmoidf_(v1[3]) * bfhi(pj.w); }
;                     v4u w; w.x = pg8::cvt_pk_bf16(v0[0], v0[1]); w.y = pg8::cvt_pk_bf16(v0[2], v0[3]); w.z = pg8::cvt_pk_bf16(v1[0], v1[1]); w.w = pg8::cvt_pk_bf16(v1[2], v1[3]);
;                     *(v4u*)(OUTP + ro) = w; asm volatile("" ::: "memory"); }
.LBB0_1230:
	v_cvt_f32_i32_e32 v67, v67
	v_cvt_f32_i32_e32 v66, v66
	v_lshl_add_u64 v[100:101], v[74:75], 1, s[24:25]
	v_cvt_f32_i32_e32 v71, v71
	v_cvt_f32_i32_e32 v70, v70
	v_cvt_f32_i32_e32 v73, v73
	v_cvt_f32_i32_e32 v72, v72
	v_cvt_f32_i32_e32 v69, v69
	v_cvt_f32_i32_e32 v68, v68
	v_cvt_pk_bf16_f32 v102, v102, v103
	v_cvt_pk_bf16_f32 v103, v104, v105
	v_cvt_pk_bf16_f32 v104, v112, v113
	v_cvt_pk_bf16_f32 v105, v110, v111
	global_store_dwordx4 v[100:101], v[102:105], off
	v_pk_mul_f32 v[90:91], v[154:155], v[90:91] op_sel_hi:[0,1]
	v_pk_fma_f32 v[80:81], v[154:155], v[82:83], v[80:81] op_sel:[1,0,0]
	v_lshlrev_b64 v[98:99], 11, v[186:187]
	v_pk_mul_f32 v[96:97], v[154:155], v[96:97] op_sel_hi:[0,1]
	v_pk_mul_f32 v[94:95], v[154:155], v[94:95] op_sel_hi:[0,1]
	v_pk_mul_f32 v[92:93], v[154:155], v[92:93] op_sel_hi:[0,1]
	v_pk_fma_f32 v[88:89], v[154:155], v[150:151], v[88:89] op_sel:[1,0,0]
	v_pk_fma_f32 v[84:85], v[154:155], v[86:87], v[84:85] op_sel:[1,0,0]
	v_pk_fma_f32 v[80:81], v[90:91], v[66:67], v[80:81]
	v_pk_fma_f32 v[66:67], v[154:155], v[78:79], v[76:77] op_sel:[1,0,0]
	v_lshl_add_u64 v[74:75], v[98:99], 0, v[180:181]
	v_pk_fma_f32 v[70:71], v[94:95], v[70:71], v[88:89]
	v_pk_fma_f32 v[72:73], v[96:97], v[72:73], v[84:85]
	s_and_b64 vcc, exec, s[2:3]
	v_pk_fma_f32 v[76:77], v[92:93], v[68:69], v[66:67]
	s_cbranch_vccnz .LBB0_1232
	v_lshl_add_u64 v[66:67], v[74:75], 1, s[6:7]
	global_load_dwordx4 v[66:69], v[66:67], off
	v_mul_f32_e32 v0, 0xbfb8aa3b, v70
	v_exp_f32_e32 v70, v0
	v_mul_f32_e32 v0, 0xbfb8aa3b, v71
	v_exp_f32_e32 v71, v0
	s_nop 0
	v_pk_add_f32 v[70:71], v[70:71], 1.0 op_sel_hi:[1,0]
	s_nop 0
	v_rcp_f32_e32 v71, v71
	s_nop 0
	v_rcp_f32_e32 v70, v70
	s_nop 0
	v_mul_f32_e32 v0, 0xbfb8aa3b, v72
	v_exp_f32_e32 v72, v0
	v_mul_f32_e32 v0, 0xbfb8aa3b, v73
	v_exp_f32_e32 v73, v0
	s_waitcnt vmcnt(0)
	v_lshlrev_b32_e32 v78, 16, v66
	v_pk_add_f32 v[72:73], v[72:73], 1.0 op_sel_hi:[1,0]
	v_and_b32_e32 v79, 0xffff0000, v66
	v_pk_mul_f32 v[70:71], v[70:71], v[78:79]
	v_rcp_f32_e32 v73, v73
	s_nop 0
	v_rcp_f32_e32 v72, v72
	s_nop 0
	v_lshlrev_b32_e32 v66, 16, v67
	v_and_b32_e32 v67, 0xffff0000, v67
	v_mul_f32_e32 v0, 0xbfb8aa3b, v80
	v_pk_mul_f32 v[72:73], v[72:73], v[66:67]
	v_exp_f32_e32 v66, v0
	v_mul_f32_e32 v0, 0xbfb8aa3b, v81
	v_exp_f32_e32 v67, v0
	s_nop 0
	v_pk_add_f32 v[66:67], v[66:67], 1.0 op_sel_hi:[1,0]
	s_nop 0
	v_rcp_f32_e32 v67, v67
	s_nop 0
	v_rcp_f32_e32 v66, v66
	s_nop 0
	v_lshlrev_b32_e32 v78, 16, v68
	v_and_b32_e32 v79, 0xffff0000, v68
	v_mul_f32_e32 v0, 0xbfb8aa3b, v76
	v_pk_mul_f32 v[80:81], v[66:67], v[78:79]
	v_exp_f32_e32 v66, v0
	v_mul_f32_e32 v0, 0xbfb8aa3b, v77
	v_exp_f32_e32 v67, v0
	s_nop 0
	v_pk_add_f32 v[66:67], v[66:67], 1.0 op_sel_hi:[1,0]
	s_nop 0
	v_rcp_f32_e32 v67, v67
	s_nop 0
	v_rcp_f32_e32 v66, v66
	s_nop 0
	v_lshlrev_b32_e32 v68, 16, v69
	v_and_b32_e32 v69, 0xffff0000, v69
	v_pk_mul_f32 v[76:77], v[66:67], v[68:69]
.LBB0_1232:
	v_lshl_add_u64 v[90:91], v[74:75], 1, s[24:25]
	v_cvt_pk_bf16_f32 v66, v70, v71
	v_cvt_pk_bf16_f32 v67, v72, v73
	v_cvt_pk_bf16_f32 v68, v80, v81
	v_cvt_pk_bf16_f32 v69, v76, v77
	global_store_dwordx4 v[90:91], v[66:69], off
	v_lshl_add_u64 v[78:79], v[182:183], 3, s[8:9]
	global_load_dwordx4 v[66:69], v[78:79], off offset:1072
	global_load_dwordx4 v[70:73], v[78:79], off offset:1056
	global_load_dwordx4 v[74:77], v[78:79], off offset:1040
	s_nop 0
	global_load_dwordx4 v[78:81], v[78:79], off offset:1024
	s_nop 0
	global_load_dwordx4 v[82:85], v[184:185], off offset:528
	global_load_dwordx4 v[86:89], v[184:185], off offset:512
	v_cvt_f32_i32_e32 v97, v63
	v_cvt_f32_i32_e32 v96, v62
	v_mov_b32_e32 v94, v178
	v_mov_b32_e32 v95, v178
	v_mov_b32_e32 v102, v179
	v_mov_b32_e32 v103, v179
	v_cvt_f32_i32_e32 v105, v65
	v_cvt_f32_i32_e32 v104, v64
	v_mov_b32_e32 v179, v178
	v_cvt_f32_i32_e32 v59, v59
	v_cvt_f32_i32_e32 v58, v58
	v_cvt_f32_i32_e32 v61, v61
	v_cvt_f32_i32_e32 v60, v60
	v_lshl_add_u64 v[92:93], v[180:181], 0, s[34:35]
	s_and_b64 vcc, exec, s[2:3]
	s_waitcnt vmcnt(2)
	v_mov_b32_e32 v62, v78
	v_mov_b32_e32 v63, v80
	v_mov_b32_e32 v80, v79
	s_waitcnt vmcnt(0)
	v_pk_mul_f32 v[64:65], v[94:95], v[86:87]
	v_pk_fma_f32 v[78:79], v[102:103], v[62:63], v[80:81]
	v_pk_mul_f32 v[110:111], v[178:179], v[88:89]
	v_pk_fma_f32 v[78:79], v[64:65], v[96:97], v[78:79]
	v_mov_b32_e32 v64, v74
	v_mov_b32_e32 v65, v76
	v_mov_b32_e32 v76, v75
	v_pk_fma_f32 v[74:75], v[102:103], v[64:65], v[76:77]
	v_pk_mul_f32 v[118:119], v[94:95], v[82:83]
	v_pk_fma_f32 v[94:95], v[110:111], v[104:105], v[74:75]
	v_mov_b32_e32 v74, v70
	v_mov_b32_e32 v75, v72
	v_mov_b32_e32 v72, v71
	v_pk_fma_f32 v[70:71], v[102:103], v[74:75], v[72:73]
	v_pk_mul_f32 v[112:113], v[178:179], v[84:85]
	v_pk_fma_f32 v[96:97], v[118:119], v[58:59], v[70:71]
	v_mov_b32_e32 v70, v66
	v_mov_b32_e32 v71, v68
	v_mov_b32_e32 v68, v67
	v_pk_fma_f32 v[58:59], v[102:103], v[70:71], v[68:69]
	s_nop 0
	v_pk_fma_f32 v[66:67], v[112:113], v[60:61], v[58:59]
	s_cbranch_vccnz .LBB0_1234
	v_lshl_add_u64 v[58:59], v[92:93], 0, v[176:177]
	v_lshl_add_u64 v[58:59], v[58:59], 1, s[6:7]
	global_load_dwordx4 v[58:61], v[58:59], off
	v_mul_f32_e32 v0, 0xbfb8aa3b, v78
	v_exp_f32_e32 v78, v0
	v_mul_f32_e32 v0, 0xbfb8aa3b, v79
	v_exp_f32_e32 v79, v0
	s_nop 0
	v_pk_add_f32 v[78:79], v[78:79], 1.0 op_sel_hi:[1,0]
	s_nop 0
	v_rcp_f32_e32 v79, v79
	s_nop 0
	v_rcp_f32_e32 v78, v78
	s_nop 0
	v_mul_f32_e32 v0, 0xbfb8aa3b, v94
	v_exp_f32_e32 v94, v0
	v_mul_f32_e32 v0, 0xbfb8aa3b, v95
	v_exp_f32_e32 v95, v0
	s_waitcnt vmcnt(0)
	v_lshlrev_b32_e32 v102, 16, v58
	v_pk_add_f32 v[94:95], v[94:95], 1.0 op_sel_hi:[1,0]
	v_and_b32_e32 v103, 0xffff0000, v58
	v_pk_mul_f32 v[78:79], v[78:79], v[102:103]
	v_rcp_f32_e32 v95, v95
	s_nop 0
	v_rcp_f32_e32 v94, v94
	s_nop 0
	v_lshlrev_b32_e32 v58, 16, v59
	v_and_b32_e32 v59, 0xffff0000, v59
	v_mul_f32_e32 v0, 0xbfb8aa3b, v96
	v_pk_mul_f32 v[94:95], v[94:95], v[58:59]
	v_exp_f32_e32 v58, v0
	v_mul_f32_e32 v0, 0xbfb8aa3b, v97
	v_exp_f32_e32 v59, v0
	s_nop 0
	v_pk_add_f32 v[58:59], v[58:59], 1.0 op_sel_hi:[1,0]
	s_nop 0
	v_rcp_f32_e32 v59, v59
	s_nop 0
	v_rcp_f32_e32 v58, v58
	s_nop 0
	v_lshlrev_b32_e32 v96, 16, v60
	v_and_b32_e32 v97, 0xffff0000, v60
	v_mul_f32_e32 v0, 0xbfb8aa3b, v66
	v_pk_mul_f32 v[96:97], v[58:59], v[96:97]
	v_exp_f32_e32 v58, v0
	v_mul_f32_e32 v0, 0xbfb8aa3b, v67
	v_exp_f32_e32 v59, v0
	s_nop 0
	v_pk_add_f32 v[58:59], v[58:59], 1.0 op_sel_hi:[1,0]
	s_nop 0
	v_rcp_f32_e32 v59, v59
	s_nop 0
	v_rcp_f32_e32 v58, v58
	s_nop 0
	v_lshlrev_b32_e32 v60, 16, v61
	v_and_b32_e32 v61, 0xffff0000, v61
	v_pk_mul_f32 v[66:67], v[58:59], v[60:61]
; __device__ __forceinline__ unsigned cvt_pk_bf16(float lo, float hi) { unsigned r; asm volatile("v_cvt_pk_bf16_f32 %0, %1, %2" : "=v"(r) : "v"(lo), "v"(hi)); return r; }
; __device__ __forceinline__ float sigmoidf_(float x) { return 1.0f / (1.0f + __expf(-x)); }
;     __device__ __forceinline__ void operator()(const pg8::f32x4 (&acc)[2][2][4][2], const pg8::Unit& u, int wr, int wc, int fr_, int fq_) const {
;     ...
;                 for (int m = 0; m < 4; ++m) { const size_t ro = (size_t)(row0 + ai * 128 + m * 16) * D + col0 + bj * 128;
;                     const float rz = rsv[ai * 4 + m].x, mr = rsv[ai * 4 + m].y;
;                     pg8::f32x4 v0 = __builtin_convertvector(__builtin_bit_cast(i32x4_, acc[ai][bj][m][0]), pg8::f32x4) * (w0 * rz);
;                     pg8::f32x4 v1 = __builtin_convertvector(__builtin_bit_cast(i32x4_, acc[ai][bj][m][1]), pg8::f32x4) * (w1 * rz);
;                     v0[0] += mr * k0[0] + k0[1]; v0[1] += mr * k0[2] + k0[3]; v0[2] += mr * k1[0] + k1[1]; v0[3] += mr * k1[2] + k1[3];
;                     v1[0] += mr * k2[0] + k2[1]; v1[1] += mr * k2[2] + k2[3]; v1[2] += mr * k3[0] + k3[1]; v1[3] += mr * k3[2] + k3[3];
;                     if (!isq) { const v4u pj = *(const v4u*)(PJ + ro);
;                         v0[0] = sigmoidf_(v0[0]) * bflo(pj.x); v0[1] = sigmoidf_(v0[1]) * bfhi(pj.x); v0[2] = sigmoidf_(v0[2]) * bflo(pj.y); v0[3] = sigmoidf_(v0[3]) * bfhi(pj.y);
;                         v1[0] = sigmoidf_(v1[0]) * bflo(pj.z); v1[1] = sigmoidf_(v1[1]) * bfhi(pj.z); v1[2] = sigmoidf_(v1[2]) * bflo(pj.w); v1[3] = sigmoidf_(v1[3]) * bfhi(pj.w); }
;                     v4u w; w.x = pg8::cvt_pk_bf16(v0[0], v0[1]); w.y = pg8::cvt_pk_bf16(v0[2], v0[3]); w.z = pg8::cvt_pk_bf16(v1[0], v1[1]); w.w = pg8::cvt_pk_bf16(v1[2], v1[3]);
;                     *(v4u*)(OUTP + ro) = w; asm volatile("" ::: "memory"); }
.LBB0_1234:
	v_cvt_f32_i32_e32 v55, v55
	v_cvt_f32_i32_e32 v54, v54
	v_cvt_f32_i32_e32 v57, v57
	v_cvt_f32_i32_e32 v56, v56
	v_mov_b32_e32 v102, v174
	v_mov_b32_e32 v103, v174
	v_mov_b32_e32 v104, v175
	v_mov_b32_e32 v105, v175
	v_cvt_pk_bf16_f32 v58, v78, v79
	v_cvt_pk_bf16_f32 v59, v94, v95
	v_cvt_pk_bf16_f32 v60, v96, v97
	v_cvt_pk_bf16_f32 v61, v66, v67
	v_cvt_f32_i32_e32 v51, v51
	v_cvt_f32_i32_e32 v50, v50
	global_store_dwordx4 v[148:149], v[58:61], off offset:256
	v_mov_b32_e32 v175, v174
	v_cvt_f32_i32_e32 v53, v53
	v_pk_mul_f32 v[60:61], v[102:103], v[86:87]
	v_cvt_f32_i32_e32 v52, v52
	v_pk_fma_f32 v[94:95], v[104:105], v[62:63], v[80:81]
	v_pk_mul_f32 v[58:59], v[174:175], v[88:89]
	v_pk_fma_f32 v[54:55], v[60:61], v[54:55], v[94:95]
	v_pk_fma_f32 v[60:61], v[104:105], v[64:65], v[76:77]
	v_pk_mul_f32 v[78:79], v[102:103], v[82:83]
	v_pk_fma_f32 v[56:57], v[58:59], v[56:57], v[60:61]
	v_pk_fma_f32 v[58:59], v[104:105], v[74:75], v[72:73]
	v_pk_mul_f32 v[66:67], v[174:175], v[84:85]
	v_pk_fma_f32 v[60:61], v[78:79], v[50:51], v[58:59]
	v_pk_fma_f32 v[50:51], v[104:105], v[70:71], v[68:69]
	s_and_b64 vcc, exec, s[2:3]
	v_pk_fma_f32 v[58:59], v[66:67], v[52:53], v[50:51]
	s_cbranch_vccnz .LBB0_1236
	v_lshl_add_u64 v[50:51], v[92:93], 0, v[146:147]
	v_lshl_add_u64 v[50:51], v[50:51], 1, s[6:7]
	global_load_dwordx4 v[50:53], v[50:51], off
	v_mul_f32_e32 v0, 0xbfb8aa3b, v54
	v_exp_f32_e32 v54, v0
	v_mul_f32_e32 v0, 0xbfb8aa3b, v55
	v_exp_f32_e32 v55, v0
	s_nop 0
	v_pk_add_f32 v[54:55], v[54:55], 1.0 op_sel_hi:[1,0]
	s_nop 0
	v_rcp_f32_e32 v55, v55
	s_nop 0
	v_rcp_f32_e32 v54, v54
	s_nop 0
	v_mul_f32_e32 v0, 0xbfb8aa3b, v56
	v_exp_f32_e32 v56, v0
	v_mul_f32_e32 v0, 0xbfb8aa3b, v57
	v_exp_f32_e32 v57, v0
	s_waitcnt vmcnt(0)
	v_lshlrev_b32_e32 v66, 16, v50
	v_pk_add_f32 v[56:57], v[56:57], 1.0 op_sel_hi:[1,0]
	v_and_b32_e32 v67, 0xffff0000, v50
	v_pk_mul_f32 v[54:55], v[54:55], v[66:67]
	v_rcp_f32_e32 v57, v57
	s_nop 0
	v_rcp_f32_e32 v56, v56
	s_nop 0
	v_lshlrev_b32_e32 v50, 16, v51
	v_and_b32_e32 v51, 0xffff0000, v51
	v_mul_f32_e32 v0, 0xbfb8aa3b, v60
	v_pk_mul_f32 v[56:57], v[56:57], v[50:51]
	v_exp_f32_e32 v50, v0
	v_mul_f32_e32 v0, 0xbfb8aa3b, v61
	v_exp_f32_e32 v51, v0
	s_nop 0
	v_pk_add_f32 v[50:51], v[50:51], 1.0 op_sel_hi:[1,0]
	s_nop 0
	v_rcp_f32_e32 v51, v51
	s_nop 0
	v_rcp_f32_e32 v50, v50
	s_nop 0
	v_lshlrev_b32_e32 v60, 16, v52
	v_and_b32_e32 v61, 0xffff0000, v52
	v_mul_f32_e32 v0, 0xbfb8aa3b, v58
	v_pk_mul_f32 v[60:61], v[50:51], v[60:61]
	v_exp_f32_e32 v50, v0
	v_mul_f32_e32 v0, 0xbfb8aa3b, v59
	v_exp_f32_e32 v51, v0
	s_nop 0
	v_pk_add_f32 v[50:51], v[50:51], 1.0 op_sel_hi:[1,0]
	s_nop 0
	v_rcp_f32_e32 v51, v51
	s_nop 0
	v_rcp_f32_e32 v50, v50
	s_nop 0
	v_lshlrev_b32_e32 v52, 16, v53
	v_and_b32_e32 v53, 0xffff0000, v53
	v_pk_mul_f32 v[58:59], v[50:51], v[52:53]
.LBB0_1236:
	v_cvt_f32_i32_e32 v47, v47
	v_cvt_f32_i32_e32 v46, v46
	v_cvt_f32_i32_e32 v49, v49
	v_cvt_f32_i32_e32 v48, v48
	v_mov_b32_e32 v66, v172
	v_mov_b32_e32 v67, v172
	v_mov_b32_e32 v78, v173
	v_mov_b32_e32 v79, v173
	v_cvt_pk_bf16_f32 v50, v54, v55
	v_cvt_pk_bf16_f32 v51, v56, v57
	v_cvt_pk_bf16_f32 v52, v60, v61
	v_cvt_pk_bf16_f32 v53, v58, v59
	v_cvt_f32_i32_e32 v43, v43
	v_cvt_f32_i32_e32 v42, v42
	global_store_dwordx4 v[140:141], v[50:53], off offset:256
	v_mov_b32_e32 v173, v172
	v_cvt_f32_i32_e32 v45, v45
	v_pk_mul_f32 v[52:53], v[66:67], v[86:87]
	v_cvt_f32_i32_e32 v44, v44
	v_pk_fma_f32 v[58:59], v[78:79], v[62:63], v[80:81]
	v_pk_mul_f32 v[50:51], v[172:173], v[88:89]
	v_pk_fma_f32 v[46:47], v[52:53], v[46:47], v[58:59]
	v_pk_fma_f32 v[52:53], v[78:79], v[64:65], v[76:77]
	v_pk_mul_f32 v[56:57], v[66:67], v[82:83]
	v_pk_fma_f32 v[48:49], v[50:51], v[48:49], v[52:53]
	v_pk_fma_f32 v[50:51], v[78:79], v[74:75], v[72:73]
	v_pk_mul_f32 v[54:55], v[172:173], v[84:85]
	v_pk_fma_f32 v[52:53], v[56:57], v[42:43], v[50:51]
	v_pk_fma_f32 v[42:43], v[78:79], v[70:71], v[68:69]
	s_and_b64 vcc, exec, s[2:3]
	v_pk_fma_f32 v[50:51], v[54:55], v[44:45], v[42:43]
	s_cbranch_vccnz .LBB0_1238
	v_lshl_add_u64 v[42:43], v[92:93], 0, v[138:139]
	v_lshl_add_u64 v[42:43], v[42:43], 1, s[6:7]
	global_load_dwordx4 v[42:45], v[42:43], off
	v_mul_f32_e32 v0, 0xbfb8aa3b, v46
	v_exp_f32_e32 v46, v0
	v_mul_f32_e32 v0, 0xbfb8aa3b, v47
	v_exp_f32_e32 v47, v0
	s_nop 0
	v_pk_add_f32 v[46:47], v[46:47], 1.0 op_sel_hi:[1,0]
	s_nop 0
	v_rcp_f32_e32 v47, v47
	s_nop 0
	v_rcp_f32_e32 v46, v46
	s_nop 0
	v_mul_f32_e32 v0, 0xbfb8aa3b, v48
	v_exp_f32_e32 v48, v0
	v_mul_f32_e32 v0, 0xbfb8aa3b, v49
	v_exp_f32_e32 v49, v0
	s_waitcnt vmcnt(0)
	v_lshlrev_b32_e32 v54, 16, v42
	v_pk_add_f32 v[48:49], v[48:49], 1.0 op_sel_hi:[1,0]
	v_and_b32_e32 v55, 0xffff0000, v42
	v_pk_mul_f32 v[46:47], v[46:47], v[54:55]
	v_rcp_f32_e32 v49, v49
	s_nop 0
	v_rcp_f32_e32 v48, v48
	s_nop 0
	v_lshlrev_b32_e32 v42, 16, v43
	v_and_b32_e32 v43, 0xffff0000, v43
	v_mul_f32_e32 v0, 0xbfb8aa3b, v52
	v_pk_mul_f32 v[48:49], v[48:49], v[42:43]
	v_exp_f32_e32 v42, v0
	v_mul_f32_e32 v0, 0xbfb8aa3b, v53
	v_exp_f32_e32 v43, v0
	s_nop 0
	v_pk_add_f32 v[42:43], v[42:43], 1.0 op_sel_hi:[1,0]
	s_nop 0
	v_rcp_f32_e32 v43, v43
	s_nop 0
	v_rcp_f32_e32 v42, v42
	s_nop 0
	v_lshlrev_b32_e32 v52, 16, v44
	v_and_b32_e32 v53, 0xffff0000, v44
	v_mul_f32_e32 v0, 0xbfb8aa3b, v50
	v_pk_mul_f32 v[52:53], v[42:43], v[52:53]
	v_exp_f32_e32 v42, v0
	v_mul_f32_e32 v0, 0xbfb8aa3b, v51
	v_exp_f32_e32 v43, v0
	s_nop 0
	v_pk_add_f32 v[42:43], v[42:43], 1.0 op_sel_hi:[1,0]
	s_nop 0
	v_rcp_f32_e32 v43, v43
	s_nop 0
	v_rcp_f32_e32 v42, v42
	s_nop 0
	v_lshlrev_b32_e32 v44, 16, v45
	v_and_b32_e32 v45, 0xffff0000, v45
	v_pk_mul_f32 v[50:51], v[42:43], v[44:45]
; __device__ __forceinline__ unsigned cvt_pk_bf16(float lo, float hi) { unsigned r; asm volatile("v_cvt_pk_bf16_f32 %0, %1, %2" : "=v"(r) : "v"(lo), "v"(hi)); return r; }
; __device__ __forceinline__ float sigmoidf_(float x) { return 1.0f / (1.0f + __expf(-x)); }
;     __device__ __forceinline__ void operator()(const pg8::f32x4 (&acc)[2][2][4][2], const pg8::Unit& u, int wr, int wc, int fr_, int fq_) const {
;     ...
;                 for (int m = 0; m < 4; ++m) { const size_t ro = (size_t)(row0 + ai * 128 + m * 16) * D + col0 + bj * 128;
;                     const float rz = rsv[ai * 4 + m].x, mr = rsv[ai * 4 + m].y;
;                     pg8::f32x4 v0 = __builtin_convertvector(__builtin_bit_cast(i32x4_, acc[ai][bj][m][0]), pg8::f32x4) * (w0 * rz);
;                     pg8::f32x4 v1 = __builtin_convertvector(__builtin_bit_cast(i32x4_, acc[ai][bj][m][1]), pg8::f32x4) * (w1 * rz);
;                     v0[0] += mr * k0[0] + k0[1]; v0[1] += mr * k0[2] + k0[3]; v0[2] += mr * k1[0] + k1[1]; v0[3] += mr * k1[2] + k1[3];
;                     v1[0] += mr * k2[0] + k2[1]; v1[1] += mr * k2[2] + k2[3]; v1[2] += mr * k3[0] + k3[1]; v1[3] += mr * k3[2] + k3[3];
;                     if (!isq) { const v4u pj = *(const v4u*)(PJ + ro);
;                         v0[0] = sigmoidf_(v0[0]) * bflo(pj.x); v0[1] = sigmoidf_(v0[1]) * bfhi(pj.x); v0[2] = sigmoidf_(v0[2]) * bflo(pj.y); v0[3] = sigmoidf_(v0[3]) * bfhi(pj.y);
;                         v1[0] = sigmoidf_(v1[0]) * bflo(pj.z); v1[1] = sigmoidf_(v1[1]) * bfhi(pj.z); v1[2] = sigmoidf_(v1[2]) * bflo(pj.w); v1[3] = sigmoidf_(v1[3]) * bfhi(pj.w); }
;                     v4u w; w.x = pg8::cvt_pk_bf16(v0[0], v0[1]); w.y = pg8::cvt_pk_bf16(v0[2], v0[3]); w.z = pg8::cvt_pk_bf16(v1[0], v1[1]); w.w = pg8::cvt_pk_bf16(v1[2], v1[3]);
;                     *(v4u*)(OUTP + ro) = w; asm volatile("" ::: "memory"); }
.LBB0_1238:
	v_cvt_f32_i32_e32 v39, v39
	v_cvt_f32_i32_e32 v38, v38
	v_cvt_f32_i32_e32 v41, v41
	v_cvt_f32_i32_e32 v40, v40
	v_mov_b32_e32 v54, v170
	v_mov_b32_e32 v55, v170
	v_mov_b32_e32 v56, v171
	v_mov_b32_e32 v57, v171
	v_cvt_pk_bf16_f32 v42, v46, v47
	v_cvt_pk_bf16_f32 v43, v48, v49
	v_cvt_pk_bf16_f32 v44, v52, v53
	v_cvt_pk_bf16_f32 v45, v50, v51
	v_cvt_f32_i32_e32 v35, v35
	v_cvt_f32_i32_e32 v34, v34
	global_store_dwordx4 v[132:133], v[42:45], off offset:256
	v_mov_b32_e32 v171, v170
	v_cvt_f32_i32_e32 v37, v37
	v_pk_mul_f32 v[44:45], v[54:55], v[86:87]
	v_cvt_f32_i32_e32 v36, v36
	v_pk_fma_f32 v[50:51], v[56:57], v[62:63], v[80:81]
	v_pk_mul_f32 v[42:43], v[170:171], v[88:89]
	v_pk_fma_f32 v[38:39], v[44:45], v[38:39], v[50:51]
	v_pk_fma_f32 v[44:45], v[56:57], v[64:65], v[76:77]
	v_pk_mul_f32 v[48:49], v[54:55], v[82:83]
	v_pk_fma_f32 v[40:41], v[42:43], v[40:41], v[44:45]
	v_pk_fma_f32 v[42:43], v[56:57], v[74:75], v[72:73]
	v_pk_mul_f32 v[46:47], v[170:171], v[84:85]
	v_pk_fma_f32 v[44:45], v[48:49], v[34:35], v[42:43]
	v_pk_fma_f32 v[34:35], v[56:57], v[70:71], v[68:69]
	s_and_b64 vcc, exec, s[2:3]
	v_pk_fma_f32 v[42:43], v[46:47], v[36:37], v[34:35]
	s_cbranch_vccnz .LBB0_1240
	v_lshl_add_u64 v[34:35], v[92:93], 0, v[130:131]
	v_lshl_add_u64 v[34:35], v[34:35], 1, s[6:7]
	global_load_dwordx4 v[34:37], v[34:35], off
	v_mul_f32_e32 v0, 0xbfb8aa3b, v38
	v_exp_f32_e32 v38, v0
	v_mul_f32_e32 v0, 0xbfb8aa3b, v39
	v_exp_f32_e32 v39, v0
	s_nop 0
	v_pk_add_f32 v[38:39], v[38:39], 1.0 op_sel_hi:[1,0]
	s_nop 0
	v_rcp_f32_e32 v39, v39
	s_nop 0
	v_rcp_f32_e32 v38, v38
	s_nop 0
	v_mul_f32_e32 v0, 0xbfb8aa3b, v40
	v_exp_f32_e32 v40, v0
	v_mul_f32_e32 v0, 0xbfb8aa3b, v41
	v_exp_f32_e32 v41, v0
	s_waitcnt vmcnt(0)
	v_lshlrev_b32_e32 v46, 16, v34
	v_pk_add_f32 v[40:41], v[40:41], 1.0 op_sel_hi:[1,0]
	v_and_b32_e32 v47, 0xffff0000, v34
	v_pk_mul_f32 v[38:39], v[38:39], v[46:47]
	v_rcp_f32_e32 v41, v41
	s_nop 0
	v_rcp_f32_e32 v40, v40
	s_nop 0
	v_lshlrev_b32_e32 v34, 16, v35
	v_and_b32_e32 v35, 0xffff0000, v35
	v_mul_f32_e32 v0, 0xbfb8aa3b, v44
	v_pk_mul_f32 v[40:41], v[40:41], v[34:35]
	v_exp_f32_e32 v34, v0
	v_mul_f32_e32 v0, 0xbfb8aa3b, v45
	v_exp_f32_e32 v35, v0
	s_nop 0
	v_pk_add_f32 v[34:35], v[34:35], 1.0 op_sel_hi:[1,0]
	s_nop 0
	v_rcp_f32_e32 v35, v35
	s_nop 0
	v_rcp_f32_e32 v34, v34
	s_nop 0
	v_lshlrev_b32_e32 v44, 16, v36
	v_and_b32_e32 v45, 0xffff0000, v36
	v_mul_f32_e32 v0, 0xbfb8aa3b, v42
	v_pk_mul_f32 v[44:45], v[34:35], v[44:45]
	v_exp_f32_e32 v34, v0
	v_mul_f32_e32 v0, 0xbfb8aa3b, v43
	v_exp_f32_e32 v35, v0
	s_nop 0
	v_pk_add_f32 v[34:35], v[34:35], 1.0 op_sel_hi:[1,0]
	s_nop 0
	v_rcp_f32_e32 v35, v35
	s_nop 0
	v_rcp_f32_e32 v34, v34
	s_nop 0
	v_lshlrev_b32_e32 v36, 16, v37
	v_and_b32_e32 v37, 0xffff0000, v37
	v_pk_mul_f32 v[42:43], v[34:35], v[36:37]
.LBB0_1240:
	v_cvt_f32_i32_e32 v31, v31
	v_cvt_f32_i32_e32 v30, v30
	v_cvt_f32_i32_e32 v33, v33
	v_cvt_f32_i32_e32 v32, v32
	v_mov_b32_e32 v46, v160
	v_mov_b32_e32 v47, v160
	v_mov_b32_e32 v48, v161
	v_mov_b32_e32 v49, v161
	v_cvt_pk_bf16_f32 v34, v38, v39
	v_cvt_pk_bf16_f32 v35, v40, v41
	v_cvt_pk_bf16_f32 v36, v44, v45
	v_cvt_pk_bf16_f32 v37, v42, v43
	v_cvt_f32_i32_e32 v27, v27
	v_cvt_f32_i32_e32 v26, v26
	global_store_dwordx4 v[124:125], v[34:37], off offset:256
	v_mov_b32_e32 v161, v160
	v_cvt_f32_i32_e32 v29, v29
	v_pk_mul_f32 v[36:37], v[46:47], v[86:87]
	v_cvt_f32_i32_e32 v28, v28
	v_pk_fma_f32 v[42:43], v[48:49], v[62:63], v[80:81]
	v_pk_mul_f32 v[34:35], v[160:161], v[88:89]
	v_pk_fma_f32 v[30:31], v[36:37], v[30:31], v[42:43]
	v_pk_fma_f32 v[36:37], v[48:49], v[64:65], v[76:77]
	v_pk_mul_f32 v[40:41], v[46:47], v[82:83]
	v_pk_fma_f32 v[32:33], v[34:35], v[32:33], v[36:37]
	v_pk_fma_f32 v[34:35], v[48:49], v[74:75], v[72:73]
	v_pk_mul_f32 v[38:39], v[160:161], v[84:85]
	v_pk_fma_f32 v[36:37], v[40:41], v[26:27], v[34:35]
	v_pk_fma_f32 v[26:27], v[48:49], v[70:71], v[68:69]
	s_and_b64 vcc, exec, s[2:3]
	v_pk_fma_f32 v[34:35], v[38:39], v[28:29], v[26:27]
	s_cbranch_vccnz .LBB0_1242
	v_lshl_add_u64 v[26:27], v[92:93], 0, v[122:123]
	v_lshl_add_u64 v[26:27], v[26:27], 1, s[6:7]
	global_load_dwordx4 v[26:29], v[26:27], off
	v_mul_f32_e32 v0, 0xbfb8aa3b, v30
	v_exp_f32_e32 v30, v0
	v_mul_f32_e32 v0, 0xbfb8aa3b, v31
	v_exp_f32_e32 v31, v0
	s_nop 0
	v_pk_add_f32 v[30:31], v[30:31], 1.0 op_sel_hi:[1,0]
	s_nop 0
	v_rcp_f32_e32 v31, v31
	s_nop 0
	v_rcp_f32_e32 v30, v30
	s_nop 0
	v_mul_f32_e32 v0, 0xbfb8aa3b, v32
	v_exp_f32_e32 v32, v0
	v_mul_f32_e32 v0, 0xbfb8aa3b, v33
	v_exp_f32_e32 v33, v0
	s_waitcnt vmcnt(0)
	v_lshlrev_b32_e32 v38, 16, v26
	v_pk_add_f32 v[32:33], v[32:33], 1.0 op_sel_hi:[1,0]
	v_and_b32_e32 v39, 0xffff0000, v26
	v_pk_mul_f32 v[30:31], v[30:31], v[38:39]
	v_rcp_f32_e32 v33, v33
	s_nop 0
	v_rcp_f32_e32 v32, v32
	s_nop 0
	v_lshlrev_b32_e32 v26, 16, v27
	v_and_b32_e32 v27, 0xffff0000, v27
	v_mul_f32_e32 v0, 0xbfb8aa3b, v36
	v_pk_mul_f32 v[32:33], v[32:33], v[26:27]
	v_exp_f32_e32 v26, v0
	v_mul_f32_e32 v0, 0xbfb8aa3b, v37
	v_exp_f32_e32 v27, v0
	s_nop 0
	v_pk_add_f32 v[26:27], v[26:27], 1.0 op_sel_hi:[1,0]
	s_nop 0
	v_rcp_f32_e32 v27, v27
	s_nop 0
	v_rcp_f32_e32 v26, v26
	s_nop 0
	v_lshlrev_b32_e32 v36, 16, v28
	v_and_b32_e32 v37, 0xffff0000, v28
	v_mul_f32_e32 v0, 0xbfb8aa3b, v34
	v_pk_mul_f32 v[36:37], v[26:27], v[36:37]
	v_exp_f32_e32 v26, v0
	v_mul_f32_e32 v0, 0xbfb8aa3b, v35
	v_exp_f32_e32 v27, v0
	s_nop 0
	v_pk_add_f32 v[26:27], v[26:27], 1.0 op_sel_hi:[1,0]
	s_nop 0
	v_rcp_f32_e32 v27, v27
	s_nop 0
	v_rcp_f32_e32 v26, v26
	s_nop 0
	v_lshlrev_b32_e32 v28, 16, v29
	v_and_b32_e32 v29, 0xffff0000, v29
	v_pk_mul_f32 v[34:35], v[26:27], v[28:29]
; __device__ __forceinline__ unsigned cvt_pk_bf16(float lo, float hi) { unsigned r; asm volatile("v_cvt_pk_bf16_f32 %0, %1, %2" : "=v"(r) : "v"(lo), "v"(hi)); return r; }
; __device__ __forceinline__ float sigmoidf_(float x) { return 1.0f / (1.0f + __expf(-x)); }
;     __device__ __forceinline__ void operator()(const pg8::f32x4 (&acc)[2][2][4][2], const pg8::Unit& u, int wr, int wc, int fr_, int fq_) const {
;     ...
;                 for (int m = 0; m < 4; ++m) { const size_t ro = (size_t)(row0 + ai * 128 + m * 16) * D + col0 + bj * 128;
;                     const float rz = rsv[ai * 4 + m].x, mr = rsv[ai * 4 + m].y;
;                     pg8::f32x4 v0 = __builtin_convertvector(__builtin_bit_cast(i32x4_, acc[ai][bj][m][0]), pg8::f32x4) * (w0 * rz);
;                     pg8::f32x4 v1 = __builtin_convertvector(__builtin_bit_cast(i32x4_, acc[ai][bj][m][1]), pg8::f32x4) * (w1 * rz);
;                     v0[0] += mr * k0[0] + k0[1]; v0[1] += mr * k0[2] + k0[3]; v0[2] += mr * k1[0] + k1[1]; v0[3] += mr * k1[2] + k1[3];
;                     v1[0] += mr * k2[0] + k2[1]; v1[1] += mr * k2[2] + k2[3]; v1[2] += mr * k3[0] + k3[1]; v1[3] += mr * k3[2] + k3[3];
;                     if (!isq) { const v4u pj = *(const v4u*)(PJ + ro);
;                         v0[0] = sigmoidf_(v0[0]) * bflo(pj.x); v0[1] = sigmoidf_(v0[1]) * bfhi(pj.x); v0[2] = sigmoidf_(v0[2]) * bflo(pj.y); v0[3] = sigmoidf_(v0[3]) * bfhi(pj.y);
;                         v1[0] = sigmoidf_(v1[0]) * bflo(pj.z); v1[1] = sigmoidf_(v1[1]) * bfhi(pj.z); v1[2] = sigmoidf_(v1[2]) * bflo(pj.w); v1[3] = sigmoidf_(v1[3]) * bfhi(pj.w); }
;                     v4u w; w.x = pg8::cvt_pk_bf16(v0[0], v0[1]); w.y = pg8::cvt_pk_bf16(v0[2], v0[3]); w.z = pg8::cvt_pk_bf16(v1[0], v1[1]); w.w = pg8::cvt_pk_bf16(v1[2], v1[3]);
;                     *(v4u*)(OUTP + ro) = w; asm volatile("" ::: "memory"); }
.LBB0_1242:
	v_cvt_f32_i32_e32 v23, v23
	v_cvt_f32_i32_e32 v22, v22
	v_cvt_f32_i32_e32 v25, v25
	v_cvt_f32_i32_e32 v24, v24
	v_mov_b32_e32 v38, v158
	v_mov_b32_e32 v39, v158
	v_mov_b32_e32 v40, v159
	v_mov_b32_e32 v41, v159
	v_cvt_pk_bf16_f32 v26, v30, v31
	v_cvt_pk_bf16_f32 v27, v32, v33
	v_cvt_pk_bf16_f32 v28, v36, v37
	v_cvt_pk_bf16_f32 v29, v34, v35
	v_cvt_f32_i32_e32 v19, v19
	v_cvt_f32_i32_e32 v18, v18
	global_store_dwordx4 v[116:117], v[26:29], off offset:256
	v_mov_b32_e32 v159, v158
	v_cvt_f32_i32_e32 v21, v21
	v_pk_mul_f32 v[28:29], v[38:39], v[86:87]
	v_cvt_f32_i32_e32 v20, v20
	v_pk_fma_f32 v[34:35], v[40:41], v[62:63], v[80:81]
	v_pk_mul_f32 v[26:27], v[158:159], v[88:89]
	v_pk_fma_f32 v[22:23], v[28:29], v[22:23], v[34:35]
	v_pk_fma_f32 v[28:29], v[40:41], v[64:65], v[76:77]
	v_pk_mul_f32 v[32:33], v[38:39], v[82:83]
	v_pk_fma_f32 v[24:25], v[26:27], v[24:25], v[28:29]
	v_pk_fma_f32 v[26:27], v[40:41], v[74:75], v[72:73]
	v_pk_mul_f32 v[30:31], v[158:159], v[84:85]
	v_pk_fma_f32 v[28:29], v[32:33], v[18:19], v[26:27]
	v_pk_fma_f32 v[18:19], v[40:41], v[70:71], v[68:69]
	s_and_b64 vcc, exec, s[2:3]
	v_pk_fma_f32 v[26:27], v[30:31], v[20:21], v[18:19]
	s_cbranch_vccnz .LBB0_1244
	v_lshl_add_u64 v[18:19], v[92:93], 0, v[114:115]
	v_lshl_add_u64 v[18:19], v[18:19], 1, s[6:7]
	global_load_dwordx4 v[18:21], v[18:19], off
	v_mul_f32_e32 v0, 0xbfb8aa3b, v22
	v_exp_f32_e32 v22, v0
	v_mul_f32_e32 v0, 0xbfb8aa3b, v23
	v_exp_f32_e32 v23, v0
	s_nop 0
	v_pk_add_f32 v[22:23], v[22:23], 1.0 op_sel_hi:[1,0]
	s_nop 0
	v_rcp_f32_e32 v23, v23
	s_nop 0
	v_rcp_f32_e32 v22, v22
	s_nop 0
	v_mul_f32_e32 v0, 0xbfb8aa3b, v24
	v_exp_f32_e32 v24, v0
	v_mul_f32_e32 v0, 0xbfb8aa3b, v25
	v_exp_f32_e32 v25, v0
	s_waitcnt vmcnt(0)
	v_lshlrev_b32_e32 v30, 16, v18
	v_pk_add_f32 v[24:25], v[24:25], 1.0 op_sel_hi:[1,0]
	v_and_b32_e32 v31, 0xffff0000, v18
	v_pk_mul_f32 v[22:23], v[22:23], v[30:31]
	v_rcp_f32_e32 v25, v25
	s_nop 0
	v_rcp_f32_e32 v24, v24
	s_nop 0
	v_lshlrev_b32_e32 v18, 16, v19
	v_and_b32_e32 v19, 0xffff0000, v19
	v_mul_f32_e32 v0, 0xbfb8aa3b, v28
	v_pk_mul_f32 v[24:25], v[24:25], v[18:19]
	v_exp_f32_e32 v18, v0
	v_mul_f32_e32 v0, 0xbfb8aa3b, v29
	v_exp_f32_e32 v19, v0
	s_nop 0
	v_pk_add_f32 v[18:19], v[18:19], 1.0 op_sel_hi:[1,0]
	s_nop 0
	v_rcp_f32_e32 v19, v19
	s_nop 0
	v_rcp_f32_e32 v18, v18
	s_nop 0
	v_lshlrev_b32_e32 v28, 16, v20
	v_and_b32_e32 v29, 0xffff0000, v20
	v_mul_f32_e32 v0, 0xbfb8aa3b, v26
	v_pk_mul_f32 v[28:29], v[18:19], v[28:29]
	v_exp_f32_e32 v18, v0
	v_mul_f32_e32 v0, 0xbfb8aa3b, v27
	v_exp_f32_e32 v19, v0
	s_nop 0
	v_pk_add_f32 v[18:19], v[18:19], 1.0 op_sel_hi:[1,0]
	s_nop 0
	v_rcp_f32_e32 v19, v19
	s_nop 0
	v_rcp_f32_e32 v18, v18
	s_nop 0
	v_lshlrev_b32_e32 v20, 16, v21
	v_and_b32_e32 v21, 0xffff0000, v21
	v_pk_mul_f32 v[26:27], v[18:19], v[20:21]
; __device__ __forceinline__ unsigned cvt_pk_bf16(float lo, float hi) { unsigned r; asm volatile("v_cvt_pk_bf16_f32 %0, %1, %2" : "=v"(r) : "v"(lo), "v"(hi)); return r; }
; __device__ __forceinline__ float sigmoidf_(float x) { return 1.0f / (1.0f + __expf(-x)); }
;     __device__ __forceinline__ void operator()(const pg8::f32x4 (&acc)[2][2][4][2], const pg8::Unit& u, int wr, int wc, int fr_, int fq_) const {
;     ...
;                 for (int m = 0; m < 4; ++m) { const size_t ro = (size_t)(row0 + ai * 128 + m * 16) * D + col0 + bj * 128;
;                     const float rz = rsv[ai * 4 + m].x, mr = rsv[ai * 4 + m].y;
;                     pg8::f32x4 v0 = __builtin_convertvector(__builtin_bit_cast(i32x4_, acc[ai][bj][m][0]), pg8::f32x4) * (w0 * rz);
;                     pg8::f32x4 v1 = __builtin_convertvector(__builtin_bit_cast(i32x4_, acc[ai][bj][m][1]), pg8::f32x4) * (w1 * rz);
;                     v0[0] += mr * k0[0] + k0[1]; v0[1] += mr * k0[2] + k0[3]; v0[2] += mr * k1[0] + k1[1]; v0[3] += mr * k1[2] + k1[3];
;                     v1[0] += mr * k2[0] + k2[1]; v1[1] += mr * k2[2] + k2[3]; v1[2] += mr * k3[0] + k3[1]; v1[3] += mr * k3[2] + k3[3];
;                     if (!isq) { const v4u pj = *(const v4u*)(PJ + ro);
;                         v0[0] = sigmoidf_(v0[0]) * bflo(pj.x); v0[1] = sigmoidf_(v0[1]) * bfhi(pj.x); v0[2] = sigmoidf_(v0[2]) * bflo(pj.y); v0[3] = sigmoidf_(v0[3]) * bfhi(pj.y);
;                         v1[0] = sigmoidf_(v1[0]) * bflo(pj.z); v1[1] = sigmoidf_(v1[1]) * bfhi(pj.z); v1[2] = sigmoidf_(v1[2]) * bflo(pj.w); v1[3] = sigmoidf_(v1[3]) * bfhi(pj.w); }
;                     v4u w; w.x = pg8::cvt_pk_bf16(v0[0], v0[1]); w.y = pg8::cvt_pk_bf16(v0[2], v0[3]); w.z = pg8::cvt_pk_bf16(v1[0], v1[1]); w.w = pg8::cvt_pk_bf16(v1[2], v1[3]);
;                     *(v4u*)(OUTP + ro) = w; asm volatile("" ::: "memory"); }
.LBB0_1244:
	v_cvt_f32_i32_e32 v15, v15
	v_cvt_f32_i32_e32 v14, v14
	v_cvt_f32_i32_e32 v17, v17
	v_cvt_f32_i32_e32 v16, v16
	v_mov_b32_e32 v30, v156
	v_mov_b32_e32 v31, v156
	v_mov_b32_e32 v32, v157
	v_mov_b32_e32 v33, v157
	v_cvt_pk_bf16_f32 v18, v22, v23
	v_cvt_pk_bf16_f32 v19, v24, v25
	v_cvt_pk_bf16_f32 v20, v28, v29
	v_cvt_pk_bf16_f32 v21, v26, v27
	v_cvt_f32_i32_e32 v11, v11
	v_cvt_f32_i32_e32 v10, v10
	global_store_dwordx4 v[108:109], v[18:21], off offset:256
	v_mov_b32_e32 v157, v156
	v_cvt_f32_i32_e32 v13, v13
	v_pk_mul_f32 v[20:21], v[30:31], v[86:87]
	v_cvt_f32_i32_e32 v12, v12
	v_pk_fma_f32 v[26:27], v[32:33], v[62:63], v[80:81]
	v_pk_mul_f32 v[18:19], v[156:157], v[88:89]
	v_pk_fma_f32 v[14:15], v[20:21], v[14:15], v[26:27]
	v_pk_fma_f32 v[20:21], v[32:33], v[64:65], v[76:77]
	v_pk_mul_f32 v[24:25], v[30:31], v[82:83]
	v_pk_fma_f32 v[16:17], v[18:19], v[16:17], v[20:21]
	v_pk_fma_f32 v[18:19], v[32:33], v[74:75], v[72:73]
	v_pk_mul_f32 v[22:23], v[156:157], v[84:85]
	v_pk_fma_f32 v[20:21], v[24:25], v[10:11], v[18:19]
	v_pk_fma_f32 v[10:11], v[32:33], v[70:71], v[68:69]
	s_and_b64 vcc, exec, s[2:3]
	v_pk_fma_f32 v[18:19], v[22:23], v[12:13], v[10:11]
	s_cbranch_vccnz .LBB0_1246
	v_lshl_add_u64 v[10:11], v[92:93], 0, v[106:107]
	v_lshl_add_u64 v[10:11], v[10:11], 1, s[6:7]
	global_load_dwordx4 v[10:13], v[10:11], off
	v_mul_f32_e32 v0, 0xbfb8aa3b, v14
	v_exp_f32_e32 v14, v0
	v_mul_f32_e32 v0, 0xbfb8aa3b, v15
	v_exp_f32_e32 v15, v0
	s_nop 0
	v_pk_add_f32 v[14:15], v[14:15], 1.0 op_sel_hi:[1,0]
	s_nop 0
	v_rcp_f32_e32 v15, v15
	s_nop 0
	v_rcp_f32_e32 v14, v14
	s_nop 0
	v_mul_f32_e32 v0, 0xbfb8aa3b, v16
	v_exp_f32_e32 v16, v0
	v_mul_f32_e32 v0, 0xbfb8aa3b, v17
	v_exp_f32_e32 v17, v0
	s_waitcnt vmcnt(0)
	v_lshlrev_b32_e32 v22, 16, v10
	v_pk_add_f32 v[16:17], v[16:17], 1.0 op_sel_hi:[1,0]
	v_and_b32_e32 v23, 0xffff0000, v10
	v_pk_mul_f32 v[14:15], v[14:15], v[22:23]
	v_rcp_f32_e32 v17, v17
	s_nop 0
	v_rcp_f32_e32 v16, v16
	s_nop 0
	v_lshlrev_b32_e32 v10, 16, v11
	v_and_b32_e32 v11, 0xffff0000, v11
	v_mul_f32_e32 v0, 0xbfb8aa3b, v20
	v_pk_mul_f32 v[16:17], v[16:17], v[10:11]
	v_exp_f32_e32 v10, v0
	v_mul_f32_e32 v0, 0xbfb8aa3b, v21
	v_exp_f32_e32 v11, v0
	s_nop 0
	v_pk_add_f32 v[10:11], v[10:11], 1.0 op_sel_hi:[1,0]
	s_nop 0
	v_rcp_f32_e32 v11, v11
	s_nop 0
	v_rcp_f32_e32 v10, v10
	s_nop 0
	v_lshlrev_b32_e32 v20, 16, v12
	v_and_b32_e32 v21, 0xffff0000, v12
	v_mul_f32_e32 v0, 0xbfb8aa3b, v18
	v_pk_mul_f32 v[20:21], v[10:11], v[20:21]
	v_exp_f32_e32 v10, v0
	v_mul_f32_e32 v0, 0xbfb8aa3b, v19
	v_exp_f32_e32 v11, v0
	s_nop 0
	v_pk_add_f32 v[10:11], v[10:11], 1.0 op_sel_hi:[1,0]
	s_nop 0
	v_rcp_f32_e32 v11, v11
	s_nop 0
	v_rcp_f32_e32 v10, v10
	s_nop 0
	v_lshlrev_b32_e32 v12, 16, v13
	v_and_b32_e32 v13, 0xffff0000, v13
	v_pk_mul_f32 v[18:19], v[10:11], v[12:13]
.LBB0_1246:
	v_cvt_f32_i32_e32 v7, v7
	v_cvt_f32_i32_e32 v6, v6
	v_cvt_f32_i32_e32 v9, v9
	v_cvt_f32_i32_e32 v8, v8
	v_mov_b32_e32 v22, v154
	v_mov_b32_e32 v23, v154
	v_mov_b32_e32 v24, v155
	v_mov_b32_e32 v25, v155
	v_cvt_pk_bf16_f32 v10, v14, v15
	v_cvt_pk_bf16_f32 v11, v16, v17
	v_cvt_pk_bf16_f32 v12, v20, v21
	v_cvt_pk_bf16_f32 v13, v18, v19
	v_cvt_f32_i32_e32 v3, v3
	v_cvt_f32_i32_e32 v2, v2
	global_store_dwordx4 v[100:101], v[10:13], off offset:256
	v_mov_b32_e32 v155, v154
	v_cvt_f32_i32_e32 v5, v5
	v_pk_mul_f32 v[12:13], v[22:23], v[86:87]
	v_cvt_f32_i32_e32 v4, v4
	v_pk_fma_f32 v[18:19], v[24:25], v[62:63], v[80:81]
	v_pk_mul_f32 v[10:11], v[154:155], v[88:89]
	v_pk_fma_f32 v[6:7], v[12:13], v[6:7], v[18:19]
	v_pk_fma_f32 v[12:13], v[24:25], v[64:65], v[76:77]
	v_pk_mul_f32 v[16:17], v[22:23], v[82:83]
	v_pk_fma_f32 v[8:9], v[10:11], v[8:9], v[12:13]
	v_pk_fma_f32 v[10:11], v[24:25], v[74:75], v[72:73]
	v_pk_mul_f32 v[14:15], v[154:155], v[84:85]
	v_pk_fma_f32 v[12:13], v[16:17], v[2:3], v[10:11]
	v_pk_fma_f32 v[2:3], v[24:25], v[70:71], v[68:69]
	s_and_b64 vcc, exec, s[2:3]
	v_pk_fma_f32 v[10:11], v[14:15], v[4:5], v[2:3]
	s_cbranch_vccnz .LBB0_1248
	v_lshl_add_u64 v[2:3], v[92:93], 0, v[98:99]
	v_lshl_add_u64 v[2:3], v[2:3], 1, s[6:7]
	global_load_dwordx4 v[2:5], v[2:3], off
	v_mul_f32_e32 v0, 0xbfb8aa3b, v6
	v_exp_f32_e32 v6, v0
	v_mul_f32_e32 v0, 0xbfb8aa3b, v7
	v_exp_f32_e32 v7, v0
	s_nop 0
	v_pk_add_f32 v[6:7], v[6:7], 1.0 op_sel_hi:[1,0]
	s_nop 0
	v_rcp_f32_e32 v7, v7
	s_nop 0
	v_rcp_f32_e32 v6, v6
	s_nop 0
	v_mul_f32_e32 v0, 0xbfb8aa3b, v8
	v_exp_f32_e32 v8, v0
	v_mul_f32_e32 v0, 0xbfb8aa3b, v9
	v_exp_f32_e32 v9, v0
	s_waitcnt vmcnt(0)
	v_lshlrev_b32_e32 v14, 16, v2
	v_pk_add_f32 v[8:9], v[8:9], 1.0 op_sel_hi:[1,0]
	v_and_b32_e32 v15, 0xffff0000, v2
	v_pk_mul_f32 v[6:7], v[6:7], v[14:15]
	v_rcp_f32_e32 v9, v9
	s_nop 0
	v_rcp_f32_e32 v8, v8
	s_nop 0
	v_lshlrev_b32_e32 v2, 16, v3
	v_and_b32_e32 v3, 0xffff0000, v3
	v_mul_f32_e32 v0, 0xbfb8aa3b, v12
	v_pk_mul_f32 v[8:9], v[8:9], v[2:3]
	v_exp_f32_e32 v2, v0
	v_mul_f32_e32 v0, 0xbfb8aa3b, v13
	v_exp_f32_e32 v3, v0
	s_nop 0
	v_pk_add_f32 v[2:3], v[2:3], 1.0 op_sel_hi:[1,0]
	s_nop 0
	v_rcp_f32_e32 v3, v3
	s_nop 0
	v_rcp_f32_e32 v2, v2
	s_nop 0
	v_lshlrev_b32_e32 v12, 16, v4
	v_and_b32_e32 v13, 0xffff0000, v4
	v_mul_f32_e32 v0, 0xbfb8aa3b, v10
	v_pk_mul_f32 v[12:13], v[2:3], v[12:13]
	v_exp_f32_e32 v2, v0
	v_mul_f32_e32 v0, 0xbfb8aa3b, v11
	v_exp_f32_e32 v3, v0
	s_nop 0
	v_pk_add_f32 v[2:3], v[2:3], 1.0 op_sel_hi:[1,0]
	s_nop 0
	v_rcp_f32_e32 v3, v3
	s_nop 0
	v_rcp_f32_e32 v2, v2
	s_nop 0
	v_lshlrev_b32_e32 v4, 16, v5
	v_and_b32_e32 v5, 0xffff0000, v5
	v_pk_mul_f32 v[10:11], v[2:3], v[4:5]
